# v8 + nt policy on the P12 token stream loads (x2 rows, expert output rows)
# baseline (speedup 1.0000x reference)
.LBB0_1428:
	s_or_b64 exec, exec, s[0:1]
	ds_bpermute_b32 v26, v95, v130
	ds_bpermute_b32 v30, v97, v130
	v_lshl_add_u64 v[20:21], s[82:83], 0, v[16:17]
	v_add_co_u32_e32 v22, vcc, 0x68200000, v20
	s_waitcnt lgkmcnt(1)
	v_ashrrev_i32_e32 v27, 31, v26
	v_lshlrev_b64 v[26:27], 11, v[26:27]
	v_addc_co_u32_e32 v23, vcc, 0, v21, vcc
	v_lshl_add_u64 v[26:27], v[4:5], 0, v[26:27]
	s_waitcnt lgkmcnt(0)
	v_ashrrev_i32_e32 v31, 31, v30
	global_load_dwordx2 v[24:25], v[22:23], off nt
	global_load_dwordx2 v[40:41], v[22:23], off offset:512 nt
	global_load_dwordx2 v[54:55], v[22:23], off offset:1024 nt
	global_load_dwordx2 v[64:65], v[22:23], off offset:1536 nt
	global_load_dwordx2 v[68:69], v[22:23], off offset:2048 nt
	global_load_dwordx2 v[48:49], v[22:23], off offset:2560 nt
	global_load_dwordx2 v[28:29], v[22:23], off offset:3072 nt
	s_nop 0
	global_load_dwordx2 v[22:23], v[22:23], off offset:3584 nt
	s_nop 0
	global_load_dword v62, v[26:27], off nt
	global_load_dword v139, v[26:27], off offset:256 nt
	global_load_dword v141, v[26:27], off offset:512 nt
	global_load_dword v142, v[26:27], off offset:768 nt
	global_load_dword v144, v[26:27], off offset:1024 nt
	global_load_dword v78, v[26:27], off offset:1280 nt
	global_load_dword v80, v[26:27], off offset:1536 nt
	global_load_dword v131, v[26:27], off offset:1792 nt
	v_lshlrev_b64 v[26:27], 11, v[30:31]
	ds_bpermute_b32 v30, v98, v130
	v_lshl_add_u64 v[26:27], v[4:5], 0, v[26:27]
	global_load_dword v63, v[26:27], off nt
	global_load_dword v149, v[26:27], off offset:256 nt
	global_load_dword v152, v[26:27], off offset:512 nt
	global_load_dword v168, v[26:27], off offset:768 nt
	global_load_dword v170, v[26:27], off offset:1024 nt
	global_load_dword v79, v[26:27], off offset:1280 nt
	global_load_dword v81, v[26:27], off offset:1536 nt
	global_load_dword v133, v[26:27], off offset:1792 nt
	ds_bpermute_b32 v34, v101, v130
	ds_bpermute_b32 v44, v102, v130
	s_waitcnt lgkmcnt(2)
	v_ashrrev_i32_e32 v31, 31, v30
	v_lshlrev_b64 v[26:27], 11, v[30:31]
	ds_bpermute_b32 v30, v99, v130
	v_lshl_add_u64 v[26:27], v[4:5], 0, v[26:27]
	global_load_dword v70, v[26:27], off nt
	global_load_dword v158, v[26:27], off offset:256 nt
	global_load_dword v176, v[26:27], off offset:512 nt
	global_load_dword v178, v[26:27], off offset:768 nt
	global_load_dword v184, v[26:27], off offset:1024 nt
	global_load_dword v186, v[26:27], off offset:1280 nt
	global_load_dword v84, v[26:27], off offset:1536 nt
	global_load_dword v134, v[26:27], off offset:1792 nt
	s_waitcnt lgkmcnt(2)
	v_ashrrev_i32_e32 v35, 31, v34
	v_lshlrev_b64 v[34:35], 11, v[34:35]
	s_waitcnt lgkmcnt(0)
	v_ashrrev_i32_e32 v31, 31, v30
	v_lshlrev_b64 v[26:27], 11, v[30:31]
	ds_bpermute_b32 v30, v100, v130
	v_lshl_add_u64 v[26:27], v[4:5], 0, v[26:27]
	global_load_dword v74, v[26:27], off nt
	global_load_dword v159, v[26:27], off offset:256 nt
	global_load_dword v182, v[26:27], off offset:512 nt
	global_load_dword v189, v[26:27], off offset:768 nt
	global_load_dword v196, v[26:27], off offset:1024 nt
	global_load_dword v199, v[26:27], off offset:1280 nt
	global_load_dword v85, v[26:27], off offset:1536 nt
	global_load_dword v136, v[26:27], off offset:1792 nt
	v_add_co_u32_e32 v26, vcc, s3, v20
	s_waitcnt lgkmcnt(0)
	v_ashrrev_i32_e32 v31, 31, v30
	v_lshlrev_b64 v[30:31], 11, v[30:31]
	v_addc_co_u32_e32 v27, vcc, 0, v21, vcc
	v_lshl_add_u64 v[32:33], v[4:5], 0, v[30:31]
	v_ashrrev_i32_e32 v45, 31, v44
	global_load_dwordx2 v[52:53], v[26:27], off offset:512 nt
	global_load_dwordx2 v[46:47], v[26:27], off offset:1024 nt
	global_load_dwordx2 v[42:43], v[26:27], off offset:1536 nt
	global_load_dwordx2 v[38:39], v[26:27], off offset:2048 nt
	global_load_dwordx2 v[36:37], v[26:27], off offset:2560 nt
	global_load_dwordx2 v[30:31], v[26:27], off offset:3072 nt
	s_nop 0
	global_load_dwordx2 v[26:27], v[26:27], off offset:3584 nt
	s_nop 0
	global_load_dword v181, v[32:33], off nt
	v_lshl_add_u64 v[34:35], v[4:5], 0, v[34:35]
	global_load_dword v173, v[32:33], off offset:256 nt
	global_load_dword v165, v[32:33], off offset:512 nt
	global_load_dword v88, v[32:33], off offset:768 nt
	global_load_dword v155, v[32:33], off offset:1024 nt
	global_load_dword v147, v[32:33], off offset:1280 nt
	global_load_dword v140, v[32:33], off offset:1536 nt
	global_load_dword v132, v[32:33], off offset:1792 nt
	global_load_dword v185, v[34:35], off nt
	v_lshlrev_b64 v[32:33], 11, v[44:45]
	ds_bpermute_b32 v44, v103, v130
	v_add_co_u32_e32 v56, vcc, s26, v20
	v_lshl_add_u64 v[32:33], v[4:5], 0, v[32:33]
	global_load_dword v177, v[34:35], off offset:256 nt
	global_load_dword v169, v[34:35], off offset:512 nt
	global_load_dword v89, v[34:35], off offset:768 nt
	global_load_dword v156, v[34:35], off offset:1024 nt
	global_load_dword v148, v[34:35], off offset:1280 nt
	global_load_dword v143, v[34:35], off offset:1536 nt
	global_load_dword v135, v[34:35], off offset:1792 nt
	global_load_dword v187, v[32:33], off nt
	s_waitcnt lgkmcnt(0)
	v_ashrrev_i32_e32 v45, 31, v44
	v_lshlrev_b64 v[34:35], 11, v[44:45]
	v_addc_co_u32_e32 v57, vcc, 0, v21, vcc
	v_lshl_add_u64 v[34:35], v[4:5], 0, v[34:35]
	global_load_dword v179, v[32:33], off offset:256 nt
	global_load_dword v171, v[32:33], off offset:512 nt
	global_load_dword v163, v[32:33], off offset:768 nt
	global_load_dword v157, v[32:33], off offset:1024 nt
	global_load_dword v153, v[32:33], off offset:1280 nt
	global_load_dword v145, v[32:33], off offset:1536 nt
	global_load_dword v137, v[32:33], off offset:1792 nt
	global_load_dword v188, v[34:35], off nt
	global_load_dwordx2 v[60:61], v[56:57], off offset:-4096 nt
	global_load_dword v180, v[34:35], off offset:256 nt
	global_load_dword v172, v[34:35], off offset:512 nt
	global_load_dword v164, v[34:35], off offset:768 nt
	global_load_dword v162, v[34:35], off offset:1024 nt
	global_load_dword v154, v[34:35], off offset:1280 nt
	global_load_dword v146, v[34:35], off offset:1536 nt
	global_load_dword v138, v[34:35], off offset:1792 nt
	ds_bpermute_b32 v59, v95, v19
	ds_bpermute_b32 v58, v97, v19
	ds_bpermute_b32 v51, v98, v19
	ds_bpermute_b32 v50, v99, v19

	s_waitcnt vmcnt(63)
	v_cvt_pk_f32_fp8_e32 v[32:33], v62
	v_cvt_pk_f32_fp8_sdwa v[34:35], v62 src0_sel:WORD_1
	v_lshlrev_b32_e32 v77, 16, v25
	v_lshlrev_b32_e32 v76, 16, v24
	v_cvt_pk_f32_fp8_e32 v[44:45], v63
	v_cvt_pk_f32_fp8_sdwa v[62:63], v63 src0_sel:WORD_1
	v_mov_b32_e32 v86, v32
	v_and_b32_e32 v83, 0xffff0000, v25
	v_and_b32_e32 v82, 0xffff0000, v24
	v_mov_b32_e32 v87, v62
	v_mov_b32_e32 v62, v33

	s_waitcnt vmcnt(55)
	v_cvt_pk_f32_fp8_e32 v[66:67], v70
	v_cvt_pk_f32_fp8_sdwa v[70:71], v70 src0_sel:WORD_1
	v_mov_b32_e32 v24, v44
	v_mov_b32_e32 v25, v34
	s_waitcnt lgkmcnt(2)
	v_pk_mul_f32 v[86:87], v[86:87], v[58:59] op_sel:[0,1] op_sel_hi:[1,0]
	v_mov_b32_e32 v34, v45
	v_pk_mul_f32 v[32:33], v[62:63], v[58:59] op_sel:[0,1] op_sel_hi:[1,0]

	s_waitcnt vmcnt(47)
	v_cvt_pk_f32_fp8_e32 v[72:73], v74
	v_cvt_pk_f32_fp8_sdwa v[74:75], v74 src0_sel:WORD_1
	v_pk_fma_f32 v[24:25], v[24:25], v[58:59], v[86:87]
	v_mov_b32_e32 v87, v70
	v_mov_b32_e32 v150, v66
	v_mov_b32_e32 v151, v74
	v_mov_b32_e32 v74, v67
	v_pk_fma_f32 v[32:33], v[34:35], v[58:59], v[32:33]
	v_mov_b32_e32 v70, v73
	s_waitcnt lgkmcnt(0)
	v_pk_mul_f32 v[34:35], v[74:75], v[50:51] op_sel:[0,1] op_sel_hi:[1,0]
	v_mov_b32_e32 v86, v72
	v_pk_mul_f32 v[150:151], v[150:151], v[50:51] op_sel:[0,1] op_sel_hi:[1,0]
	v_pk_fma_f32 v[34:35], v[70:71], v[50:51], v[34:35]
	v_pk_fma_f32 v[86:87], v[86:87], v[50:51], v[150:151]
	v_pk_add_f32 v[32:33], v[32:33], v[34:35]
	v_pk_add_f32 v[24:25], v[24:25], v[86:87]
	v_pk_add_f32 v[34:35], v[32:33], v[82:83]
	v_pk_add_f32 v[24:25], v[24:25], v[76:77]
	v_and_b32_sdwa v44, v35, v129 dst_sel:DWORD dst_unused:UNUSED_PAD src0_sel:WORD_1 src1_sel:DWORD
	v_and_b32_sdwa v32, v25, v129 dst_sel:DWORD dst_unused:UNUSED_PAD src0_sel:WORD_1 src1_sel:DWORD
	v_and_b32_sdwa v45, v34, v129 dst_sel:DWORD dst_unused:UNUSED_PAD src0_sel:WORD_1 src1_sel:DWORD
	v_add3_u32 v44, v35, v44, s4
	v_add_co_u32_e32 v66, vcc, s5, v20
	v_and_b32_sdwa v33, v24, v129 dst_sel:DWORD dst_unused:UNUSED_PAD src0_sel:WORD_1 src1_sel:DWORD
	v_add3_u32 v32, v25, v32, s4
	v_add3_u32 v45, v34, v45, s4
	v_and_b32_e32 v44, 0xffff0000, v44
	v_addc_co_u32_e32 v67, vcc, 0, v21, vcc
	v_add3_u32 v33, v24, v33, s4
	v_and_b32_e32 v62, 0xffff0000, v45
	v_or_b32_sdwa v45, v44, v32 dst_sel:DWORD dst_unused:UNUSED_PAD src0_sel:DWORD src1_sel:WORD_1
	v_add_co_u32_e32 v32, vcc, s27, v20
	v_or_b32_sdwa v44, v62, v33 dst_sel:DWORD dst_unused:UNUSED_PAD src0_sel:DWORD src1_sel:WORD_1
	s_nop 0
	v_addc_co_u32_e32 v33, vcc, 0, v21, vcc
	global_store_dwordx2 v[32:33], v[44:45], off offset:-4096
	v_pk_mul_f32 v[44:45], v[34:35], v[34:35]
	s_nop 0
	v_pk_fma_f32 v[70:71], v[24:25], v[24:25], v[44:45]
	v_cvt_pk_f32_fp8_e32 v[44:45], v139
	v_cvt_pk_f32_fp8_sdwa v[74:75], v149 src0_sel:WORD_1
	v_cvt_pk_f32_fp8_sdwa v[62:63], v139 src0_sel:WORD_1
	v_cvt_pk_f32_fp8_e32 v[72:73], v149
	v_cvt_pk_f32_fp8_e32 v[76:77], v158

	s_waitcnt vmcnt(47)
	v_cvt_pk_f32_fp8_sdwa v[150:151], v159 src0_sel:WORD_1
	v_cvt_pk_f32_fp8_sdwa v[82:83], v158 src0_sel:WORD_1
	v_cvt_pk_f32_fp8_e32 v[86:87], v159
	v_mov_b32_e32 v166, v44
	v_mov_b32_e32 v167, v74
	v_lshlrev_b32_e32 v159, 16, v41
	v_lshlrev_b32_e32 v158, 16, v40
	v_and_b32_e32 v161, 0xffff0000, v41
	v_and_b32_e32 v160, 0xffff0000, v40
	v_mov_b32_e32 v40, v72
	v_mov_b32_e32 v41, v62
	v_pk_mul_f32 v[166:167], v[166:167], v[58:59] op_sel:[0,1] op_sel_hi:[1,0]
	v_mov_b32_e32 v174, v76
	v_mov_b32_e32 v175, v150
	v_mov_b32_e32 v74, v45
	v_pk_fma_f32 v[40:41], v[40:41], v[58:59], v[166:167]
	v_mov_b32_e32 v166, v86
	v_mov_b32_e32 v167, v82
	v_pk_mul_f32 v[174:175], v[174:175], v[50:51] op_sel:[0,1] op_sel_hi:[1,0]
	v_mov_b32_e32 v62, v73
	v_pk_mul_f32 v[44:45], v[74:75], v[58:59] op_sel:[0,1] op_sel_hi:[1,0]
	v_mov_b32_e32 v150, v77
	v_pk_fma_f32 v[166:167], v[166:167], v[50:51], v[174:175]
	v_pk_fma_f32 v[44:45], v[62:63], v[58:59], v[44:45]
	v_mov_b32_e32 v82, v87
	v_pk_mul_f32 v[62:63], v[150:151], v[50:51] op_sel:[0,1] op_sel_hi:[1,0]
	v_pk_add_f32 v[40:41], v[40:41], v[166:167]
	v_pk_fma_f32 v[62:63], v[82:83], v[50:51], v[62:63]
	v_pk_add_f32 v[40:41], v[40:41], v[158:159]
	v_pk_add_f32 v[44:45], v[44:45], v[62:63]
	v_and_b32_sdwa v63, v40, v129 dst_sel:DWORD dst_unused:UNUSED_PAD src0_sel:WORD_1 src1_sel:DWORD
	v_pk_add_f32 v[44:45], v[44:45], v[160:161]
	v_add3_u32 v72, v40, v63, s4
	v_and_b32_sdwa v63, v45, v129 dst_sel:DWORD dst_unused:UNUSED_PAD src0_sel:WORD_1 src1_sel:DWORD
	v_and_b32_sdwa v73, v44, v129 dst_sel:DWORD dst_unused:UNUSED_PAD src0_sel:WORD_1 src1_sel:DWORD
	v_and_b32_sdwa v62, v41, v129 dst_sel:DWORD dst_unused:UNUSED_PAD src0_sel:WORD_1 src1_sel:DWORD
	v_add3_u32 v63, v45, v63, s4
	v_add3_u32 v73, v44, v73, s4
	v_add3_u32 v62, v41, v62, s4
	v_and_b32_e32 v63, 0xffff0000, v63
	v_and_b32_e32 v73, 0xffff0000, v73
	v_or_b32_sdwa v63, v63, v62 dst_sel:DWORD dst_unused:UNUSED_PAD src0_sel:DWORD src1_sel:WORD_1
	v_or_b32_sdwa v62, v73, v72 dst_sel:DWORD dst_unused:UNUSED_PAD src0_sel:DWORD src1_sel:WORD_1
	global_store_dwordx2 v[66:67], v[62:63], off offset:512
	v_pk_mul_f32 v[62:63], v[44:45], v[44:45]
	s_nop 0
	v_pk_fma_f32 v[76:77], v[40:41], v[40:41], v[62:63]
	v_cvt_pk_f32_fp8_e32 v[62:63], v141
	v_cvt_pk_f32_fp8_sdwa v[82:83], v152 src0_sel:WORD_1
	v_cvt_pk_f32_fp8_sdwa v[72:73], v141 src0_sel:WORD_1
	v_cvt_pk_f32_fp8_e32 v[74:75], v152
	v_cvt_pk_f32_fp8_e32 v[86:87], v176

	s_waitcnt vmcnt(47)
	v_cvt_pk_f32_fp8_sdwa v[160:161], v182 src0_sel:WORD_1
	v_cvt_pk_f32_fp8_sdwa v[150:151], v176 src0_sel:WORD_1
	v_cvt_pk_f32_fp8_e32 v[158:159], v182
	v_mov_b32_e32 v182, v62
	v_mov_b32_e32 v183, v82
	v_lshlrev_b32_e32 v167, 16, v55
	v_lshlrev_b32_e32 v166, 16, v54
	v_and_b32_e32 v175, 0xffff0000, v55
	v_and_b32_e32 v174, 0xffff0000, v54
	v_mov_b32_e32 v54, v74
	v_mov_b32_e32 v55, v72
	v_pk_mul_f32 v[182:183], v[182:183], v[58:59] op_sel:[0,1] op_sel_hi:[1,0]
	v_mov_b32_e32 v190, v86
	v_mov_b32_e32 v191, v160
	v_mov_b32_e32 v82, v63
	v_pk_fma_f32 v[54:55], v[54:55], v[58:59], v[182:183]
	v_mov_b32_e32 v182, v158
	v_mov_b32_e32 v183, v150
	v_pk_mul_f32 v[190:191], v[190:191], v[50:51] op_sel:[0,1] op_sel_hi:[1,0]
	v_mov_b32_e32 v72, v75
	v_pk_mul_f32 v[62:63], v[82:83], v[58:59] op_sel:[0,1] op_sel_hi:[1,0]
	v_mov_b32_e32 v160, v87
	v_pk_fma_f32 v[182:183], v[182:183], v[50:51], v[190:191]
	v_pk_fma_f32 v[62:63], v[72:73], v[58:59], v[62:63]
	v_mov_b32_e32 v150, v159
	v_pk_mul_f32 v[72:73], v[160:161], v[50:51] op_sel:[0,1] op_sel_hi:[1,0]
	v_pk_add_f32 v[54:55], v[54:55], v[182:183]
	v_pk_fma_f32 v[72:73], v[150:151], v[50:51], v[72:73]
	v_pk_add_f32 v[54:55], v[54:55], v[166:167]
	v_pk_add_f32 v[62:63], v[62:63], v[72:73]
	v_and_b32_sdwa v73, v54, v129 dst_sel:DWORD dst_unused:UNUSED_PAD src0_sel:WORD_1 src1_sel:DWORD
	v_pk_add_f32 v[62:63], v[62:63], v[174:175]
	v_add3_u32 v74, v54, v73, s4
	v_and_b32_sdwa v73, v63, v129 dst_sel:DWORD dst_unused:UNUSED_PAD src0_sel:WORD_1 src1_sel:DWORD
	v_and_b32_sdwa v75, v62, v129 dst_sel:DWORD dst_unused:UNUSED_PAD src0_sel:WORD_1 src1_sel:DWORD
	v_and_b32_sdwa v72, v55, v129 dst_sel:DWORD dst_unused:UNUSED_PAD src0_sel:WORD_1 src1_sel:DWORD
	v_add3_u32 v73, v63, v73, s4
	v_add3_u32 v75, v62, v75, s4
	v_add3_u32 v72, v55, v72, s4
	v_and_b32_e32 v73, 0xffff0000, v73
	v_and_b32_e32 v75, 0xffff0000, v75
	v_or_b32_sdwa v73, v73, v72 dst_sel:DWORD dst_unused:UNUSED_PAD src0_sel:DWORD src1_sel:WORD_1
	v_or_b32_sdwa v72, v75, v74 dst_sel:DWORD dst_unused:UNUSED_PAD src0_sel:DWORD src1_sel:WORD_1
	global_store_dwordx2 v[66:67], v[72:73], off offset:1024
	v_pk_mul_f32 v[72:73], v[62:63], v[62:63]
	s_nop 0
	v_pk_fma_f32 v[82:83], v[54:55], v[54:55], v[72:73]
	v_cvt_pk_f32_fp8_e32 v[72:73], v142
	v_cvt_pk_f32_fp8_sdwa v[150:151], v168 src0_sel:WORD_1
	v_cvt_pk_f32_fp8_sdwa v[74:75], v142 src0_sel:WORD_1
	v_cvt_pk_f32_fp8_e32 v[86:87], v168
	v_cvt_pk_f32_fp8_e32 v[158:159], v178

	s_waitcnt vmcnt(47)
	v_cvt_pk_f32_fp8_sdwa v[174:175], v189 src0_sel:WORD_1
	v_cvt_pk_f32_fp8_sdwa v[160:161], v178 src0_sel:WORD_1
	v_cvt_pk_f32_fp8_e32 v[166:167], v189
	v_mov_b32_e32 v192, v72
	v_mov_b32_e32 v193, v150
	v_lshlrev_b32_e32 v183, 16, v65
	v_lshlrev_b32_e32 v182, 16, v64
	v_and_b32_e32 v191, 0xffff0000, v65
	v_and_b32_e32 v190, 0xffff0000, v64
	v_mov_b32_e32 v64, v86
	v_mov_b32_e32 v65, v74
	v_pk_mul_f32 v[192:193], v[192:193], v[58:59] op_sel:[0,1] op_sel_hi:[1,0]
	v_mov_b32_e32 v194, v158
	v_mov_b32_e32 v195, v174
	v_mov_b32_e32 v150, v73
	v_pk_fma_f32 v[64:65], v[64:65], v[58:59], v[192:193]
	v_mov_b32_e32 v192, v166
	v_mov_b32_e32 v193, v160
	v_pk_mul_f32 v[194:195], v[194:195], v[50:51] op_sel:[0,1] op_sel_hi:[1,0]
	v_mov_b32_e32 v74, v87
	v_pk_mul_f32 v[72:73], v[150:151], v[58:59] op_sel:[0,1] op_sel_hi:[1,0]
	v_mov_b32_e32 v174, v159
	v_pk_fma_f32 v[192:193], v[192:193], v[50:51], v[194:195]
	v_pk_fma_f32 v[72:73], v[74:75], v[58:59], v[72:73]
	v_mov_b32_e32 v160, v167
	v_pk_mul_f32 v[74:75], v[174:175], v[50:51] op_sel:[0,1] op_sel_hi:[1,0]
	v_pk_add_f32 v[64:65], v[64:65], v[192:193]
	v_pk_fma_f32 v[74:75], v[160:161], v[50:51], v[74:75]
	v_pk_add_f32 v[64:65], v[64:65], v[182:183]
	v_pk_add_f32 v[72:73], v[72:73], v[74:75]
	v_and_b32_sdwa v75, v64, v129 dst_sel:DWORD dst_unused:UNUSED_PAD src0_sel:WORD_1 src1_sel:DWORD
	v_pk_add_f32 v[72:73], v[72:73], v[190:191]
	v_add3_u32 v86, v64, v75, s4
	v_and_b32_sdwa v75, v73, v129 dst_sel:DWORD dst_unused:UNUSED_PAD src0_sel:WORD_1 src1_sel:DWORD
	v_and_b32_sdwa v87, v72, v129 dst_sel:DWORD dst_unused:UNUSED_PAD src0_sel:WORD_1 src1_sel:DWORD
	v_and_b32_sdwa v74, v65, v129 dst_sel:DWORD dst_unused:UNUSED_PAD src0_sel:WORD_1 src1_sel:DWORD
	v_add3_u32 v75, v73, v75, s4
	v_add3_u32 v87, v72, v87, s4
	v_add3_u32 v74, v65, v74, s4
	v_and_b32_e32 v75, 0xffff0000, v75
	v_and_b32_e32 v87, 0xffff0000, v87
	v_or_b32_sdwa v75, v75, v74 dst_sel:DWORD dst_unused:UNUSED_PAD src0_sel:DWORD src1_sel:WORD_1
	v_or_b32_sdwa v74, v87, v86 dst_sel:DWORD dst_unused:UNUSED_PAD src0_sel:DWORD src1_sel:WORD_1
	global_store_dwordx2 v[66:67], v[74:75], off offset:1536
	v_pk_mul_f32 v[74:75], v[72:73], v[72:73]
	s_nop 0
	v_pk_fma_f32 v[86:87], v[64:65], v[64:65], v[74:75]
	v_cvt_pk_f32_fp8_e32 v[74:75], v144
	v_cvt_pk_f32_fp8_sdwa v[160:161], v170 src0_sel:WORD_1
	v_cvt_pk_f32_fp8_sdwa v[150:151], v144 src0_sel:WORD_1
	v_cvt_pk_f32_fp8_e32 v[158:159], v170
	v_cvt_pk_f32_fp8_e32 v[166:167], v184

	s_waitcnt vmcnt(47)
	v_cvt_pk_f32_fp8_sdwa v[190:191], v196 src0_sel:WORD_1
	v_cvt_pk_f32_fp8_sdwa v[174:175], v184 src0_sel:WORD_1
	v_cvt_pk_f32_fp8_e32 v[182:183], v196
	v_mov_b32_e32 v196, v74
	v_mov_b32_e32 v197, v160
	v_mov_b32_e32 v160, v75
	v_lshlrev_b32_e32 v193, 16, v69
	v_lshlrev_b32_e32 v192, 16, v68
	v_and_b32_e32 v195, 0xffff0000, v69
	v_and_b32_e32 v194, 0xffff0000, v68
	v_mov_b32_e32 v68, v158
	v_mov_b32_e32 v69, v150
	v_pk_mul_f32 v[196:197], v[196:197], v[58:59] op_sel:[0,1] op_sel_hi:[1,0]
	v_mov_b32_e32 v201, v190
	v_mov_b32_e32 v150, v159
	v_pk_mul_f32 v[74:75], v[160:161], v[58:59] op_sel:[0,1] op_sel_hi:[1,0]
	v_mov_b32_e32 v190, v167
	v_pk_fma_f32 v[68:69], v[68:69], v[58:59], v[196:197]
	v_mov_b32_e32 v197, v174
	v_mov_b32_e32 v200, v166
	v_pk_fma_f32 v[74:75], v[150:151], v[58:59], v[74:75]
	v_mov_b32_e32 v174, v183
	v_pk_mul_f32 v[150:151], v[190:191], v[50:51] op_sel:[0,1] op_sel_hi:[1,0]
	v_mov_b32_e32 v196, v182
	v_pk_mul_f32 v[200:201], v[200:201], v[50:51] op_sel:[0,1] op_sel_hi:[1,0]
	v_pk_fma_f32 v[150:151], v[174:175], v[50:51], v[150:151]
	v_pk_fma_f32 v[196:197], v[196:197], v[50:51], v[200:201]
	v_pk_add_f32 v[74:75], v[74:75], v[150:151]
	v_pk_add_f32 v[68:69], v[68:69], v[196:197]
	v_pk_add_f32 v[74:75], v[74:75], v[194:195]
	v_pk_add_f32 v[68:69], v[68:69], v[192:193]
	v_and_b32_sdwa v142, v75, v129 dst_sel:DWORD dst_unused:UNUSED_PAD src0_sel:WORD_1 src1_sel:DWORD
	v_and_b32_sdwa v144, v74, v129 dst_sel:DWORD dst_unused:UNUSED_PAD src0_sel:WORD_1 src1_sel:DWORD
	v_and_b32_sdwa v139, v69, v129 dst_sel:DWORD dst_unused:UNUSED_PAD src0_sel:WORD_1 src1_sel:DWORD
	v_and_b32_sdwa v141, v68, v129 dst_sel:DWORD dst_unused:UNUSED_PAD src0_sel:WORD_1 src1_sel:DWORD
	v_add3_u32 v142, v75, v142, s4
	v_add3_u32 v144, v74, v144, s4
	v_add3_u32 v141, v68, v141, s4
	v_add3_u32 v139, v69, v139, s4
	v_and_b32_e32 v142, 0xffff0000, v142
	v_and_b32_e32 v144, 0xffff0000, v144
	v_or_b32_sdwa v151, v142, v139 dst_sel:DWORD dst_unused:UNUSED_PAD src0_sel:DWORD src1_sel:WORD_1
	v_or_b32_sdwa v150, v144, v141 dst_sel:DWORD dst_unused:UNUSED_PAD src0_sel:DWORD src1_sel:WORD_1
	global_store_dwordx2 v[66:67], v[150:151], off offset:2048
	v_pk_mul_f32 v[150:151], v[74:75], v[74:75]
	s_nop 0
	v_pk_fma_f32 v[150:151], v[68:69], v[68:69], v[150:151]
	v_cvt_pk_f32_fp8_e32 v[158:159], v78
	v_cvt_pk_f32_fp8_sdwa v[160:161], v78 src0_sel:WORD_1
	v_cvt_pk_f32_fp8_e32 v[166:167], v79
	v_cvt_pk_f32_fp8_sdwa v[78:79], v79 src0_sel:WORD_1
	v_cvt_pk_f32_fp8_e32 v[174:175], v186

	s_waitcnt vmcnt(47)
	v_cvt_pk_f32_fp8_sdwa v[192:193], v199 src0_sel:WORD_1
	v_cvt_pk_f32_fp8_sdwa v[182:183], v186 src0_sel:WORD_1
	v_cvt_pk_f32_fp8_e32 v[190:191], v199
	v_mov_b32_e32 v200, v158
	v_mov_b32_e32 v201, v78
	v_lshlrev_b32_e32 v195, 16, v49
	v_lshlrev_b32_e32 v194, 16, v48
	v_and_b32_e32 v197, 0xffff0000, v49
	v_and_b32_e32 v196, 0xffff0000, v48
	v_mov_b32_e32 v48, v166
	v_mov_b32_e32 v49, v160
	v_pk_mul_f32 v[200:201], v[200:201], v[58:59] op_sel:[0,1] op_sel_hi:[1,0]
	v_mov_b32_e32 v203, v192
	v_mov_b32_e32 v78, v159
	v_mov_b32_e32 v192, v175
	v_pk_fma_f32 v[48:49], v[48:49], v[58:59], v[200:201]
	v_mov_b32_e32 v201, v182
	v_mov_b32_e32 v202, v174
	v_mov_b32_e32 v160, v167
	v_pk_mul_f32 v[78:79], v[78:79], v[58:59] op_sel:[0,1] op_sel_hi:[1,0]
	v_mov_b32_e32 v182, v191
	v_pk_mul_f32 v[158:159], v[192:193], v[50:51] op_sel:[0,1] op_sel_hi:[1,0]
	v_mov_b32_e32 v200, v190
	v_pk_mul_f32 v[202:203], v[202:203], v[50:51] op_sel:[0,1] op_sel_hi:[1,0]
	v_pk_fma_f32 v[78:79], v[160:161], v[58:59], v[78:79]
	v_pk_fma_f32 v[158:159], v[182:183], v[50:51], v[158:159]
	v_pk_fma_f32 v[200:201], v[200:201], v[50:51], v[202:203]
	v_pk_add_f32 v[78:79], v[78:79], v[158:159]
	v_pk_add_f32 v[48:49], v[48:49], v[200:201]
	v_pk_add_f32 v[78:79], v[78:79], v[196:197]
	v_pk_add_f32 v[48:49], v[48:49], v[194:195]
	v_and_b32_sdwa v142, v79, v129 dst_sel:DWORD dst_unused:UNUSED_PAD src0_sel:WORD_1 src1_sel:DWORD
	v_and_b32_sdwa v144, v78, v129 dst_sel:DWORD dst_unused:UNUSED_PAD src0_sel:WORD_1 src1_sel:DWORD
	v_and_b32_sdwa v139, v49, v129 dst_sel:DWORD dst_unused:UNUSED_PAD src0_sel:WORD_1 src1_sel:DWORD
	v_and_b32_sdwa v141, v48, v129 dst_sel:DWORD dst_unused:UNUSED_PAD src0_sel:WORD_1 src1_sel:DWORD
	v_add3_u32 v142, v79, v142, s4
	v_add3_u32 v144, v78, v144, s4
	v_add3_u32 v141, v48, v141, s4
	v_add3_u32 v139, v49, v139, s4
	v_and_b32_e32 v142, 0xffff0000, v142
	v_and_b32_e32 v144, 0xffff0000, v144
	v_or_b32_sdwa v159, v142, v139 dst_sel:DWORD dst_unused:UNUSED_PAD src0_sel:DWORD src1_sel:WORD_1
	v_or_b32_sdwa v158, v144, v141 dst_sel:DWORD dst_unused:UNUSED_PAD src0_sel:DWORD src1_sel:WORD_1
	global_store_dwordx2 v[66:67], v[158:159], off offset:2560
	v_pk_mul_f32 v[158:159], v[78:79], v[78:79]
	s_nop 0
	v_pk_fma_f32 v[158:159], v[48:49], v[48:49], v[158:159]
	v_cvt_pk_f32_fp8_e32 v[160:161], v80
	v_cvt_pk_f32_fp8_sdwa v[182:183], v81 src0_sel:WORD_1
	v_cvt_pk_f32_fp8_sdwa v[166:167], v80 src0_sel:WORD_1
	v_cvt_pk_f32_fp8_e32 v[174:175], v81
	v_cvt_pk_f32_fp8_e32 v[190:191], v84
	v_cvt_pk_f32_fp8_sdwa v[192:193], v84 src0_sel:WORD_1

	s_waitcnt vmcnt(47)
	v_cvt_pk_f32_fp8_e32 v[194:195], v85
	v_cvt_pk_f32_fp8_sdwa v[84:85], v85 src0_sel:WORD_1
	v_mov_b32_e32 v200, v160
	v_mov_b32_e32 v201, v182
	v_mov_b32_e32 v196, v174
	v_mov_b32_e32 v197, v166
	v_pk_mul_f32 v[200:201], v[200:201], v[58:59] op_sel:[0,1] op_sel_hi:[1,0]
	v_mov_b32_e32 v202, v190
	v_mov_b32_e32 v203, v84
	v_pk_fma_f32 v[196:197], v[196:197], v[58:59], v[200:201]
	v_mov_b32_e32 v200, v194
	v_mov_b32_e32 v201, v192
	v_pk_mul_f32 v[202:203], v[202:203], v[50:51] op_sel:[0,1] op_sel_hi:[1,0]
	v_mov_b32_e32 v182, v161
	v_mov_b32_e32 v84, v191
	v_pk_fma_f32 v[200:201], v[200:201], v[50:51], v[202:203]
	v_mov_b32_e32 v166, v175
	v_pk_mul_f32 v[160:161], v[182:183], v[58:59] op_sel:[0,1] op_sel_hi:[1,0]
	v_mov_b32_e32 v192, v195
	v_pk_mul_f32 v[84:85], v[84:85], v[50:51] op_sel:[0,1] op_sel_hi:[1,0]
	v_lshlrev_b32_e32 v81, 16, v29
	v_lshlrev_b32_e32 v80, 16, v28
	v_pk_add_f32 v[196:197], v[196:197], v[200:201]
	v_pk_fma_f32 v[160:161], v[166:167], v[58:59], v[160:161]
	v_pk_fma_f32 v[84:85], v[192:193], v[50:51], v[84:85]
	v_and_b32_e32 v29, 0xffff0000, v29
	v_and_b32_e32 v28, 0xffff0000, v28
	v_pk_add_f32 v[80:81], v[196:197], v[80:81]
	v_pk_add_f32 v[84:85], v[160:161], v[84:85]
	s_nop 0
	v_pk_add_f32 v[84:85], v[84:85], v[28:29]
	v_and_b32_sdwa v29, v80, v129 dst_sel:DWORD dst_unused:UNUSED_PAD src0_sel:WORD_1 src1_sel:DWORD
	v_add3_u32 v139, v80, v29, s4
	v_and_b32_sdwa v29, v85, v129 dst_sel:DWORD dst_unused:UNUSED_PAD src0_sel:WORD_1 src1_sel:DWORD
	v_and_b32_sdwa v141, v84, v129 dst_sel:DWORD dst_unused:UNUSED_PAD src0_sel:WORD_1 src1_sel:DWORD
	v_and_b32_sdwa v28, v81, v129 dst_sel:DWORD dst_unused:UNUSED_PAD src0_sel:WORD_1 src1_sel:DWORD
	v_add3_u32 v29, v85, v29, s4
	v_add3_u32 v141, v84, v141, s4
	v_add3_u32 v28, v81, v28, s4
	v_and_b32_e32 v29, 0xffff0000, v29
	v_and_b32_e32 v141, 0xffff0000, v141
	v_or_b32_sdwa v29, v29, v28 dst_sel:DWORD dst_unused:UNUSED_PAD src0_sel:DWORD src1_sel:WORD_1
	v_or_b32_sdwa v28, v141, v139 dst_sel:DWORD dst_unused:UNUSED_PAD src0_sel:DWORD src1_sel:WORD_1
	global_store_dwordx2 v[66:67], v[28:29], off offset:3072
	v_pk_mul_f32 v[28:29], v[84:85], v[84:85]
	s_nop 0
	v_pk_fma_f32 v[160:161], v[80:81], v[80:81], v[28:29]
	v_cvt_pk_f32_fp8_e32 v[166:167], v131
	v_cvt_pk_f32_fp8_sdwa v[190:191], v133 src0_sel:WORD_1
	v_cvt_pk_f32_fp8_sdwa v[174:175], v131 src0_sel:WORD_1
	v_cvt_pk_f32_fp8_e32 v[182:183], v133
	v_cvt_pk_f32_fp8_e32 v[192:193], v134

	s_waitcnt vmcnt(47)
	v_cvt_pk_f32_fp8_sdwa v[200:201], v136 src0_sel:WORD_1
	v_cvt_pk_f32_fp8_sdwa v[194:195], v134 src0_sel:WORD_1
	v_cvt_pk_f32_fp8_e32 v[196:197], v136
	v_mov_b32_e32 v204, v166
	v_mov_b32_e32 v205, v190
	v_mov_b32_e32 v202, v182
	v_mov_b32_e32 v203, v174
	v_pk_mul_f32 v[204:205], v[204:205], v[58:59] op_sel:[0,1] op_sel_hi:[1,0]
	v_mov_b32_e32 v206, v192
	v_mov_b32_e32 v207, v200
	v_mov_b32_e32 v190, v167
	v_pk_fma_f32 v[202:203], v[202:203], v[58:59], v[204:205]
	v_mov_b32_e32 v204, v196
	v_mov_b32_e32 v205, v194
	v_pk_mul_f32 v[206:207], v[206:207], v[50:51] op_sel:[0,1] op_sel_hi:[1,0]
	v_mov_b32_e32 v174, v183
	v_pk_mul_f32 v[166:167], v[190:191], v[58:59] op_sel:[0,1] op_sel_hi:[1,0]
	v_mov_b32_e32 v200, v193
	v_pk_fma_f32 v[204:205], v[204:205], v[50:51], v[206:207]
	v_pk_fma_f32 v[58:59], v[174:175], v[58:59], v[166:167]
	v_mov_b32_e32 v194, v197
	v_pk_mul_f32 v[166:167], v[200:201], v[50:51] op_sel:[0,1] op_sel_hi:[1,0]
	v_lshlrev_b32_e32 v29, 16, v23
	v_lshlrev_b32_e32 v28, 16, v22
	v_pk_add_f32 v[202:203], v[202:203], v[204:205]
	v_pk_fma_f32 v[50:51], v[194:195], v[50:51], v[166:167]
	v_and_b32_e32 v23, 0xffff0000, v23
	v_and_b32_e32 v22, 0xffff0000, v22
	v_pk_add_f32 v[28:29], v[202:203], v[28:29]
	v_pk_add_f32 v[50:51], v[58:59], v[50:51]
	s_nop 0
	v_pk_add_f32 v[58:59], v[50:51], v[22:23]
	v_and_b32_sdwa v23, v28, v129 dst_sel:DWORD dst_unused:UNUSED_PAD src0_sel:WORD_1 src1_sel:DWORD
	v_add3_u32 v50, v28, v23, s4
	v_and_b32_sdwa v23, v59, v129 dst_sel:DWORD dst_unused:UNUSED_PAD src0_sel:WORD_1 src1_sel:DWORD
	v_and_b32_sdwa v51, v58, v129 dst_sel:DWORD dst_unused:UNUSED_PAD src0_sel:WORD_1 src1_sel:DWORD
	v_and_b32_sdwa v22, v29, v129 dst_sel:DWORD dst_unused:UNUSED_PAD src0_sel:WORD_1 src1_sel:DWORD
	v_add3_u32 v23, v59, v23, s4
	v_add3_u32 v51, v58, v51, s4
	v_add3_u32 v22, v29, v22, s4
	v_and_b32_e32 v23, 0xffff0000, v23
	v_and_b32_e32 v51, 0xffff0000, v51
	v_or_b32_sdwa v23, v23, v22 dst_sel:DWORD dst_unused:UNUSED_PAD src0_sel:DWORD src1_sel:WORD_1
	v_or_b32_sdwa v22, v51, v50 dst_sel:DWORD dst_unused:UNUSED_PAD src0_sel:DWORD src1_sel:WORD_1
	v_add_f32_e32 v50, v76, v77
	v_add_f32_e32 v51, v70, v71
	v_add_f32_e32 v50, v51, v50
	v_add_f32_e32 v51, v82, v83
	v_add_f32_e32 v50, v50, v51
	v_add_f32_e32 v51, v86, v87
	v_add_f32_e32 v50, v50, v51
	v_add_f32_e32 v51, v150, v151
	global_store_dwordx2 v[66:67], v[22:23], off offset:3584
	v_pk_mul_f32 v[22:23], v[58:59], v[58:59]
	v_add_f32_e32 v50, v50, v51
	v_add_f32_e32 v51, v158, v159
	v_pk_fma_f32 v[22:23], v[28:29], v[28:29], v[22:23]
	v_add_f32_e32 v50, v50, v51
	v_add_f32_e32 v51, v160, v161
	v_add_f32_e32 v50, v50, v51
	v_add_f32_e32 v22, v22, v23
	v_add_f32_e32 v22, v50, v22
	v_mov_b64_e32 v[158:159], v[212:213]
	v_mov_b64_e32 v[160:161], v[214:215]
	ds_bpermute_b32 v23, v1, v22


	s_waitcnt vmcnt(16)
	v_cvt_pk_f32_fp8_sdwa v[82:83], v188 src0_sel:WORD_1
	v_mov_b32_e32 v189, v82
	s_waitcnt lgkmcnt(0)
	v_add_f32_e32 v22, v22, v23
	ds_bpermute_b32 v23, v90, v22
	s_waitcnt lgkmcnt(0)
	v_add_f32_e32 v22, v22, v23
	ds_bpermute_b32 v23, v91, v22
	s_waitcnt lgkmcnt(0)
	v_add_f32_e32 v22, v22, v23
	ds_bpermute_b32 v23, v92, v22
	s_waitcnt lgkmcnt(0)
	v_add_f32_e32 v22, v22, v23
	ds_bpermute_b32 v23, v93, v22
	s_waitcnt lgkmcnt(0)
	v_add_f32_e32 v22, v22, v23
	ds_bpermute_b32 v23, v94, v22
	s_waitcnt lgkmcnt(0)
	v_add_f32_e32 v22, v22, v23
	v_fmamk_f32 v22, v22, 0x3a000000, v127
	v_mul_f32_e32 v23, 0x4f800000, v22
	v_cmp_gt_f32_e32 vcc, s19, v22
	s_nop 1
	v_cndmask_b32_e32 v50, v22, v23, vcc
	v_sqrt_f32_e32 v51, v50
	v_lshl_add_u64 v[22:23], s[82:83], 0, v[14:15]
	v_add_u32_e32 v66, -1, v51
	v_add_u32_e32 v67, 1, v51
	v_fma_f32 v70, -v66, v51, v50
	v_fma_f32 v71, -v67, v51, v50
	v_cmp_ge_f32_e64 s[8:9], 0, v70
	s_nop 1
	v_cndmask_b32_e64 v51, v51, v66, s[8:9]
	v_cmp_lt_f32_e64 s[8:9], 0, v71
	s_nop 1
	v_cndmask_b32_e64 v51, v51, v67, s[8:9]
	v_mul_f32_e32 v66, 0x37800000, v51
	v_cndmask_b32_e32 v51, v51, v66, vcc
	v_cmp_class_f32_e32 vcc, v50, v128
	v_mov_b32_e32 v67, 0
	s_nop 0
	v_cndmask_b32_e32 v50, v51, v50, vcc
	v_div_scale_f32 v51, s[0:1], v50, v50, 1.0
	v_rcp_f32_e32 v66, v51
	v_div_scale_f32 v70, vcc, 1.0, v50, 1.0
	v_fma_f32 v71, -v51, v66, 1.0
	v_fmac_f32_e32 v66, v71, v66
	v_mul_f32_e32 v71, v70, v66
	v_fma_f32 v76, -v51, v71, v70
	v_fmac_f32_e32 v71, v76, v66
	v_fma_f32 v51, -v51, v71, v70
	v_div_fmas_f32 v51, v51, v66, v71
	v_div_fixup_f32 v66, v51, v50, 1.0
	v_mul_f32_e32 v24, v66, v24
	v_mul_f32_e32 v34, v66, v34

	v_mul_f32_e32 v24, v158, v24
	v_mul_f32_e32 v34, v159, v34
	v_cvt_pk_fp8_f32 v67, v24, v34
	v_mul_f32_e32 v25, v66, v25
	v_mul_f32_e32 v24, v66, v35
	v_mul_f32_e32 v25, v160, v25
	v_mul_f32_e32 v24, v161, v24
	v_cvt_pk_fp8_f32 v67, v25, v24 op_sel:[0,0,1]
	v_add_co_u32_e32 v24, vcc, s30, v22
	v_mul_f32_e32 v35, v66, v40
	s_nop 0
	v_addc_co_u32_e32 v25, vcc, 0, v23, vcc
	global_store_dword v[24:25], v67, off offset:-4096
	v_mov_b64_e32 v[158:159], v[216:217]
	v_mov_b64_e32 v[160:161], v[218:219]
	v_mul_f32_e32 v40, v66, v44
	v_mov_b32_e32 v34, 0
	v_mul_f32_e32 v41, v66, v41
	v_add_co_u32_e32 v50, vcc, s21, v22
	v_mul_f32_e32 v28, v66, v28
	s_nop 0
	v_addc_co_u32_e32 v51, vcc, 0, v23, vcc
	ds_bpermute_b32 v44, v105, v130
	v_mul_f32_e32 v29, v66, v29
	ds_bpermute_b32 v67, v102, v19
	v_cvt_pk_f32_fp8_sdwa v[70:71], v181 src0_sel:WORD_1
	v_cvt_pk_f32_fp8_e32 v[76:77], v187
	v_mov_b32_e32 v82, v77

	v_mul_f32_e32 v35, v158, v35
	v_mul_f32_e32 v40, v159, v40
	v_cvt_pk_fp8_f32 v34, v35, v40
	v_mul_f32_e32 v35, v66, v45
	v_mul_f32_e32 v40, v160, v41
	v_mul_f32_e32 v35, v161, v35
	v_cvt_pk_fp8_f32 v34, v40, v35 op_sel:[0,0,1]
	v_mul_f32_e32 v35, v66, v54
	v_mul_f32_e32 v40, v66, v62
	v_mul_f32_e32 v41, v66, v55
	global_store_dword v[50:51], v34, off offset:256
	v_mov_b64_e32 v[158:159], v[220:221]
	v_mov_b64_e32 v[160:161], v[222:223]
	v_mov_b32_e32 v34, 0
	v_mul_f32_e32 v55, v66, v58
	v_mov_b32_e32 v54, 0
	s_waitcnt lgkmcnt(1)
	v_ashrrev_i32_e32 v45, 31, v44
	v_lshlrev_b64 v[44:45], 11, v[44:45]

	v_mul_f32_e32 v35, v158, v35
	v_mul_f32_e32 v40, v159, v40
	v_cvt_pk_fp8_f32 v34, v35, v40
	v_mul_f32_e32 v35, v66, v63
	v_mul_f32_e32 v40, v160, v41
	v_mul_f32_e32 v35, v161, v35
	v_cvt_pk_fp8_f32 v34, v40, v35 op_sel:[0,0,1]
	v_mul_f32_e32 v35, v66, v64
	v_mul_f32_e32 v40, v66, v72
	v_mul_f32_e32 v41, v66, v65
	global_store_dword v[50:51], v34, off offset:512
	v_mov_b64_e32 v[158:159], v[224:225]
	v_mov_b64_e32 v[160:161], v[226:227]
	v_mov_b32_e32 v34, 0

	v_mul_f32_e32 v35, v158, v35
	v_mul_f32_e32 v40, v159, v40
	v_cvt_pk_fp8_f32 v34, v35, v40
	v_mul_f32_e32 v35, v66, v73
	v_mul_f32_e32 v40, v160, v41
	v_mul_f32_e32 v35, v161, v35
	v_cvt_pk_fp8_f32 v34, v40, v35 op_sel:[0,0,1]
	v_mul_f32_e32 v35, v66, v68
	v_mul_f32_e32 v40, v66, v74
	v_mul_f32_e32 v41, v66, v69
	global_store_dword v[50:51], v34, off offset:768
	v_mov_b64_e32 v[62:63], v[228:229]
	v_mov_b64_e32 v[64:65], v[230:231]
	v_mov_b32_e32 v34, 0
	ds_bpermute_b32 v69, v100, v19
	ds_bpermute_b32 v68, v101, v19
	v_cvt_pk_f32_fp8_e32 v[72:73], v185

	v_mul_f32_e32 v35, v62, v35
	v_mul_f32_e32 v40, v63, v40
	v_cvt_pk_fp8_f32 v34, v35, v40
	v_mul_f32_e32 v35, v66, v75
	v_mul_f32_e32 v40, v64, v41
	v_mul_f32_e32 v35, v65, v35
	v_cvt_pk_fp8_f32 v34, v40, v35 op_sel:[0,0,1]
	v_mul_f32_e32 v35, v66, v48
	v_mul_f32_e32 v40, v66, v78
	v_mul_f32_e32 v41, v66, v49
	global_store_dword v[50:51], v34, off offset:1024
	v_mov_b64_e32 v[62:63], v[232:233]
	v_mov_b64_e32 v[64:65], v[234:235]
	v_mov_b32_e32 v34, 0
	ds_bpermute_b32 v48, v104, v130
	v_cvt_pk_f32_fp8_sdwa v[74:75], v185 src0_sel:WORD_1
	s_waitcnt lgkmcnt(0)
	v_ashrrev_i32_e32 v49, 31, v48
	v_lshlrev_b64 v[48:49], 11, v[48:49]
	v_mov_b32_e32 v87, v74

	v_mul_f32_e32 v35, v62, v35
	v_mul_f32_e32 v40, v63, v40
	v_cvt_pk_fp8_f32 v34, v35, v40
	v_mul_f32_e32 v35, v66, v79
	v_mul_f32_e32 v40, v64, v41
	v_mul_f32_e32 v35, v65, v35
	v_cvt_pk_fp8_f32 v34, v40, v35 op_sel:[0,0,1]
	v_mul_f32_e32 v35, v66, v80
	v_mul_f32_e32 v40, v66, v84
	v_mul_f32_e32 v41, v66, v81
	global_store_dword v[50:51], v34, off offset:1280
	v_mov_b64_e32 v[62:63], v[236:237]
	v_mov_b64_e32 v[64:65], v[238:239]
	v_mov_b32_e32 v34, 0
	v_cvt_pk_f32_fp8_sdwa v[78:79], v187 src0_sel:WORD_1
	v_cvt_pk_f32_fp8_e32 v[80:81], v188
	v_mov_b32_e32 v84, v72
	v_mov_b32_e32 v188, v76

	v_mul_f32_e32 v35, v62, v35
	v_mul_f32_e32 v40, v63, v40
	v_cvt_pk_fp8_f32 v34, v35, v40
	v_mul_f32_e32 v35, v66, v85
	v_mul_f32_e32 v40, v64, v41
	v_mul_f32_e32 v35, v65, v35
	v_cvt_pk_fp8_f32 v34, v40, v35 op_sel:[0,0,1]
	ds_bpermute_b32 v40, v106, v130
	v_mov_b32_e32 v85, v70
	v_mov_b32_e32 v70, v73
	global_store_dword v[50:51], v34, off offset:1536
	v_mov_b64_e32 v[62:63], v[240:241]
	v_mov_b64_e32 v[64:65], v[242:243]
	ds_bpermute_b32 v34, v107, v130
	s_waitcnt lgkmcnt(1)
	v_ashrrev_i32_e32 v41, 31, v40
	v_lshlrev_b64 v[40:41], 11, v[40:41]
	s_waitcnt lgkmcnt(0)
	v_ashrrev_i32_e32 v35, 31, v34
	v_lshlrev_b64 v[34:35], 11, v[34:35]
	v_lshl_add_u64 v[34:35], v[4:5], 0, v[34:35]

	v_mul_f32_e32 v28, v62, v28
	v_mul_f32_e32 v55, v63, v55
	v_cvt_pk_fp8_f32 v54, v28, v55
	v_mul_f32_e32 v28, v66, v59
	v_mul_f32_e32 v29, v64, v29
	v_mul_f32_e32 v28, v65, v28
	v_cvt_pk_fp8_f32 v54, v29, v28 op_sel:[0,0,1]
	v_lshl_add_u64 v[28:29], v[4:5], 0, v[40:41]
	v_lshl_add_u64 v[40:41], v[4:5], 0, v[44:45]
	v_lshl_add_u64 v[44:45], v[4:5], 0, v[48:49]
	global_store_dword v[50:51], v54, off offset:1792
	global_load_dword v131, v[34:35], off offset:1792 nt
	global_load_dword v139, v[34:35], off offset:1536 nt
	global_load_dword v149, v[34:35], off offset:1280 nt
	global_load_dword v158, v[34:35], off offset:1024 nt
	global_load_dword v166, v[34:35], off offset:768 nt
	global_load_dword v174, v[34:35], off offset:512 nt
	global_load_dword v182, v[34:35], off offset:256 nt
	global_load_dword v190, v[34:35], off nt
	global_load_dword v133, v[28:29], off offset:1792 nt
	global_load_dword v141, v[28:29], off offset:1536 nt
	global_load_dword v150, v[28:29], off offset:1280 nt
	global_load_dword v159, v[28:29], off offset:1024 nt
	global_load_dword v167, v[28:29], off offset:768 nt
	global_load_dword v175, v[28:29], off offset:512 nt
	global_load_dword v183, v[28:29], off offset:256 nt
	global_load_dword v191, v[28:29], off nt
	global_load_dword v134, v[40:41], off offset:1792 nt
	global_load_dword v142, v[40:41], off offset:1536 nt
	global_load_dword v151, v[40:41], off offset:1280 nt
	global_load_dword v160, v[40:41], off offset:1024 nt
	global_load_dword v168, v[40:41], off offset:768 nt
	global_load_dword v176, v[40:41], off offset:512 nt
	global_load_dword v184, v[40:41], off offset:256 nt
	global_load_dword v193, v[40:41], off nt
	global_load_dword v136, v[44:45], off offset:1792 nt
	global_load_dword v144, v[44:45], off offset:1536 nt
	global_load_dword v152, v[44:45], off offset:1280 nt
	global_load_dword v161, v[44:45], off offset:1024 nt
	global_load_dword v170, v[44:45], off offset:768 nt
	global_load_dword v178, v[44:45], off offset:512 nt
	global_load_dword v186, v[44:45], off offset:256 nt
	global_load_dword v196, v[44:45], off nt
	global_load_dwordx2 v[28:29], v[56:57], off offset:3584 nt
	global_load_dwordx2 v[34:35], v[56:57], off offset:3072 nt
	global_load_dwordx2 v[40:41], v[56:57], off offset:2560 nt
	s_nop 0
	global_load_dwordx2 v[44:45], v[56:57], off offset:2048 nt
	global_load_dwordx2 v[48:49], v[56:57], off offset:1536 nt
	global_load_dwordx2 v[54:55], v[56:57], off offset:1024 nt
	global_load_dwordx2 v[58:59], v[56:57], off offset:512 nt
	global_load_dwordx2 v[62:63], v[56:57], off nt
	v_cvt_pk_f32_fp8_e32 v[64:65], v181
	ds_bpermute_b32 v66, v103, v19
	s_waitcnt vmcnt(63)
	v_lshlrev_b32_e32 v57, 16, v61
	v_lshlrev_b32_e32 v56, 16, v60
	v_mov_b32_e32 v86, v64
	v_pk_mul_f32 v[86:87], v[86:87], v[68:69] op_sel:[0,1] op_sel_hi:[1,0]
	v_mov_b32_e32 v74, v65
	v_pk_fma_f32 v[84:85], v[84:85], v[68:69], v[86:87]
	v_mov_b32_e32 v86, v80
	v_mov_b32_e32 v87, v78
	s_waitcnt lgkmcnt(0)
	v_pk_mul_f32 v[188:189], v[188:189], v[66:67] op_sel:[0,1] op_sel_hi:[1,0]
	v_pk_mul_f32 v[64:65], v[74:75], v[68:69] op_sel:[0,1] op_sel_hi:[1,0]
	v_pk_fma_f32 v[86:87], v[86:87], v[66:67], v[188:189]
	v_pk_fma_f32 v[64:65], v[70:71], v[68:69], v[64:65]
	v_mov_b32_e32 v78, v81
	v_pk_mul_f32 v[70:71], v[82:83], v[66:67] op_sel:[0,1] op_sel_hi:[1,0]
	v_pk_add_f32 v[84:85], v[84:85], v[86:87]
	v_pk_fma_f32 v[70:71], v[78:79], v[66:67], v[70:71]
	v_and_b32_e32 v61, 0xffff0000, v61
	v_and_b32_e32 v60, 0xffff0000, v60
	v_pk_add_f32 v[56:57], v[84:85], v[56:57]
	v_pk_add_f32 v[64:65], v[64:65], v[70:71]
	s_nop 0
	v_pk_add_f32 v[60:61], v[64:65], v[60:61]
	v_and_b32_sdwa v65, v56, v129 dst_sel:DWORD dst_unused:UNUSED_PAD src0_sel:WORD_1 src1_sel:DWORD
	v_add3_u32 v70, v56, v65, s4
	v_and_b32_sdwa v65, v61, v129 dst_sel:DWORD dst_unused:UNUSED_PAD src0_sel:WORD_1 src1_sel:DWORD
	v_and_b32_sdwa v71, v60, v129 dst_sel:DWORD dst_unused:UNUSED_PAD src0_sel:WORD_1 src1_sel:DWORD
	v_and_b32_sdwa v64, v57, v129 dst_sel:DWORD dst_unused:UNUSED_PAD src0_sel:WORD_1 src1_sel:DWORD
	v_add3_u32 v65, v61, v65, s4
	v_add3_u32 v71, v60, v71, s4
	v_add3_u32 v64, v57, v64, s4
	v_and_b32_e32 v65, 0xffff0000, v65
	v_and_b32_e32 v71, 0xffff0000, v71
	v_or_b32_sdwa v65, v65, v64 dst_sel:DWORD dst_unused:UNUSED_PAD src0_sel:DWORD src1_sel:WORD_1
	v_or_b32_sdwa v64, v71, v70 dst_sel:DWORD dst_unused:UNUSED_PAD src0_sel:DWORD src1_sel:WORD_1
	global_store_dwordx2 v[32:33], v[64:65], off
	v_pk_mul_f32 v[64:65], v[60:61], v[60:61]
	s_nop 0
	v_pk_fma_f32 v[72:73], v[56:57], v[56:57], v[64:65]
	v_cvt_pk_f32_fp8_e32 v[64:65], v173
	v_cvt_pk_f32_fp8_sdwa v[76:77], v177 src0_sel:WORD_1
	v_cvt_pk_f32_fp8_sdwa v[70:71], v173 src0_sel:WORD_1
	v_cvt_pk_f32_fp8_e32 v[74:75], v177
	v_cvt_pk_f32_fp8_e32 v[78:79], v179
	s_waitcnt vmcnt(63)
	v_cvt_pk_f32_fp8_sdwa v[84:85], v180 src0_sel:WORD_1
	v_cvt_pk_f32_fp8_sdwa v[80:81], v179 src0_sel:WORD_1
	v_cvt_pk_f32_fp8_e32 v[82:83], v180
	v_mov_b32_e32 v188, v64
	v_mov_b32_e32 v189, v76
	v_lshlrev_b32_e32 v87, 16, v53
	v_lshlrev_b32_e32 v86, 16, v52
	v_and_b32_e32 v181, 0xffff0000, v53
	v_and_b32_e32 v180, 0xffff0000, v52
	v_mov_b32_e32 v52, v74
	v_mov_b32_e32 v53, v70
	v_pk_mul_f32 v[188:189], v[188:189], v[68:69] op_sel:[0,1] op_sel_hi:[1,0]
	v_mov_b32_e32 v194, v78
	v_mov_b32_e32 v195, v84
	v_mov_b32_e32 v76, v65
	v_pk_fma_f32 v[52:53], v[52:53], v[68:69], v[188:189]
	v_mov_b32_e32 v188, v82
	v_mov_b32_e32 v189, v80
	v_pk_mul_f32 v[194:195], v[194:195], v[66:67] op_sel:[0,1] op_sel_hi:[1,0]
	v_mov_b32_e32 v70, v75
	v_pk_mul_f32 v[64:65], v[76:77], v[68:69] op_sel:[0,1] op_sel_hi:[1,0]
	v_mov_b32_e32 v84, v79
	v_pk_fma_f32 v[188:189], v[188:189], v[66:67], v[194:195]
	v_pk_fma_f32 v[64:65], v[70:71], v[68:69], v[64:65]
	v_mov_b32_e32 v80, v83
	v_pk_mul_f32 v[70:71], v[84:85], v[66:67] op_sel:[0,1] op_sel_hi:[1,0]
	v_pk_add_f32 v[52:53], v[52:53], v[188:189]
	v_pk_fma_f32 v[70:71], v[80:81], v[66:67], v[70:71]
	v_pk_add_f32 v[52:53], v[52:53], v[86:87]
	v_pk_add_f32 v[64:65], v[64:65], v[70:71]
	v_and_b32_sdwa v71, v52, v129 dst_sel:DWORD dst_unused:UNUSED_PAD src0_sel:WORD_1 src1_sel:DWORD
	v_pk_add_f32 v[64:65], v[64:65], v[180:181]
	v_add3_u32 v74, v52, v71, s4
	v_and_b32_sdwa v71, v65, v129 dst_sel:DWORD dst_unused:UNUSED_PAD src0_sel:WORD_1 src1_sel:DWORD
	v_and_b32_sdwa v75, v64, v129 dst_sel:DWORD dst_unused:UNUSED_PAD src0_sel:WORD_1 src1_sel:DWORD
	v_and_b32_sdwa v70, v53, v129 dst_sel:DWORD dst_unused:UNUSED_PAD src0_sel:WORD_1 src1_sel:DWORD
	v_add3_u32 v71, v65, v71, s4
	v_add3_u32 v75, v64, v75, s4
	v_add3_u32 v70, v53, v70, s4
	v_and_b32_e32 v71, 0xffff0000, v71
	v_and_b32_e32 v75, 0xffff0000, v75
	v_or_b32_sdwa v71, v71, v70 dst_sel:DWORD dst_unused:UNUSED_PAD src0_sel:DWORD src1_sel:WORD_1
	v_or_b32_sdwa v70, v75, v74 dst_sel:DWORD dst_unused:UNUSED_PAD src0_sel:DWORD src1_sel:WORD_1
	global_store_dwordx2 v[32:33], v[70:71], off offset:512
	v_pk_mul_f32 v[70:71], v[64:65], v[64:65]
	s_nop 0
	v_pk_fma_f32 v[78:79], v[52:53], v[52:53], v[70:71]
	v_cvt_pk_f32_fp8_e32 v[70:71], v165
	v_cvt_pk_f32_fp8_sdwa v[80:81], v169 src0_sel:WORD_1
	v_cvt_pk_f32_fp8_sdwa v[74:75], v165 src0_sel:WORD_1
	v_cvt_pk_f32_fp8_e32 v[76:77], v169
	v_cvt_pk_f32_fp8_e32 v[82:83], v171
	s_waitcnt vmcnt(63)
	v_cvt_pk_f32_fp8_e32 v[86:87], v172
	v_cvt_pk_f32_fp8_sdwa v[172:173], v172 src0_sel:WORD_1
	v_cvt_pk_f32_fp8_sdwa v[84:85], v171 src0_sel:WORD_1
	v_mov_b32_e32 v194, v70
	v_mov_b32_e32 v195, v80
	v_lshlrev_b32_e32 v181, 16, v47
	v_lshlrev_b32_e32 v180, 16, v46
	v_and_b32_e32 v189, 0xffff0000, v47
	v_and_b32_e32 v188, 0xffff0000, v46
	v_mov_b32_e32 v46, v76
	v_mov_b32_e32 v47, v74
	v_pk_mul_f32 v[194:195], v[194:195], v[68:69] op_sel:[0,1] op_sel_hi:[1,0]
	v_mov_b32_e32 v200, v82
	v_mov_b32_e32 v201, v172
	v_mov_b32_e32 v80, v71
	v_pk_fma_f32 v[46:47], v[46:47], v[68:69], v[194:195]
	v_mov_b32_e32 v194, v86
	v_mov_b32_e32 v195, v84
	v_pk_mul_f32 v[200:201], v[200:201], v[66:67] op_sel:[0,1] op_sel_hi:[1,0]
	v_mov_b32_e32 v74, v77
	v_pk_mul_f32 v[70:71], v[80:81], v[68:69] op_sel:[0,1] op_sel_hi:[1,0]
	v_mov_b32_e32 v172, v83
	v_pk_fma_f32 v[194:195], v[194:195], v[66:67], v[200:201]
	v_pk_fma_f32 v[70:71], v[74:75], v[68:69], v[70:71]
	v_mov_b32_e32 v84, v87
	v_pk_mul_f32 v[74:75], v[172:173], v[66:67] op_sel:[0,1] op_sel_hi:[1,0]
	v_pk_add_f32 v[46:47], v[46:47], v[194:195]
	v_pk_fma_f32 v[74:75], v[84:85], v[66:67], v[74:75]
	v_pk_add_f32 v[46:47], v[46:47], v[180:181]
	v_pk_add_f32 v[70:71], v[70:71], v[74:75]
	v_and_b32_sdwa v75, v46, v129 dst_sel:DWORD dst_unused:UNUSED_PAD src0_sel:WORD_1 src1_sel:DWORD
	v_pk_add_f32 v[70:71], v[70:71], v[188:189]
	v_add3_u32 v76, v46, v75, s4
	v_and_b32_sdwa v75, v71, v129 dst_sel:DWORD dst_unused:UNUSED_PAD src0_sel:WORD_1 src1_sel:DWORD
	v_and_b32_sdwa v77, v70, v129 dst_sel:DWORD dst_unused:UNUSED_PAD src0_sel:WORD_1 src1_sel:DWORD
	v_and_b32_sdwa v74, v47, v129 dst_sel:DWORD dst_unused:UNUSED_PAD src0_sel:WORD_1 src1_sel:DWORD
	v_add3_u32 v75, v71, v75, s4
	v_add3_u32 v77, v70, v77, s4
	v_add3_u32 v74, v47, v74, s4
	v_and_b32_e32 v75, 0xffff0000, v75
	v_and_b32_e32 v77, 0xffff0000, v77
	v_or_b32_sdwa v75, v75, v74 dst_sel:DWORD dst_unused:UNUSED_PAD src0_sel:DWORD src1_sel:WORD_1
	v_or_b32_sdwa v74, v77, v76 dst_sel:DWORD dst_unused:UNUSED_PAD src0_sel:DWORD src1_sel:WORD_1
	global_store_dwordx2 v[32:33], v[74:75], off offset:1024
	v_pk_mul_f32 v[74:75], v[70:71], v[70:71]
	s_nop 0
	v_pk_fma_f32 v[82:83], v[46:47], v[46:47], v[74:75]
	v_cvt_pk_f32_fp8_e32 v[74:75], v88
	v_cvt_pk_f32_fp8_sdwa v[84:85], v89 src0_sel:WORD_1
	v_cvt_pk_f32_fp8_sdwa v[76:77], v88 src0_sel:WORD_1
	v_cvt_pk_f32_fp8_e32 v[80:81], v89
	v_cvt_pk_f32_fp8_e32 v[86:87], v163
	s_waitcnt vmcnt(63)
	v_cvt_pk_f32_fp8_e32 v[172:173], v164
	v_cvt_pk_f32_fp8_sdwa v[164:165], v164 src0_sel:WORD_1
	v_cvt_pk_f32_fp8_sdwa v[88:89], v163 src0_sel:WORD_1
	v_mov_b32_e32 v194, v74
	v_mov_b32_e32 v195, v84
	v_lshlrev_b32_e32 v181, 16, v43
	v_lshlrev_b32_e32 v180, 16, v42
	v_and_b32_e32 v189, 0xffff0000, v43
	v_and_b32_e32 v188, 0xffff0000, v42
	v_mov_b32_e32 v42, v80
	v_mov_b32_e32 v43, v76
	v_pk_mul_f32 v[194:195], v[194:195], v[68:69] op_sel:[0,1] op_sel_hi:[1,0]
	v_mov_b32_e32 v200, v86
	v_mov_b32_e32 v201, v164
	v_mov_b32_e32 v84, v75
	v_pk_fma_f32 v[42:43], v[42:43], v[68:69], v[194:195]
	v_mov_b32_e32 v194, v172
	v_mov_b32_e32 v195, v88
	v_pk_mul_f32 v[200:201], v[200:201], v[66:67] op_sel:[0,1] op_sel_hi:[1,0]
	v_mov_b32_e32 v76, v81
	v_pk_mul_f32 v[74:75], v[84:85], v[68:69] op_sel:[0,1] op_sel_hi:[1,0]
	v_mov_b32_e32 v164, v87
	v_pk_fma_f32 v[194:195], v[194:195], v[66:67], v[200:201]
	v_pk_fma_f32 v[74:75], v[76:77], v[68:69], v[74:75]
	v_mov_b32_e32 v88, v173
	v_pk_mul_f32 v[76:77], v[164:165], v[66:67] op_sel:[0,1] op_sel_hi:[1,0]
	v_pk_add_f32 v[42:43], v[42:43], v[194:195]
	v_pk_fma_f32 v[76:77], v[88:89], v[66:67], v[76:77]
	v_pk_add_f32 v[42:43], v[42:43], v[180:181]
	v_pk_add_f32 v[74:75], v[74:75], v[76:77]
	v_and_b32_sdwa v77, v42, v129 dst_sel:DWORD dst_unused:UNUSED_PAD src0_sel:WORD_1 src1_sel:DWORD
	v_pk_add_f32 v[74:75], v[74:75], v[188:189]
	v_add3_u32 v80, v42, v77, s4
	v_and_b32_sdwa v77, v75, v129 dst_sel:DWORD dst_unused:UNUSED_PAD src0_sel:WORD_1 src1_sel:DWORD
	v_and_b32_sdwa v81, v74, v129 dst_sel:DWORD dst_unused:UNUSED_PAD src0_sel:WORD_1 src1_sel:DWORD
	v_and_b32_sdwa v76, v43, v129 dst_sel:DWORD dst_unused:UNUSED_PAD src0_sel:WORD_1 src1_sel:DWORD
	v_add3_u32 v77, v75, v77, s4
	v_add3_u32 v81, v74, v81, s4
	v_add3_u32 v76, v43, v76, s4
	v_and_b32_e32 v77, 0xffff0000, v77
	v_and_b32_e32 v81, 0xffff0000, v81
	v_or_b32_sdwa v77, v77, v76 dst_sel:DWORD dst_unused:UNUSED_PAD src0_sel:DWORD src1_sel:WORD_1
	v_or_b32_sdwa v76, v81, v80 dst_sel:DWORD dst_unused:UNUSED_PAD src0_sel:DWORD src1_sel:WORD_1
	global_store_dwordx2 v[32:33], v[76:77], off offset:1536
	v_pk_mul_f32 v[76:77], v[74:75], v[74:75]
	s_nop 0
	v_pk_fma_f32 v[88:89], v[42:43], v[42:43], v[76:77]
	v_cvt_pk_f32_fp8_e32 v[76:77], v155
	v_cvt_pk_f32_fp8_sdwa v[86:87], v156 src0_sel:WORD_1
	v_cvt_pk_f32_fp8_sdwa v[80:81], v155 src0_sel:WORD_1
	v_cvt_pk_f32_fp8_e32 v[84:85], v156
	v_cvt_pk_f32_fp8_e32 v[164:165], v157
	s_waitcnt vmcnt(63)
	v_cvt_pk_f32_fp8_e32 v[172:173], v162
	v_cvt_pk_f32_fp8_sdwa v[162:163], v162 src0_sel:WORD_1
	v_cvt_pk_f32_fp8_sdwa v[156:157], v157 src0_sel:WORD_1
	v_mov_b32_e32 v194, v76
	v_mov_b32_e32 v195, v86
	v_lshlrev_b32_e32 v181, 16, v39
	v_lshlrev_b32_e32 v180, 16, v38
	v_and_b32_e32 v189, 0xffff0000, v39
	v_and_b32_e32 v188, 0xffff0000, v38
	v_mov_b32_e32 v38, v84
	v_mov_b32_e32 v39, v80
	v_pk_mul_f32 v[194:195], v[194:195], v[68:69] op_sel:[0,1] op_sel_hi:[1,0]
	v_mov_b32_e32 v200, v164
	v_mov_b32_e32 v201, v162
	v_mov_b32_e32 v86, v77
	v_pk_fma_f32 v[38:39], v[38:39], v[68:69], v[194:195]
	v_mov_b32_e32 v194, v172
	v_mov_b32_e32 v195, v156
	v_pk_mul_f32 v[200:201], v[200:201], v[66:67] op_sel:[0,1] op_sel_hi:[1,0]
	v_mov_b32_e32 v80, v85
	v_pk_mul_f32 v[76:77], v[86:87], v[68:69] op_sel:[0,1] op_sel_hi:[1,0]
	v_mov_b32_e32 v162, v165
	v_pk_fma_f32 v[194:195], v[194:195], v[66:67], v[200:201]
	v_pk_fma_f32 v[76:77], v[80:81], v[68:69], v[76:77]
	v_mov_b32_e32 v156, v173
	v_pk_mul_f32 v[80:81], v[162:163], v[66:67] op_sel:[0,1] op_sel_hi:[1,0]
	v_pk_add_f32 v[38:39], v[38:39], v[194:195]
	v_pk_fma_f32 v[80:81], v[156:157], v[66:67], v[80:81]
	v_pk_add_f32 v[38:39], v[38:39], v[180:181]
	v_pk_add_f32 v[76:77], v[76:77], v[80:81]
	v_and_b32_sdwa v81, v38, v129 dst_sel:DWORD dst_unused:UNUSED_PAD src0_sel:WORD_1 src1_sel:DWORD
	v_pk_add_f32 v[76:77], v[76:77], v[188:189]
	v_add3_u32 v84, v38, v81, s4
	v_and_b32_sdwa v81, v77, v129 dst_sel:DWORD dst_unused:UNUSED_PAD src0_sel:WORD_1 src1_sel:DWORD
	v_and_b32_sdwa v85, v76, v129 dst_sel:DWORD dst_unused:UNUSED_PAD src0_sel:WORD_1 src1_sel:DWORD
	v_and_b32_sdwa v80, v39, v129 dst_sel:DWORD dst_unused:UNUSED_PAD src0_sel:WORD_1 src1_sel:DWORD
	v_add3_u32 v81, v77, v81, s4
	v_add3_u32 v85, v76, v85, s4
	v_add3_u32 v80, v39, v80, s4
	v_and_b32_e32 v81, 0xffff0000, v81
	v_and_b32_e32 v85, 0xffff0000, v85
	v_or_b32_sdwa v81, v81, v80 dst_sel:DWORD dst_unused:UNUSED_PAD src0_sel:DWORD src1_sel:WORD_1
	v_or_b32_sdwa v80, v85, v84 dst_sel:DWORD dst_unused:UNUSED_PAD src0_sel:DWORD src1_sel:WORD_1
	global_store_dwordx2 v[32:33], v[80:81], off offset:2048
	v_pk_mul_f32 v[80:81], v[76:77], v[76:77]
	s_nop 0
	v_pk_fma_f32 v[156:157], v[38:39], v[38:39], v[80:81]
	v_cvt_pk_f32_fp8_e32 v[80:81], v147
	v_cvt_pk_f32_fp8_sdwa v[162:163], v148 src0_sel:WORD_1
	v_cvt_pk_f32_fp8_sdwa v[84:85], v147 src0_sel:WORD_1
	v_cvt_pk_f32_fp8_e32 v[86:87], v148
	v_cvt_pk_f32_fp8_e32 v[164:165], v153
	s_waitcnt vmcnt(63)
	v_cvt_pk_f32_fp8_e32 v[180:181], v154
	v_cvt_pk_f32_fp8_sdwa v[154:155], v154 src0_sel:WORD_1
	v_cvt_pk_f32_fp8_sdwa v[172:173], v153 src0_sel:WORD_1
	v_mov_b32_e32 v200, v80
	v_mov_b32_e32 v201, v162
	v_lshlrev_b32_e32 v189, 16, v37
	v_lshlrev_b32_e32 v188, 16, v36
	v_and_b32_e32 v195, 0xffff0000, v37
	v_and_b32_e32 v194, 0xffff0000, v36
	v_mov_b32_e32 v36, v86
	v_mov_b32_e32 v37, v84
	v_pk_mul_f32 v[200:201], v[200:201], v[68:69] op_sel:[0,1] op_sel_hi:[1,0]
	v_mov_b32_e32 v202, v164
	v_mov_b32_e32 v203, v154
	v_mov_b32_e32 v162, v81
	v_pk_fma_f32 v[36:37], v[36:37], v[68:69], v[200:201]
	v_mov_b32_e32 v200, v180
	v_mov_b32_e32 v201, v172
	v_pk_mul_f32 v[202:203], v[202:203], v[66:67] op_sel:[0,1] op_sel_hi:[1,0]
	v_mov_b32_e32 v84, v87
	v_pk_mul_f32 v[80:81], v[162:163], v[68:69] op_sel:[0,1] op_sel_hi:[1,0]
	v_mov_b32_e32 v154, v165
	v_pk_fma_f32 v[200:201], v[200:201], v[66:67], v[202:203]
	v_pk_fma_f32 v[80:81], v[84:85], v[68:69], v[80:81]
	v_mov_b32_e32 v172, v181
	v_pk_mul_f32 v[84:85], v[154:155], v[66:67] op_sel:[0,1] op_sel_hi:[1,0]
	v_pk_add_f32 v[36:37], v[36:37], v[200:201]
	v_pk_fma_f32 v[84:85], v[172:173], v[66:67], v[84:85]
	v_pk_add_f32 v[36:37], v[36:37], v[188:189]
	v_pk_add_f32 v[80:81], v[80:81], v[84:85]
	v_and_b32_sdwa v85, v36, v129 dst_sel:DWORD dst_unused:UNUSED_PAD src0_sel:WORD_1 src1_sel:DWORD
	v_pk_add_f32 v[80:81], v[80:81], v[194:195]
	v_add3_u32 v86, v36, v85, s4
	v_and_b32_sdwa v85, v81, v129 dst_sel:DWORD dst_unused:UNUSED_PAD src0_sel:WORD_1 src1_sel:DWORD
	v_and_b32_sdwa v87, v80, v129 dst_sel:DWORD dst_unused:UNUSED_PAD src0_sel:WORD_1 src1_sel:DWORD
	v_and_b32_sdwa v84, v37, v129 dst_sel:DWORD dst_unused:UNUSED_PAD src0_sel:WORD_1 src1_sel:DWORD
	v_add3_u32 v85, v81, v85, s4
	v_add3_u32 v87, v80, v87, s4
	v_add3_u32 v84, v37, v84, s4
	v_and_b32_e32 v85, 0xffff0000, v85
	v_and_b32_e32 v87, 0xffff0000, v87
	v_or_b32_sdwa v85, v85, v84 dst_sel:DWORD dst_unused:UNUSED_PAD src0_sel:DWORD src1_sel:WORD_1
	v_or_b32_sdwa v84, v87, v86 dst_sel:DWORD dst_unused:UNUSED_PAD src0_sel:DWORD src1_sel:WORD_1
	global_store_dwordx2 v[32:33], v[84:85], off offset:2560
	v_pk_mul_f32 v[84:85], v[80:81], v[80:81]
	s_nop 0
	v_pk_fma_f32 v[154:155], v[36:37], v[36:37], v[84:85]
	v_cvt_pk_f32_fp8_e32 v[86:87], v140
	v_cvt_pk_f32_fp8_sdwa v[172:173], v143 src0_sel:WORD_1
	v_cvt_pk_f32_fp8_sdwa v[162:163], v140 src0_sel:WORD_1
	v_cvt_pk_f32_fp8_e32 v[164:165], v143
	v_cvt_pk_f32_fp8_e32 v[180:181], v145
	s_waitcnt vmcnt(63)
	v_cvt_pk_f32_fp8_e32 v[194:195], v146
	v_cvt_pk_f32_fp8_sdwa v[146:147], v146 src0_sel:WORD_1
	v_cvt_pk_f32_fp8_sdwa v[188:189], v145 src0_sel:WORD_1
	v_mov_b32_e32 v202, v86
	v_mov_b32_e32 v203, v172
	v_mov_b32_e32 v200, v164
	v_mov_b32_e32 v201, v162
	v_pk_mul_f32 v[202:203], v[202:203], v[68:69] op_sel:[0,1] op_sel_hi:[1,0]
	v_mov_b32_e32 v204, v180
	v_mov_b32_e32 v205, v146
	v_pk_fma_f32 v[200:201], v[200:201], v[68:69], v[202:203]
	v_mov_b32_e32 v202, v194
	v_mov_b32_e32 v203, v188
	v_pk_mul_f32 v[204:205], v[204:205], v[66:67] op_sel:[0,1] op_sel_hi:[1,0]
	v_mov_b32_e32 v172, v87
	v_mov_b32_e32 v146, v181
	v_pk_fma_f32 v[202:203], v[202:203], v[66:67], v[204:205]
	v_mov_b32_e32 v162, v165
	v_pk_mul_f32 v[86:87], v[172:173], v[68:69] op_sel:[0,1] op_sel_hi:[1,0]
	v_mov_b32_e32 v188, v195
	v_pk_mul_f32 v[146:147], v[146:147], v[66:67] op_sel:[0,1] op_sel_hi:[1,0]
	v_lshlrev_b32_e32 v85, 16, v31
	v_lshlrev_b32_e32 v84, 16, v30
	v_pk_add_f32 v[200:201], v[200:201], v[202:203]
	v_pk_fma_f32 v[86:87], v[162:163], v[68:69], v[86:87]
	v_pk_fma_f32 v[146:147], v[188:189], v[66:67], v[146:147]
	v_and_b32_e32 v31, 0xffff0000, v31
	v_and_b32_e32 v30, 0xffff0000, v30
	v_pk_add_f32 v[84:85], v[200:201], v[84:85]
	v_pk_add_f32 v[86:87], v[86:87], v[146:147]
	s_nop 0
	v_pk_add_f32 v[86:87], v[86:87], v[30:31]
	v_and_b32_sdwa v31, v84, v129 dst_sel:DWORD dst_unused:UNUSED_PAD src0_sel:WORD_1 src1_sel:DWORD
	v_add3_u32 v140, v84, v31, s4
	v_and_b32_sdwa v31, v87, v129 dst_sel:DWORD dst_unused:UNUSED_PAD src0_sel:WORD_1 src1_sel:DWORD
	v_and_b32_sdwa v143, v86, v129 dst_sel:DWORD dst_unused:UNUSED_PAD src0_sel:WORD_1 src1_sel:DWORD
	v_and_b32_sdwa v30, v85, v129 dst_sel:DWORD dst_unused:UNUSED_PAD src0_sel:WORD_1 src1_sel:DWORD
	v_add3_u32 v31, v87, v31, s4
	v_add3_u32 v143, v86, v143, s4
	v_add3_u32 v30, v85, v30, s4
	v_and_b32_e32 v31, 0xffff0000, v31
	v_and_b32_e32 v143, 0xffff0000, v143
	v_or_b32_sdwa v31, v31, v30 dst_sel:DWORD dst_unused:UNUSED_PAD src0_sel:DWORD src1_sel:WORD_1
	v_or_b32_sdwa v30, v143, v140 dst_sel:DWORD dst_unused:UNUSED_PAD src0_sel:DWORD src1_sel:WORD_1
	global_store_dwordx2 v[32:33], v[30:31], off offset:3072
	v_pk_mul_f32 v[30:31], v[86:87], v[86:87]
	s_nop 0
	v_pk_fma_f32 v[146:147], v[84:85], v[84:85], v[30:31]
	v_cvt_pk_f32_fp8_e32 v[30:31], v132
	v_cvt_pk_f32_fp8_sdwa v[172:173], v135 src0_sel:WORD_1
	v_cvt_pk_f32_fp8_sdwa v[162:163], v132 src0_sel:WORD_1
	v_cvt_pk_f32_fp8_e32 v[164:165], v135
	v_cvt_pk_f32_fp8_e32 v[180:181], v137
	s_waitcnt vmcnt(63)
	v_cvt_pk_f32_fp8_sdwa v[200:201], v138 src0_sel:WORD_1
	v_cvt_pk_f32_fp8_sdwa v[188:189], v137 src0_sel:WORD_1
	v_cvt_pk_f32_fp8_e32 v[194:195], v138
	v_mov_b32_e32 v206, v30
	v_mov_b32_e32 v207, v172
	v_lshlrev_b32_e32 v203, 16, v27
	v_lshlrev_b32_e32 v202, 16, v26
	v_and_b32_e32 v205, 0xffff0000, v27
	v_and_b32_e32 v204, 0xffff0000, v26
	v_mov_b32_e32 v26, v164
	v_mov_b32_e32 v27, v162
	v_pk_mul_f32 v[206:207], v[206:207], v[68:69] op_sel:[0,1] op_sel_hi:[1,0]
	v_mov_b32_e32 v208, v180
	v_mov_b32_e32 v209, v200
	v_mov_b32_e32 v172, v31
	v_pk_fma_f32 v[26:27], v[26:27], v[68:69], v[206:207]
	v_mov_b32_e32 v206, v194
	v_mov_b32_e32 v207, v188
	v_pk_mul_f32 v[208:209], v[208:209], v[66:67] op_sel:[0,1] op_sel_hi:[1,0]
	v_mov_b32_e32 v162, v165
	v_pk_mul_f32 v[30:31], v[172:173], v[68:69] op_sel:[0,1] op_sel_hi:[1,0]
	v_mov_b32_e32 v200, v181
	v_pk_fma_f32 v[206:207], v[206:207], v[66:67], v[208:209]
	v_pk_fma_f32 v[30:31], v[162:163], v[68:69], v[30:31]
	v_mov_b32_e32 v188, v195
	v_pk_mul_f32 v[68:69], v[200:201], v[66:67] op_sel:[0,1] op_sel_hi:[1,0]
	v_pk_add_f32 v[26:27], v[26:27], v[206:207]
	v_pk_fma_f32 v[66:67], v[188:189], v[66:67], v[68:69]
	v_pk_add_f32 v[26:27], v[26:27], v[202:203]
	v_pk_add_f32 v[30:31], v[30:31], v[66:67]
	v_and_b32_sdwa v67, v26, v129 dst_sel:DWORD dst_unused:UNUSED_PAD src0_sel:WORD_1 src1_sel:DWORD
	v_pk_add_f32 v[30:31], v[30:31], v[204:205]
	v_add3_u32 v68, v26, v67, s4
	v_and_b32_sdwa v67, v31, v129 dst_sel:DWORD dst_unused:UNUSED_PAD src0_sel:WORD_1 src1_sel:DWORD
	v_and_b32_sdwa v69, v30, v129 dst_sel:DWORD dst_unused:UNUSED_PAD src0_sel:WORD_1 src1_sel:DWORD
	v_and_b32_sdwa v66, v27, v129 dst_sel:DWORD dst_unused:UNUSED_PAD src0_sel:WORD_1 src1_sel:DWORD
	v_add3_u32 v67, v31, v67, s4
	v_add3_u32 v69, v30, v69, s4
	v_add3_u32 v66, v27, v66, s4
	v_and_b32_e32 v67, 0xffff0000, v67
	v_and_b32_e32 v69, 0xffff0000, v69
	v_or_b32_sdwa v67, v67, v66 dst_sel:DWORD dst_unused:UNUSED_PAD src0_sel:DWORD src1_sel:WORD_1
	v_or_b32_sdwa v66, v69, v68 dst_sel:DWORD dst_unused:UNUSED_PAD src0_sel:DWORD src1_sel:WORD_1
	global_store_dwordx2 v[32:33], v[66:67], off offset:3584
	v_add_f32_e32 v66, v78, v79
	v_add_f32_e32 v67, v72, v73
	v_add_f32_e32 v66, v67, v66
	v_add_f32_e32 v67, v82, v83
	v_add_f32_e32 v66, v66, v67
	v_add_f32_e32 v67, v88, v89
	v_add_f32_e32 v66, v66, v67
	v_add_f32_e32 v67, v156, v157
	v_pk_mul_f32 v[32:33], v[30:31], v[30:31]
	v_add_f32_e32 v66, v66, v67
	v_add_f32_e32 v67, v154, v155
	v_pk_fma_f32 v[32:33], v[26:27], v[26:27], v[32:33]
	v_add_f32_e32 v66, v66, v67
	v_add_f32_e32 v67, v146, v147
	v_add_f32_e32 v66, v66, v67
	v_add_f32_e32 v32, v32, v33
	v_add_f32_e32 v32, v66, v32
	v_mov_b64_e32 v[66:67], v[212:213]
	v_mov_b64_e32 v[68:69], v[214:215]
	ds_bpermute_b32 v33, v1, v32
	s_waitcnt lgkmcnt(0)
	v_add_f32_e32 v32, v32, v33
	ds_bpermute_b32 v33, v90, v32
	s_waitcnt lgkmcnt(0)
	v_add_f32_e32 v32, v32, v33
	ds_bpermute_b32 v33, v91, v32
	s_waitcnt lgkmcnt(0)
	v_add_f32_e32 v32, v32, v33
	ds_bpermute_b32 v33, v92, v32
	s_waitcnt lgkmcnt(0)
	v_add_f32_e32 v32, v32, v33
	ds_bpermute_b32 v33, v93, v32
	s_waitcnt lgkmcnt(0)
	v_add_f32_e32 v32, v32, v33
	ds_bpermute_b32 v33, v94, v32
	s_waitcnt lgkmcnt(0)
	v_add_f32_e32 v32, v32, v33
	v_fmamk_f32 v32, v32, 0x3a000000, v127
	v_mul_f32_e32 v33, 0x4f800000, v32
	v_cmp_gt_f32_e32 vcc, s19, v32
	s_nop 1
	v_cndmask_b32_e32 v32, v32, v33, vcc
	v_sqrt_f32_e32 v33, v32
	s_nop 0
	v_add_u32_e32 v72, -1, v33
	v_add_u32_e32 v73, 1, v33
	v_fma_f32 v78, -v72, v33, v32
	v_fma_f32 v79, -v73, v33, v32
	v_cmp_ge_f32_e64 s[8:9], 0, v78
	s_nop 1
	v_cndmask_b32_e64 v33, v33, v72, s[8:9]
	v_cmp_lt_f32_e64 s[8:9], 0, v79
	s_nop 1
	v_cndmask_b32_e64 v33, v33, v73, s[8:9]
	v_mul_f32_e32 v72, 0x37800000, v33
	v_cndmask_b32_e32 v33, v33, v72, vcc
	v_cmp_class_f32_e32 vcc, v32, v128
	v_mov_b32_e32 v73, 0
	s_nop 0
	v_cndmask_b32_e32 v32, v33, v32, vcc
	v_div_scale_f32 v33, s[0:1], v32, v32, 1.0
	v_rcp_f32_e32 v72, v33
	v_div_scale_f32 v78, vcc, 1.0, v32, 1.0
	v_fma_f32 v79, -v33, v72, 1.0
	v_fmac_f32_e32 v72, v79, v72
	v_mul_f32_e32 v79, v78, v72
	v_fma_f32 v82, -v33, v79, v78
	v_fmac_f32_e32 v79, v82, v72
	v_fma_f32 v33, -v33, v79, v78
	v_div_fmas_f32 v33, v33, v72, v79
	v_div_fixup_f32 v72, v33, v32, 1.0
	v_mul_f32_e32 v32, v72, v56
	v_mul_f32_e32 v33, v72, v60

	v_mul_f32_e32 v32, v66, v32
	v_mul_f32_e32 v33, v67, v33
	v_cvt_pk_fp8_f32 v73, v32, v33
	v_mul_f32_e32 v56, v72, v57
	v_mul_f32_e32 v32, v72, v61
	v_mul_f32_e32 v33, v68, v56
	v_mul_f32_e32 v32, v69, v32
	v_cvt_pk_fp8_f32 v73, v33, v32 op_sel:[0,0,1]
	v_mul_f32_e32 v33, v72, v52
	v_mul_f32_e32 v52, v72, v64
	v_mov_b32_e32 v32, 0
	global_store_dword v[50:51], v73, off offset:2048
	v_mov_b64_e32 v[66:67], v[216:217]
	v_mov_b64_e32 v[68:69], v[218:219]
	v_mul_f32_e32 v53, v72, v53
	v_mul_f32_e32 v47, v72, v47
	v_mul_f32_e32 v43, v72, v43
	v_mul_f32_e32 v39, v72, v39
	v_mul_f32_e32 v37, v72, v37
	v_mul_f32_e32 v26, v72, v26
	v_mul_f32_e32 v30, v72, v30
	ds_bpermute_b32 v56, v111, v130
	v_mul_f32_e32 v27, v72, v27
	s_waitcnt vmcnt(41)
	v_cvt_pk_f32_fp8_e32 v[78:79], v190
	s_waitcnt lgkmcnt(0)
	v_ashrrev_i32_e32 v57, 31, v56
	v_lshlrev_b64 v[56:57], 11, v[56:57]

	v_mul_f32_e32 v33, v66, v33
	v_mul_f32_e32 v52, v67, v52
	v_cvt_pk_fp8_f32 v32, v33, v52
	v_mul_f32_e32 v33, v72, v65
	v_mul_f32_e32 v52, v68, v53
	v_mul_f32_e32 v33, v69, v33
	v_cvt_pk_fp8_f32 v32, v52, v33 op_sel:[0,0,1]
	v_mul_f32_e32 v33, v72, v46
	v_mul_f32_e32 v46, v72, v70
	v_mov_b32_e32 v68, 0
	global_store_dword v[50:51], v32, off offset:2304
	v_mov_b64_e32 v[64:65], v[220:221]
	v_mov_b64_e32 v[66:67], v[222:223]
	v_mov_b32_e32 v32, 0
	v_add_co_u32_e32 v52, vcc, s28, v20
	ds_bpermute_b32 v69, v104, v19
	s_nop 0
	v_addc_co_u32_e32 v53, vcc, 0, v21, vcc
	v_add_co_u32_e32 v60, vcc, s31, v20

	v_mul_f32_e32 v33, v64, v33
	v_mul_f32_e32 v46, v65, v46
	v_cvt_pk_fp8_f32 v32, v33, v46
	v_mul_f32_e32 v33, v72, v71
	v_mul_f32_e32 v46, v66, v47
	v_mul_f32_e32 v33, v67, v33
	v_cvt_pk_fp8_f32 v32, v46, v33 op_sel:[0,0,1]
	v_mul_f32_e32 v33, v72, v42
	v_mul_f32_e32 v42, v72, v74
	ds_bpermute_b32 v46, v110, v130
	global_store_dword v[50:51], v32, off offset:2560
	v_mov_b64_e32 v[64:65], v[224:225]
	v_mov_b64_e32 v[66:67], v[226:227]
	v_mov_b32_e32 v32, 0
	v_addc_co_u32_e32 v61, vcc, 0, v21, vcc
	s_waitcnt lgkmcnt(0)
	v_ashrrev_i32_e32 v47, 31, v46
	v_lshlrev_b64 v[46:47], 11, v[46:47]
	s_waitcnt vmcnt(27)
	v_cvt_pk_f32_fp8_e32 v[70:71], v193
	v_mov_b32_e32 v82, v70

	v_mul_f32_e32 v33, v64, v33
	v_mul_f32_e32 v42, v65, v42
	v_cvt_pk_fp8_f32 v32, v33, v42
	v_mul_f32_e32 v33, v72, v75
	v_mul_f32_e32 v42, v66, v43
	v_mul_f32_e32 v33, v67, v33
	v_cvt_pk_fp8_f32 v32, v42, v33 op_sel:[0,0,1]
	v_mul_f32_e32 v33, v72, v38
	v_mul_f32_e32 v38, v72, v76
	v_mul_f32_e32 v42, v72, v86
	global_store_dword v[50:51], v32, off offset:2816
	v_mov_b64_e32 v[64:65], v[228:229]
	v_mov_b64_e32 v[66:67], v[230:231]
	v_mov_b32_e32 v32, 0
	v_mul_f32_e32 v43, v72, v85
	v_cvt_pk_f32_fp8_e32 v[74:75], v191
	v_mov_b32_e32 v86, v74

	v_mul_f32_e32 v33, v64, v33
	v_mul_f32_e32 v38, v65, v38
	v_cvt_pk_fp8_f32 v32, v33, v38
	v_mul_f32_e32 v33, v72, v77
	v_mul_f32_e32 v38, v66, v39
	v_mul_f32_e32 v33, v67, v33
	v_cvt_pk_fp8_f32 v32, v38, v33 op_sel:[0,0,1]
	v_mul_f32_e32 v33, v72, v36
	v_mul_f32_e32 v36, v72, v80
	v_cvt_pk_f32_fp8_sdwa v[76:77], v191 src0_sel:WORD_1
	global_store_dword v[50:51], v32, off offset:3072
	v_mov_b64_e32 v[64:65], v[232:233]
	v_mov_b64_e32 v[66:67], v[234:235]
	v_mov_b32_e32 v32, 0

	v_mul_f32_e32 v33, v64, v33
	v_mul_f32_e32 v36, v65, v36
	v_cvt_pk_fp8_f32 v32, v33, v36
	v_mul_f32_e32 v33, v72, v81
	v_mul_f32_e32 v36, v66, v37
	v_mul_f32_e32 v33, v67, v33
	v_cvt_pk_fp8_f32 v32, v36, v33 op_sel:[0,0,1]
	v_mul_f32_e32 v33, v72, v84
	v_lshl_add_u64 v[66:67], v[4:5], 0, v[56:57]
	v_cvt_pk_f32_fp8_sdwa v[80:81], v190 src0_sel:WORD_1
	global_store_dword v[50:51], v32, off offset:3328
	v_mov_b64_e32 v[36:37], v[236:237]
	v_mov_b64_e32 v[38:39], v[238:239]
	v_mov_b32_e32 v32, 0

	v_mul_f32_e32 v33, v36, v33
	v_mul_f32_e32 v36, v37, v42
	v_cvt_pk_fp8_f32 v32, v33, v36
	v_mul_f32_e32 v33, v72, v87
	v_mul_f32_e32 v36, v38, v43
	v_mul_f32_e32 v33, v39, v33
	v_cvt_pk_fp8_f32 v32, v36, v33 op_sel:[0,0,1]
	ds_bpermute_b32 v42, v109, v130
	v_mov_b32_e32 v87, v80
	v_mov_b32_e32 v80, v75
	global_store_dword v[50:51], v32, off offset:3584
	v_mov_b64_e32 v[36:37], v[240:241]
	v_mov_b64_e32 v[38:39], v[242:243]
	ds_bpermute_b32 v32, v108, v130
	s_waitcnt lgkmcnt(1)
	v_ashrrev_i32_e32 v43, 31, v42
	v_lshlrev_b64 v[42:43], 11, v[42:43]
	s_waitcnt lgkmcnt(0)
	v_ashrrev_i32_e32 v33, 31, v32
	v_lshlrev_b64 v[32:33], 11, v[32:33]
	v_lshl_add_u64 v[64:65], v[4:5], 0, v[32:33]

	v_mul_f32_e32 v26, v36, v26
	v_mul_f32_e32 v30, v37, v30
	v_cvt_pk_fp8_f32 v68, v26, v30
	v_mul_f32_e32 v26, v72, v31
	v_mul_f32_e32 v27, v38, v27
	v_mul_f32_e32 v26, v39, v26
	v_cvt_pk_fp8_f32 v68, v27, v26 op_sel:[0,0,1]
	v_lshl_add_u64 v[30:31], v[4:5], 0, v[42:43]
	v_lshl_add_u64 v[38:39], v[4:5], 0, v[46:47]
	v_cvt_pk_f32_fp8_sdwa v[72:73], v193 src0_sel:WORD_1
	global_store_dword v[50:51], v68, off offset:3840
	global_load_dwordx2 v[56:57], v[52:53], off offset:512 nt
	s_nop 0
	global_load_dwordx2 v[50:51], v[52:53], off offset:1024 nt
	global_load_dwordx2 v[46:47], v[52:53], off offset:1536 nt
	global_load_dwordx2 v[42:43], v[52:53], off offset:2048 nt
	global_load_dwordx2 v[36:37], v[52:53], off offset:2560 nt
	global_load_dwordx2 v[32:33], v[52:53], off offset:3072 nt
	global_load_dwordx2 v[26:27], v[52:53], off offset:3584 nt
	global_load_dword v192, v[64:65], off nt
	global_load_dword v185, v[64:65], off offset:256 nt
	global_load_dword v177, v[64:65], off offset:512 nt
	global_load_dword v169, v[64:65], off offset:768 nt
	global_load_dword v162, v[64:65], off offset:1024 nt
	global_load_dword v154, v[64:65], off offset:1280 nt
	global_load_dword v145, v[64:65], off offset:1536 nt
	global_load_dword v132, v[64:65], off offset:1792 nt
	global_load_dword v194, v[30:31], off nt
	global_load_dword v187, v[30:31], off offset:256 nt
	global_load_dword v179, v[30:31], off offset:512 nt
	global_load_dword v171, v[30:31], off offset:768 nt
	global_load_dword v163, v[30:31], off offset:1024 nt
	global_load_dword v155, v[30:31], off offset:1280 nt
	global_load_dword v146, v[30:31], off offset:1536 nt
	global_load_dword v135, v[30:31], off offset:1792 nt
	global_load_dword v195, v[38:39], off nt
	global_load_dword v188, v[38:39], off offset:256 nt
	global_load_dword v180, v[38:39], off offset:512 nt
	global_load_dword v172, v[38:39], off offset:768 nt
	global_load_dword v164, v[38:39], off offset:1024 nt
	global_load_dword v156, v[38:39], off offset:1280 nt
	global_load_dword v147, v[38:39], off offset:1536 nt
	global_load_dword v137, v[38:39], off offset:1792 nt
	global_load_dword v197, v[66:67], off nt
	global_load_dwordx2 v[64:65], v[60:61], off offset:-4096 nt
	global_load_dword v189, v[66:67], off offset:256 nt
	global_load_dword v181, v[66:67], off offset:512 nt
	global_load_dword v173, v[66:67], off offset:768 nt
	global_load_dword v165, v[66:67], off offset:1024 nt
	global_load_dword v157, v[66:67], off offset:1280 nt
	global_load_dword v148, v[66:67], off offset:1536 nt
	global_load_dword v138, v[66:67], off offset:1792 nt
	ds_bpermute_b32 v68, v105, v19
	s_waitcnt vmcnt(63)
	v_cvt_pk_f32_fp8_e32 v[30:31], v196
	ds_bpermute_b32 v67, v106, v19
	ds_bpermute_b32 v66, v107, v19
	v_cvt_pk_f32_fp8_sdwa v[52:53], v196 src0_sel:WORD_1
	v_mov_b32_e32 v84, v30
	v_mov_b32_e32 v85, v72
	v_mov_b32_e32 v72, v31
	v_mov_b32_e32 v83, v52
	s_waitcnt lgkmcnt(2)
	v_pk_mul_f32 v[84:85], v[84:85], v[68:69] op_sel:[0,1] op_sel_hi:[1,0]
	v_mov_b32_e32 v52, v71
	v_pk_mul_f32 v[30:31], v[72:73], v[68:69] op_sel:[0,1] op_sel_hi:[1,0]
	v_pk_fma_f32 v[82:83], v[82:83], v[68:69], v[84:85]
	v_mov_b32_e32 v85, v76
	v_pk_fma_f32 v[30:31], v[52:53], v[68:69], v[30:31]
	v_mov_b32_e32 v76, v79
	s_waitcnt lgkmcnt(0)
	v_pk_mul_f32 v[52:53], v[80:81], v[66:67] op_sel:[0,1] op_sel_hi:[1,0]
	v_mov_b32_e32 v84, v78
	v_pk_mul_f32 v[86:87], v[86:87], v[66:67] op_sel:[0,1] op_sel_hi:[1,0]
	v_pk_fma_f32 v[52:53], v[76:77], v[66:67], v[52:53]
	s_waitcnt vmcnt(56)
	v_lshlrev_b32_e32 v39, 16, v63
	v_lshlrev_b32_e32 v38, 16, v62
	v_and_b32_e32 v63, 0xffff0000, v63
	v_and_b32_e32 v62, 0xffff0000, v62
	v_pk_fma_f32 v[84:85], v[84:85], v[66:67], v[86:87]
	v_pk_add_f32 v[30:31], v[30:31], v[52:53]
	v_pk_add_f32 v[82:83], v[82:83], v[84:85]
	v_pk_add_f32 v[52:53], v[30:31], v[62:63]
	v_pk_add_f32 v[38:39], v[82:83], v[38:39]
	v_and_b32_sdwa v62, v53, v129 dst_sel:DWORD dst_unused:UNUSED_PAD src0_sel:WORD_1 src1_sel:DWORD
	v_and_b32_sdwa v30, v39, v129 dst_sel:DWORD dst_unused:UNUSED_PAD src0_sel:WORD_1 src1_sel:DWORD
	v_and_b32_sdwa v63, v52, v129 dst_sel:DWORD dst_unused:UNUSED_PAD src0_sel:WORD_1 src1_sel:DWORD
	v_add3_u32 v62, v53, v62, s4
	v_add_co_u32_e32 v72, vcc, s29, v20
	v_and_b32_sdwa v31, v38, v129 dst_sel:DWORD dst_unused:UNUSED_PAD src0_sel:WORD_1 src1_sel:DWORD
	v_add3_u32 v30, v39, v30, s4
	v_add3_u32 v63, v52, v63, s4
	v_and_b32_e32 v62, 0xffff0000, v62
	v_addc_co_u32_e32 v73, vcc, 0, v21, vcc
	v_add3_u32 v31, v38, v31, s4
	v_and_b32_e32 v70, 0xffff0000, v63
	v_or_b32_sdwa v63, v62, v30 dst_sel:DWORD dst_unused:UNUSED_PAD src0_sel:DWORD src1_sel:WORD_1
	v_add_co_u32_e32 v30, vcc, s33, v20
	v_or_b32_sdwa v62, v70, v31 dst_sel:DWORD dst_unused:UNUSED_PAD src0_sel:DWORD src1_sel:WORD_1
	s_nop 0
	v_addc_co_u32_e32 v31, vcc, 0, v21, vcc
	global_store_dwordx2 v[30:31], v[62:63], off offset:-4096
	v_pk_mul_f32 v[62:63], v[52:53], v[52:53]
	s_nop 0
	v_pk_fma_f32 v[74:75], v[38:39], v[38:39], v[62:63]
	v_cvt_pk_f32_fp8_e32 v[62:63], v186
	v_cvt_pk_f32_fp8_sdwa v[78:79], v184 src0_sel:WORD_1
	v_cvt_pk_f32_fp8_sdwa v[70:71], v186 src0_sel:WORD_1
	v_cvt_pk_f32_fp8_e32 v[76:77], v184
	v_cvt_pk_f32_fp8_e32 v[80:81], v183
	v_cvt_pk_f32_fp8_sdwa v[86:87], v182 src0_sel:WORD_1
	v_cvt_pk_f32_fp8_sdwa v[82:83], v183 src0_sel:WORD_1
	v_cvt_pk_f32_fp8_e32 v[84:85], v182
	v_mov_b32_e32 v190, v62
	v_mov_b32_e32 v191, v78
	v_lshlrev_b32_e32 v89, 16, v59
	v_lshlrev_b32_e32 v88, 16, v58
	v_and_b32_e32 v183, 0xffff0000, v59
	v_and_b32_e32 v182, 0xffff0000, v58
	v_mov_b32_e32 v58, v76
	v_mov_b32_e32 v59, v70
	v_pk_mul_f32 v[190:191], v[190:191], v[68:69] op_sel:[0,1] op_sel_hi:[1,0]
	v_mov_b32_e32 v200, v80
	v_mov_b32_e32 v201, v86
	v_mov_b32_e32 v78, v63
	v_pk_fma_f32 v[58:59], v[58:59], v[68:69], v[190:191]
	v_mov_b32_e32 v190, v84
	v_mov_b32_e32 v191, v82
	v_pk_mul_f32 v[200:201], v[200:201], v[66:67] op_sel:[0,1] op_sel_hi:[1,0]
	v_mov_b32_e32 v70, v77
	v_pk_mul_f32 v[62:63], v[78:79], v[68:69] op_sel:[0,1] op_sel_hi:[1,0]
	v_mov_b32_e32 v86, v81
	v_pk_fma_f32 v[190:191], v[190:191], v[66:67], v[200:201]
	v_pk_fma_f32 v[62:63], v[70:71], v[68:69], v[62:63]
	v_mov_b32_e32 v82, v85
	v_pk_mul_f32 v[70:71], v[86:87], v[66:67] op_sel:[0,1] op_sel_hi:[1,0]
	v_pk_add_f32 v[58:59], v[58:59], v[190:191]
	v_pk_fma_f32 v[70:71], v[82:83], v[66:67], v[70:71]
	v_pk_add_f32 v[58:59], v[58:59], v[88:89]
	v_pk_add_f32 v[62:63], v[62:63], v[70:71]
	v_and_b32_sdwa v71, v58, v129 dst_sel:DWORD dst_unused:UNUSED_PAD src0_sel:WORD_1 src1_sel:DWORD
	v_pk_add_f32 v[62:63], v[62:63], v[182:183]
	v_add3_u32 v76, v58, v71, s4
	v_and_b32_sdwa v71, v63, v129 dst_sel:DWORD dst_unused:UNUSED_PAD src0_sel:WORD_1 src1_sel:DWORD
	v_and_b32_sdwa v77, v62, v129 dst_sel:DWORD dst_unused:UNUSED_PAD src0_sel:WORD_1 src1_sel:DWORD
	v_and_b32_sdwa v70, v59, v129 dst_sel:DWORD dst_unused:UNUSED_PAD src0_sel:WORD_1 src1_sel:DWORD
	v_add3_u32 v71, v63, v71, s4
	v_add3_u32 v77, v62, v77, s4
	v_add3_u32 v70, v59, v70, s4
	v_and_b32_e32 v71, 0xffff0000, v71
	v_and_b32_e32 v77, 0xffff0000, v77
	v_or_b32_sdwa v71, v71, v70 dst_sel:DWORD dst_unused:UNUSED_PAD src0_sel:DWORD src1_sel:WORD_1
	v_or_b32_sdwa v70, v77, v76 dst_sel:DWORD dst_unused:UNUSED_PAD src0_sel:DWORD src1_sel:WORD_1
	global_store_dwordx2 v[72:73], v[70:71], off offset:512
	v_pk_mul_f32 v[70:71], v[62:63], v[62:63]
	s_nop 0
	v_pk_fma_f32 v[80:81], v[58:59], v[58:59], v[70:71]
	v_cvt_pk_f32_fp8_e32 v[70:71], v178
	v_cvt_pk_f32_fp8_sdwa v[82:83], v176 src0_sel:WORD_1
	v_cvt_pk_f32_fp8_sdwa v[76:77], v178 src0_sel:WORD_1
	v_cvt_pk_f32_fp8_e32 v[78:79], v176
	v_cvt_pk_f32_fp8_e32 v[84:85], v175
	v_cvt_pk_f32_fp8_sdwa v[86:87], v175 src0_sel:WORD_1
	v_cvt_pk_f32_fp8_e32 v[88:89], v174
	v_cvt_pk_f32_fp8_sdwa v[174:175], v174 src0_sel:WORD_1
	v_mov_b32_e32 v200, v70
	v_mov_b32_e32 v201, v82
	v_lshlrev_b32_e32 v183, 16, v55
	v_lshlrev_b32_e32 v182, 16, v54
	v_and_b32_e32 v191, 0xffff0000, v55
	v_and_b32_e32 v190, 0xffff0000, v54
	v_mov_b32_e32 v54, v78
	v_mov_b32_e32 v55, v76
	v_pk_mul_f32 v[200:201], v[200:201], v[68:69] op_sel:[0,1] op_sel_hi:[1,0]
	v_mov_b32_e32 v202, v84
	v_mov_b32_e32 v203, v174
	v_mov_b32_e32 v82, v71
	v_pk_fma_f32 v[54:55], v[54:55], v[68:69], v[200:201]
	v_mov_b32_e32 v200, v88
	v_mov_b32_e32 v201, v86
	v_pk_mul_f32 v[202:203], v[202:203], v[66:67] op_sel:[0,1] op_sel_hi:[1,0]
	v_mov_b32_e32 v76, v79
	v_pk_mul_f32 v[70:71], v[82:83], v[68:69] op_sel:[0,1] op_sel_hi:[1,0]
	v_mov_b32_e32 v174, v85
	v_pk_fma_f32 v[200:201], v[200:201], v[66:67], v[202:203]
	v_pk_fma_f32 v[70:71], v[76:77], v[68:69], v[70:71]
	v_mov_b32_e32 v86, v89
	v_pk_mul_f32 v[76:77], v[174:175], v[66:67] op_sel:[0,1] op_sel_hi:[1,0]
	v_pk_add_f32 v[54:55], v[54:55], v[200:201]
	v_pk_fma_f32 v[76:77], v[86:87], v[66:67], v[76:77]
	v_pk_add_f32 v[54:55], v[54:55], v[182:183]
	v_pk_add_f32 v[70:71], v[70:71], v[76:77]
	v_and_b32_sdwa v77, v54, v129 dst_sel:DWORD dst_unused:UNUSED_PAD src0_sel:WORD_1 src1_sel:DWORD
	v_pk_add_f32 v[70:71], v[70:71], v[190:191]
	v_add3_u32 v78, v54, v77, s4
	v_and_b32_sdwa v77, v71, v129 dst_sel:DWORD dst_unused:UNUSED_PAD src0_sel:WORD_1 src1_sel:DWORD
	v_and_b32_sdwa v79, v70, v129 dst_sel:DWORD dst_unused:UNUSED_PAD src0_sel:WORD_1 src1_sel:DWORD
	v_and_b32_sdwa v76, v55, v129 dst_sel:DWORD dst_unused:UNUSED_PAD src0_sel:WORD_1 src1_sel:DWORD
	v_add3_u32 v77, v71, v77, s4
	v_add3_u32 v79, v70, v79, s4
	v_add3_u32 v76, v55, v76, s4
	v_and_b32_e32 v77, 0xffff0000, v77
	v_and_b32_e32 v79, 0xffff0000, v79
	v_or_b32_sdwa v77, v77, v76 dst_sel:DWORD dst_unused:UNUSED_PAD src0_sel:DWORD src1_sel:WORD_1
	v_or_b32_sdwa v76, v79, v78 dst_sel:DWORD dst_unused:UNUSED_PAD src0_sel:DWORD src1_sel:WORD_1
	global_store_dwordx2 v[72:73], v[76:77], off offset:1024
	v_pk_mul_f32 v[76:77], v[70:71], v[70:71]
	s_nop 0
	v_pk_fma_f32 v[84:85], v[54:55], v[54:55], v[76:77]
	v_cvt_pk_f32_fp8_e32 v[76:77], v170
	v_cvt_pk_f32_fp8_sdwa v[86:87], v168 src0_sel:WORD_1
	v_cvt_pk_f32_fp8_sdwa v[78:79], v170 src0_sel:WORD_1
	v_cvt_pk_f32_fp8_e32 v[82:83], v168
	v_cvt_pk_f32_fp8_e32 v[88:89], v167
	v_cvt_pk_f32_fp8_sdwa v[174:175], v167 src0_sel:WORD_1
	v_cvt_pk_f32_fp8_e32 v[182:183], v166
	v_cvt_pk_f32_fp8_sdwa v[166:167], v166 src0_sel:WORD_1
	v_mov_b32_e32 v202, v76
	v_mov_b32_e32 v203, v86
	v_lshlrev_b32_e32 v191, 16, v49
	v_lshlrev_b32_e32 v190, 16, v48
	v_and_b32_e32 v201, 0xffff0000, v49
	v_and_b32_e32 v200, 0xffff0000, v48
	v_mov_b32_e32 v48, v82
	v_mov_b32_e32 v49, v78
	v_pk_mul_f32 v[202:203], v[202:203], v[68:69] op_sel:[0,1] op_sel_hi:[1,0]
	v_mov_b32_e32 v204, v88
	v_mov_b32_e32 v205, v166
	v_mov_b32_e32 v86, v77
	v_pk_fma_f32 v[48:49], v[48:49], v[68:69], v[202:203]
	v_mov_b32_e32 v202, v182
	v_mov_b32_e32 v203, v174
	v_pk_mul_f32 v[204:205], v[204:205], v[66:67] op_sel:[0,1] op_sel_hi:[1,0]
	v_mov_b32_e32 v78, v83
	v_pk_mul_f32 v[76:77], v[86:87], v[68:69] op_sel:[0,1] op_sel_hi:[1,0]
	v_mov_b32_e32 v166, v89
	v_pk_fma_f32 v[202:203], v[202:203], v[66:67], v[204:205]
	v_pk_fma_f32 v[76:77], v[78:79], v[68:69], v[76:77]
	v_mov_b32_e32 v174, v183
	v_pk_mul_f32 v[78:79], v[166:167], v[66:67] op_sel:[0,1] op_sel_hi:[1,0]
	v_pk_add_f32 v[48:49], v[48:49], v[202:203]
	v_pk_fma_f32 v[78:79], v[174:175], v[66:67], v[78:79]
	v_pk_add_f32 v[48:49], v[48:49], v[190:191]
	v_pk_add_f32 v[76:77], v[76:77], v[78:79]
	v_and_b32_sdwa v79, v48, v129 dst_sel:DWORD dst_unused:UNUSED_PAD src0_sel:WORD_1 src1_sel:DWORD
	v_pk_add_f32 v[76:77], v[76:77], v[200:201]
	v_add3_u32 v82, v48, v79, s4
	v_and_b32_sdwa v79, v77, v129 dst_sel:DWORD dst_unused:UNUSED_PAD src0_sel:WORD_1 src1_sel:DWORD
	v_and_b32_sdwa v83, v76, v129 dst_sel:DWORD dst_unused:UNUSED_PAD src0_sel:WORD_1 src1_sel:DWORD
	v_and_b32_sdwa v78, v49, v129 dst_sel:DWORD dst_unused:UNUSED_PAD src0_sel:WORD_1 src1_sel:DWORD
	v_add3_u32 v79, v77, v79, s4
	v_add3_u32 v83, v76, v83, s4
	v_add3_u32 v78, v49, v78, s4
	v_and_b32_e32 v79, 0xffff0000, v79
	v_and_b32_e32 v83, 0xffff0000, v83
	v_or_b32_sdwa v79, v79, v78 dst_sel:DWORD dst_unused:UNUSED_PAD src0_sel:DWORD src1_sel:WORD_1
	v_or_b32_sdwa v78, v83, v82 dst_sel:DWORD dst_unused:UNUSED_PAD src0_sel:DWORD src1_sel:WORD_1
	global_store_dwordx2 v[72:73], v[78:79], off offset:1536
	v_pk_mul_f32 v[78:79], v[76:77], v[76:77]
	s_nop 0
	v_pk_fma_f32 v[88:89], v[48:49], v[48:49], v[78:79]
	v_cvt_pk_f32_fp8_e32 v[78:79], v161
	v_cvt_pk_f32_fp8_sdwa v[82:83], v161 src0_sel:WORD_1
	v_cvt_pk_f32_fp8_e32 v[86:87], v160
	v_cvt_pk_f32_fp8_sdwa v[160:161], v160 src0_sel:WORD_1
	v_cvt_pk_f32_fp8_e32 v[166:167], v159
	v_cvt_pk_f32_fp8_sdwa v[174:175], v159 src0_sel:WORD_1
	v_cvt_pk_f32_fp8_e32 v[182:183], v158
	v_cvt_pk_f32_fp8_sdwa v[158:159], v158 src0_sel:WORD_1
	v_mov_b32_e32 v202, v78
	v_mov_b32_e32 v203, v160
	v_lshlrev_b32_e32 v191, 16, v45
	v_lshlrev_b32_e32 v190, 16, v44
	v_and_b32_e32 v201, 0xffff0000, v45
	v_and_b32_e32 v200, 0xffff0000, v44
	v_mov_b32_e32 v44, v86
	v_mov_b32_e32 v45, v82
	v_pk_mul_f32 v[202:203], v[202:203], v[68:69] op_sel:[0,1] op_sel_hi:[1,0]
	v_mov_b32_e32 v204, v166
	v_mov_b32_e32 v205, v158
	v_mov_b32_e32 v160, v79
	v_pk_fma_f32 v[44:45], v[44:45], v[68:69], v[202:203]
	v_mov_b32_e32 v202, v182
	v_mov_b32_e32 v203, v174
	v_pk_mul_f32 v[204:205], v[204:205], v[66:67] op_sel:[0,1] op_sel_hi:[1,0]
	v_mov_b32_e32 v82, v87
	v_pk_mul_f32 v[78:79], v[160:161], v[68:69] op_sel:[0,1] op_sel_hi:[1,0]
	v_mov_b32_e32 v158, v167
	v_pk_fma_f32 v[202:203], v[202:203], v[66:67], v[204:205]
	v_pk_fma_f32 v[78:79], v[82:83], v[68:69], v[78:79]
	v_mov_b32_e32 v174, v183
	v_pk_mul_f32 v[82:83], v[158:159], v[66:67] op_sel:[0,1] op_sel_hi:[1,0]
	v_pk_add_f32 v[44:45], v[44:45], v[202:203]
	v_pk_fma_f32 v[82:83], v[174:175], v[66:67], v[82:83]
	v_pk_add_f32 v[44:45], v[44:45], v[190:191]
	v_pk_add_f32 v[78:79], v[78:79], v[82:83]
	v_and_b32_sdwa v83, v44, v129 dst_sel:DWORD dst_unused:UNUSED_PAD src0_sel:WORD_1 src1_sel:DWORD
	v_pk_add_f32 v[78:79], v[78:79], v[200:201]
	v_add3_u32 v86, v44, v83, s4
	v_and_b32_sdwa v83, v79, v129 dst_sel:DWORD dst_unused:UNUSED_PAD src0_sel:WORD_1 src1_sel:DWORD
	v_and_b32_sdwa v87, v78, v129 dst_sel:DWORD dst_unused:UNUSED_PAD src0_sel:WORD_1 src1_sel:DWORD
	v_and_b32_sdwa v82, v45, v129 dst_sel:DWORD dst_unused:UNUSED_PAD src0_sel:WORD_1 src1_sel:DWORD
	v_add3_u32 v83, v79, v83, s4
	v_add3_u32 v87, v78, v87, s4
	v_add3_u32 v82, v45, v82, s4
	v_and_b32_e32 v83, 0xffff0000, v83
	v_and_b32_e32 v87, 0xffff0000, v87
	v_or_b32_sdwa v83, v83, v82 dst_sel:DWORD dst_unused:UNUSED_PAD src0_sel:DWORD src1_sel:WORD_1
	v_or_b32_sdwa v82, v87, v86 dst_sel:DWORD dst_unused:UNUSED_PAD src0_sel:DWORD src1_sel:WORD_1
	global_store_dwordx2 v[72:73], v[82:83], off offset:2048
	v_pk_mul_f32 v[82:83], v[78:79], v[78:79]
	s_nop 0
	v_pk_fma_f32 v[158:159], v[44:45], v[44:45], v[82:83]
	v_cvt_pk_f32_fp8_e32 v[82:83], v152
	v_cvt_pk_f32_fp8_sdwa v[160:161], v151 src0_sel:WORD_1
	v_cvt_pk_f32_fp8_sdwa v[86:87], v152 src0_sel:WORD_1
	v_cvt_pk_f32_fp8_e32 v[152:153], v151
	v_cvt_pk_f32_fp8_e32 v[166:167], v150
	v_cvt_pk_f32_fp8_sdwa v[182:183], v149 src0_sel:WORD_1
	v_cvt_pk_f32_fp8_sdwa v[150:151], v150 src0_sel:WORD_1
	v_cvt_pk_f32_fp8_e32 v[174:175], v149
	v_mov_b32_e32 v202, v82
	v_mov_b32_e32 v203, v160
	v_lshlrev_b32_e32 v191, 16, v41
	v_lshlrev_b32_e32 v190, 16, v40
	v_and_b32_e32 v201, 0xffff0000, v41
	v_and_b32_e32 v200, 0xffff0000, v40
	v_mov_b32_e32 v40, v152
	v_mov_b32_e32 v41, v86
	v_pk_mul_f32 v[202:203], v[202:203], v[68:69] op_sel:[0,1] op_sel_hi:[1,0]
	v_mov_b32_e32 v204, v166
	v_mov_b32_e32 v205, v182
	v_mov_b32_e32 v160, v83
	v_pk_fma_f32 v[40:41], v[40:41], v[68:69], v[202:203]
	v_mov_b32_e32 v202, v174
	v_mov_b32_e32 v203, v150
	v_pk_mul_f32 v[204:205], v[204:205], v[66:67] op_sel:[0,1] op_sel_hi:[1,0]
	v_mov_b32_e32 v86, v153
	v_pk_mul_f32 v[82:83], v[160:161], v[68:69] op_sel:[0,1] op_sel_hi:[1,0]
	v_mov_b32_e32 v182, v167
	v_pk_fma_f32 v[202:203], v[202:203], v[66:67], v[204:205]
	v_pk_fma_f32 v[82:83], v[86:87], v[68:69], v[82:83]
	v_mov_b32_e32 v150, v175
	v_pk_mul_f32 v[86:87], v[182:183], v[66:67] op_sel:[0,1] op_sel_hi:[1,0]
	v_pk_add_f32 v[40:41], v[40:41], v[202:203]
	v_pk_fma_f32 v[86:87], v[150:151], v[66:67], v[86:87]
	v_pk_add_f32 v[40:41], v[40:41], v[190:191]
	v_pk_add_f32 v[82:83], v[82:83], v[86:87]
	v_and_b32_sdwa v87, v40, v129 dst_sel:DWORD dst_unused:UNUSED_PAD src0_sel:WORD_1 src1_sel:DWORD
	v_pk_add_f32 v[82:83], v[82:83], v[200:201]
	v_add3_u32 v140, v40, v87, s4
	v_and_b32_sdwa v87, v83, v129 dst_sel:DWORD dst_unused:UNUSED_PAD src0_sel:WORD_1 src1_sel:DWORD
	v_and_b32_sdwa v143, v82, v129 dst_sel:DWORD dst_unused:UNUSED_PAD src0_sel:WORD_1 src1_sel:DWORD
	v_and_b32_sdwa v86, v41, v129 dst_sel:DWORD dst_unused:UNUSED_PAD src0_sel:WORD_1 src1_sel:DWORD
	v_add3_u32 v87, v83, v87, s4
	v_add3_u32 v143, v82, v143, s4
	v_add3_u32 v86, v41, v86, s4
	v_and_b32_e32 v87, 0xffff0000, v87
	v_and_b32_e32 v143, 0xffff0000, v143
	v_or_b32_sdwa v87, v87, v86 dst_sel:DWORD dst_unused:UNUSED_PAD src0_sel:DWORD src1_sel:WORD_1
	v_or_b32_sdwa v86, v143, v140 dst_sel:DWORD dst_unused:UNUSED_PAD src0_sel:DWORD src1_sel:WORD_1
	global_store_dwordx2 v[72:73], v[86:87], off offset:2560
	v_pk_mul_f32 v[86:87], v[82:83], v[82:83]
	s_nop 0
	v_pk_fma_f32 v[150:151], v[40:41], v[40:41], v[86:87]
	v_cvt_pk_f32_fp8_e32 v[86:87], v144
	v_cvt_pk_f32_fp8_e32 v[160:161], v142
	v_cvt_pk_f32_fp8_sdwa v[142:143], v142 src0_sel:WORD_1
	v_cvt_pk_f32_fp8_sdwa v[152:153], v144 src0_sel:WORD_1
	v_cvt_pk_f32_fp8_e32 v[166:167], v141
	v_cvt_pk_f32_fp8_sdwa v[182:183], v139 src0_sel:WORD_1
	v_cvt_pk_f32_fp8_sdwa v[140:141], v141 src0_sel:WORD_1
	v_cvt_pk_f32_fp8_e32 v[174:175], v139
	v_mov_b32_e32 v202, v86
	v_mov_b32_e32 v203, v142
	v_lshlrev_b32_e32 v191, 16, v35
	v_lshlrev_b32_e32 v190, 16, v34
	v_and_b32_e32 v201, 0xffff0000, v35
	v_and_b32_e32 v200, 0xffff0000, v34
	v_mov_b32_e32 v34, v160
	v_mov_b32_e32 v35, v152
	v_pk_mul_f32 v[202:203], v[202:203], v[68:69] op_sel:[0,1] op_sel_hi:[1,0]
	v_mov_b32_e32 v205, v182
	v_mov_b32_e32 v142, v87
	v_mov_b32_e32 v182, v167
	v_pk_fma_f32 v[34:35], v[34:35], v[68:69], v[202:203]
	v_mov_b32_e32 v203, v140
	v_mov_b32_e32 v204, v166
	v_mov_b32_e32 v152, v161
	v_pk_mul_f32 v[86:87], v[142:143], v[68:69] op_sel:[0,1] op_sel_hi:[1,0]
	v_mov_b32_e32 v140, v175
	v_pk_mul_f32 v[142:143], v[182:183], v[66:67] op_sel:[0,1] op_sel_hi:[1,0]
	v_mov_b32_e32 v202, v174
	v_pk_mul_f32 v[204:205], v[204:205], v[66:67] op_sel:[0,1] op_sel_hi:[1,0]
	v_pk_fma_f32 v[86:87], v[152:153], v[68:69], v[86:87]
	v_pk_fma_f32 v[140:141], v[140:141], v[66:67], v[142:143]
	v_pk_fma_f32 v[202:203], v[202:203], v[66:67], v[204:205]
	v_pk_add_f32 v[86:87], v[86:87], v[140:141]
	v_pk_add_f32 v[34:35], v[34:35], v[202:203]
	v_pk_add_f32 v[86:87], v[86:87], v[200:201]
	v_pk_add_f32 v[34:35], v[34:35], v[190:191]
	v_and_b32_sdwa v141, v87, v129 dst_sel:DWORD dst_unused:UNUSED_PAD src0_sel:WORD_1 src1_sel:DWORD
	v_and_b32_sdwa v142, v86, v129 dst_sel:DWORD dst_unused:UNUSED_PAD src0_sel:WORD_1 src1_sel:DWORD
	v_and_b32_sdwa v139, v35, v129 dst_sel:DWORD dst_unused:UNUSED_PAD src0_sel:WORD_1 src1_sel:DWORD
	v_and_b32_sdwa v140, v34, v129 dst_sel:DWORD dst_unused:UNUSED_PAD src0_sel:WORD_1 src1_sel:DWORD
	v_add3_u32 v141, v87, v141, s4
	v_add3_u32 v142, v86, v142, s4
	v_add3_u32 v140, v34, v140, s4
	v_add3_u32 v139, v35, v139, s4
	v_and_b32_e32 v141, 0xffff0000, v141
	v_and_b32_e32 v142, 0xffff0000, v142
	v_or_b32_sdwa v141, v141, v139 dst_sel:DWORD dst_unused:UNUSED_PAD src0_sel:DWORD src1_sel:WORD_1
	v_or_b32_sdwa v140, v142, v140 dst_sel:DWORD dst_unused:UNUSED_PAD src0_sel:DWORD src1_sel:WORD_1
	global_store_dwordx2 v[72:73], v[140:141], off offset:3072
	v_pk_mul_f32 v[140:141], v[86:87], v[86:87]
	s_nop 0
	v_pk_fma_f32 v[140:141], v[34:35], v[34:35], v[140:141]
	v_cvt_pk_f32_fp8_e32 v[142:143], v136
	v_cvt_pk_f32_fp8_sdwa v[166:167], v134 src0_sel:WORD_1
	v_cvt_pk_f32_fp8_sdwa v[152:153], v136 src0_sel:WORD_1
	v_cvt_pk_f32_fp8_e32 v[160:161], v134
	v_cvt_pk_f32_fp8_e32 v[174:175], v133
	v_cvt_pk_f32_fp8_sdwa v[200:201], v131 src0_sel:WORD_1
	v_cvt_pk_f32_fp8_sdwa v[182:183], v133 src0_sel:WORD_1
	v_cvt_pk_f32_fp8_e32 v[190:191], v131
	v_mov_b32_e32 v206, v142
	v_mov_b32_e32 v207, v166
	v_lshlrev_b32_e32 v203, 16, v29
	v_lshlrev_b32_e32 v202, 16, v28
	v_and_b32_e32 v205, 0xffff0000, v29
	v_and_b32_e32 v204, 0xffff0000, v28
	v_mov_b32_e32 v28, v160
	v_mov_b32_e32 v29, v152
	v_pk_mul_f32 v[206:207], v[206:207], v[68:69] op_sel:[0,1] op_sel_hi:[1,0]
	v_mov_b32_e32 v208, v174
	v_mov_b32_e32 v209, v200
	v_mov_b32_e32 v166, v143
	v_pk_fma_f32 v[28:29], v[28:29], v[68:69], v[206:207]
	v_mov_b32_e32 v206, v190
	v_mov_b32_e32 v207, v182
	v_pk_mul_f32 v[208:209], v[208:209], v[66:67] op_sel:[0,1] op_sel_hi:[1,0]
	v_mov_b32_e32 v152, v161
	v_pk_mul_f32 v[142:143], v[166:167], v[68:69] op_sel:[0,1] op_sel_hi:[1,0]
	v_mov_b32_e32 v200, v175
	v_pk_fma_f32 v[206:207], v[206:207], v[66:67], v[208:209]
	v_pk_fma_f32 v[68:69], v[152:153], v[68:69], v[142:143]
	v_mov_b32_e32 v182, v191
	v_pk_mul_f32 v[142:143], v[200:201], v[66:67] op_sel:[0,1] op_sel_hi:[1,0]
	v_pk_add_f32 v[28:29], v[28:29], v[206:207]
	v_pk_fma_f32 v[66:67], v[182:183], v[66:67], v[142:143]
	v_pk_add_f32 v[28:29], v[28:29], v[202:203]
	v_pk_add_f32 v[66:67], v[68:69], v[66:67]
	v_and_b32_sdwa v69, v28, v129 dst_sel:DWORD dst_unused:UNUSED_PAD src0_sel:WORD_1 src1_sel:DWORD
	v_pk_add_f32 v[66:67], v[66:67], v[204:205]
	v_add3_u32 v131, v28, v69, s4
	v_and_b32_sdwa v69, v67, v129 dst_sel:DWORD dst_unused:UNUSED_PAD src0_sel:WORD_1 src1_sel:DWORD
	v_and_b32_sdwa v133, v66, v129 dst_sel:DWORD dst_unused:UNUSED_PAD src0_sel:WORD_1 src1_sel:DWORD
	v_and_b32_sdwa v68, v29, v129 dst_sel:DWORD dst_unused:UNUSED_PAD src0_sel:WORD_1 src1_sel:DWORD
	v_add3_u32 v69, v67, v69, s4
	v_add3_u32 v133, v66, v133, s4
	v_add3_u32 v68, v29, v68, s4
	v_and_b32_e32 v69, 0xffff0000, v69
	v_and_b32_e32 v133, 0xffff0000, v133
	v_or_b32_sdwa v69, v69, v68 dst_sel:DWORD dst_unused:UNUSED_PAD src0_sel:DWORD src1_sel:WORD_1
	v_or_b32_sdwa v68, v133, v131 dst_sel:DWORD dst_unused:UNUSED_PAD src0_sel:DWORD src1_sel:WORD_1
	global_store_dwordx2 v[72:73], v[68:69], off offset:3584
	v_add_f32_e32 v72, v80, v81
	v_add_f32_e32 v73, v74, v75
	v_add_f32_e32 v72, v73, v72
	v_add_f32_e32 v73, v84, v85
	v_add_f32_e32 v72, v72, v73
	v_add_f32_e32 v73, v88, v89
	v_add_f32_e32 v72, v72, v73
	v_add_f32_e32 v73, v158, v159
	v_pk_mul_f32 v[68:69], v[66:67], v[66:67]
	v_add_f32_e32 v72, v72, v73
	v_add_f32_e32 v73, v150, v151
	v_pk_fma_f32 v[68:69], v[28:29], v[28:29], v[68:69]
	v_add_f32_e32 v72, v72, v73
	v_add_f32_e32 v73, v140, v141
	v_add_f32_e32 v72, v72, v73
	v_add_f32_e32 v68, v68, v69
	v_add_f32_e32 v68, v72, v68
	v_mov_b64_e32 v[72:73], v[212:213]
	v_mov_b64_e32 v[74:75], v[214:215]
	ds_bpermute_b32 v69, v1, v68
	s_waitcnt lgkmcnt(0)
	v_add_f32_e32 v68, v68, v69
	ds_bpermute_b32 v69, v90, v68
	s_waitcnt lgkmcnt(0)
	v_add_f32_e32 v68, v68, v69
	ds_bpermute_b32 v69, v91, v68
	s_waitcnt lgkmcnt(0)
	v_add_f32_e32 v68, v68, v69
	ds_bpermute_b32 v69, v92, v68
	s_waitcnt lgkmcnt(0)
	v_add_f32_e32 v68, v68, v69
	ds_bpermute_b32 v69, v93, v68
	s_waitcnt lgkmcnt(0)
	v_add_f32_e32 v68, v68, v69
	ds_bpermute_b32 v69, v94, v68
	s_waitcnt lgkmcnt(0)
	v_add_f32_e32 v68, v68, v69
	v_fmamk_f32 v68, v68, 0x3a000000, v127
	v_mul_f32_e32 v69, 0x4f800000, v68
	v_cmp_gt_f32_e32 vcc, s19, v68
	s_nop 1
	v_cndmask_b32_e32 v68, v68, v69, vcc
	v_sqrt_f32_e32 v69, v68
	s_nop 0
	v_add_u32_e32 v80, -1, v69
	v_add_u32_e32 v81, 1, v69
	v_fma_f32 v84, -v80, v69, v68
	v_fma_f32 v85, -v81, v69, v68
	v_cmp_ge_f32_e64 s[8:9], 0, v84
	s_nop 1
	v_cndmask_b32_e64 v69, v69, v80, s[8:9]
	v_cmp_lt_f32_e64 s[8:9], 0, v85
	s_nop 1
	v_cndmask_b32_e64 v69, v69, v81, s[8:9]
	v_mul_f32_e32 v80, 0x37800000, v69
	v_cndmask_b32_e32 v69, v69, v80, vcc
	v_cmp_class_f32_e32 vcc, v68, v128
	v_mov_b32_e32 v81, 0
	s_nop 0
	v_cndmask_b32_e32 v68, v69, v68, vcc
	v_div_scale_f32 v69, s[0:1], v68, v68, 1.0
	v_rcp_f32_e32 v80, v69
	v_div_scale_f32 v84, vcc, 1.0, v68, 1.0
	v_fma_f32 v85, -v69, v80, 1.0
	v_fmac_f32_e32 v80, v85, v80
	v_mul_f32_e32 v85, v84, v80
	v_fma_f32 v88, -v69, v85, v84
	v_fmac_f32_e32 v85, v88, v80
	v_fma_f32 v69, -v69, v85, v84
	v_div_fmas_f32 v69, v69, v80, v85
	v_div_fixup_f32 v68, v69, v68, 1.0
	v_mul_f32_e32 v38, v68, v38
	v_mul_f32_e32 v52, v68, v52

	v_mul_f32_e32 v38, v72, v38
	v_mul_f32_e32 v52, v73, v52
	v_cvt_pk_fp8_f32 v81, v38, v52
	v_mul_f32_e32 v39, v68, v39
	v_mul_f32_e32 v38, v68, v53
	v_mul_f32_e32 v39, v74, v39
	v_mul_f32_e32 v38, v75, v38
	v_cvt_pk_fp8_f32 v81, v39, v38 op_sel:[0,0,1]
	v_mul_f32_e32 v39, v68, v58
	v_mul_f32_e32 v52, v68, v62
	v_mov_b32_e32 v38, 0
	global_store_dword v[24:25], v81, off
	v_mov_b64_e32 v[72:73], v[216:217]
	v_mov_b64_e32 v[74:75], v[218:219]
	v_mul_f32_e32 v53, v68, v59
	v_mul_f32_e32 v49, v68, v49
	v_mul_f32_e32 v45, v68, v45
	v_mul_f32_e32 v41, v68, v41
	v_mul_f32_e32 v34, v68, v34
	v_mul_f32_e32 v35, v68, v35
	v_mul_f32_e32 v28, v68, v28
	v_mul_f32_e32 v29, v68, v29
	ds_bpermute_b32 v69, v108, v19
	s_waitcnt vmcnt(17)
	v_cvt_pk_f32_fp8_sdwa v[80:81], v197 src0_sel:WORD_1

	v_mul_f32_e32 v39, v72, v39
	v_mul_f32_e32 v52, v73, v52
	v_cvt_pk_fp8_f32 v38, v39, v52
	v_mul_f32_e32 v39, v68, v63
	v_mul_f32_e32 v52, v74, v53
	v_mul_f32_e32 v39, v75, v39
	v_cvt_pk_fp8_f32 v38, v52, v39 op_sel:[0,0,1]
	v_mul_f32_e32 v39, v68, v54
	v_mul_f32_e32 v52, v68, v70
	v_mul_f32_e32 v53, v68, v55
	global_store_dword v[24:25], v38, off offset:256
	v_mov_b64_e32 v[72:73], v[220:221]
	v_mov_b64_e32 v[74:75], v[222:223]
	v_mov_b32_e32 v38, 0

	v_mul_f32_e32 v39, v72, v39
	v_mul_f32_e32 v52, v73, v52
	v_cvt_pk_fp8_f32 v38, v39, v52
	v_mul_f32_e32 v39, v68, v71
	v_mul_f32_e32 v52, v74, v53
	v_mul_f32_e32 v39, v75, v39
	v_cvt_pk_fp8_f32 v38, v52, v39 op_sel:[0,0,1]
	v_mul_f32_e32 v39, v68, v48
	v_mul_f32_e32 v48, v68, v76
	v_cvt_pk_f32_fp8_sdwa v[72:73], v194 src0_sel:WORD_1
	global_store_dword v[24:25], v38, off offset:512
	v_mov_b64_e32 v[52:53], v[224:225]
	v_mov_b64_e32 v[54:55], v[226:227]
	v_mov_b32_e32 v38, 0
	v_cvt_pk_f32_fp8_e32 v[70:71], v194
	v_cvt_pk_f32_fp8_e32 v[74:75], v195
	v_mov_b32_e32 v85, v72

	v_mul_f32_e32 v39, v52, v39
	v_mul_f32_e32 v48, v53, v48
	v_cvt_pk_fp8_f32 v38, v39, v48
	v_mul_f32_e32 v39, v68, v77
	v_mul_f32_e32 v48, v54, v49
	v_mul_f32_e32 v39, v55, v39
	v_cvt_pk_fp8_f32 v38, v48, v39 op_sel:[0,0,1]
	v_mul_f32_e32 v39, v68, v44
	v_mul_f32_e32 v44, v68, v78
	ds_bpermute_b32 v48, v113, v130
	global_store_dword v[24:25], v38, off offset:768
	v_mov_b64_e32 v[52:53], v[228:229]
	v_mov_b64_e32 v[54:55], v[230:231]
	v_mov_b32_e32 v38, 0
	v_cvt_pk_f32_fp8_sdwa v[76:77], v195 src0_sel:WORD_1
	s_waitcnt lgkmcnt(0)
	v_ashrrev_i32_e32 v49, 31, v48
	v_lshlrev_b64 v[48:49], 11, v[48:49]

	v_mul_f32_e32 v39, v52, v39
	v_mul_f32_e32 v44, v53, v44
	v_cvt_pk_fp8_f32 v38, v39, v44
	v_mul_f32_e32 v39, v68, v79
	v_mul_f32_e32 v44, v54, v45
	v_mul_f32_e32 v39, v55, v39
	v_cvt_pk_fp8_f32 v38, v44, v39 op_sel:[0,0,1]
	v_mul_f32_e32 v39, v68, v40
	v_mul_f32_e32 v40, v68, v82
	v_mul_f32_e32 v45, v68, v86
	global_store_dword v[24:25], v38, off offset:1024
	v_mov_b64_e32 v[52:53], v[232:233]
	v_mov_b64_e32 v[54:55], v[234:235]
	v_mov_b32_e32 v38, 0
	v_mov_b32_e32 v44, 0
	v_cvt_pk_f32_fp8_e32 v[78:79], v197
	v_mov_b32_e32 v82, v70
	v_mov_b32_e32 v86, v74

	v_mul_f32_e32 v39, v52, v39
	v_mul_f32_e32 v40, v53, v40
	v_cvt_pk_fp8_f32 v38, v39, v40
	v_mul_f32_e32 v39, v68, v83
	v_mul_f32_e32 v40, v54, v41
	v_mul_f32_e32 v39, v55, v39
	v_cvt_pk_fp8_f32 v38, v40, v39 op_sel:[0,0,1]
	v_mul_f32_e32 v55, v68, v66
	v_mov_b32_e32 v54, 0
	ds_bpermute_b32 v52, v112, v130
	global_store_dword v[24:25], v38, off offset:1280
	v_mov_b64_e32 v[38:39], v[236:237]
	v_mov_b64_e32 v[40:41], v[238:239]
	ds_bpermute_b32 v66, v111, v19
	s_waitcnt lgkmcnt(1)
	v_ashrrev_i32_e32 v53, 31, v52
	v_lshlrev_b64 v[52:53], 11, v[52:53]

	v_mul_f32_e32 v34, v38, v34
	v_mul_f32_e32 v38, v39, v45
	v_cvt_pk_fp8_f32 v44, v34, v38
	v_mul_f32_e32 v34, v68, v87
	v_mul_f32_e32 v35, v40, v35
	v_mul_f32_e32 v34, v41, v34
	v_cvt_pk_fp8_f32 v44, v35, v34 op_sel:[0,0,1]
	ds_bpermute_b32 v34, v115, v130
	v_mov_b32_e32 v87, v80
	v_mov_b32_e32 v80, v75
	global_store_dword v[24:25], v44, off offset:1536
	v_mov_b64_e32 v[38:39], v[240:241]
	v_mov_b64_e32 v[40:41], v[242:243]
	ds_bpermute_b32 v44, v114, v130
	s_waitcnt lgkmcnt(1)
	v_ashrrev_i32_e32 v35, 31, v34
	v_lshlrev_b64 v[34:35], 11, v[34:35]
	v_lshl_add_u64 v[34:35], v[4:5], 0, v[34:35]
	s_waitcnt lgkmcnt(0)
	v_ashrrev_i32_e32 v45, 31, v44
	v_lshlrev_b64 v[44:45], 11, v[44:45]

	v_mul_f32_e32 v28, v38, v28
	v_mul_f32_e32 v38, v39, v55
	v_cvt_pk_fp8_f32 v54, v28, v38
	v_mul_f32_e32 v28, v68, v67
	v_mul_f32_e32 v29, v40, v29
	v_mul_f32_e32 v28, v41, v28
	v_cvt_pk_fp8_f32 v54, v29, v28 op_sel:[0,0,1]
	v_lshl_add_u64 v[28:29], v[4:5], 0, v[44:45]
	v_lshl_add_u64 v[38:39], v[4:5], 0, v[48:49]
	v_lshl_add_u64 v[40:41], v[4:5], 0, v[52:53]
	global_store_dword v[24:25], v54, off offset:1792
	global_load_dword v88, v[34:35], off offset:1792 nt
	global_load_dword v139, v[34:35], off offset:1536 nt
	global_load_dword v149, v[34:35], off offset:1280 nt
	global_load_dword v158, v[34:35], off offset:1024 nt
	global_load_dword v166, v[34:35], off offset:768 nt
	global_load_dword v174, v[34:35], off offset:512 nt
	global_load_dword v182, v[34:35], off offset:256 nt
	global_load_dword v190, v[34:35], off nt
	global_load_dword v89, v[28:29], off offset:1792 nt
	global_load_dword v140, v[28:29], off offset:1536 nt
	global_load_dword v150, v[28:29], off offset:1280 nt
	global_load_dword v159, v[28:29], off offset:1024 nt
	global_load_dword v167, v[28:29], off offset:768 nt
	global_load_dword v175, v[28:29], off offset:512 nt
	global_load_dword v183, v[28:29], off offset:256 nt
	global_load_dword v191, v[28:29], off nt
	global_load_dword v131, v[38:39], off offset:1792 nt
	global_load_dword v141, v[38:39], off offset:1536 nt
	global_load_dword v151, v[38:39], off offset:1280 nt
	global_load_dword v160, v[38:39], off offset:1024 nt
	global_load_dword v168, v[38:39], off offset:768 nt
	global_load_dword v176, v[38:39], off offset:512 nt
	global_load_dword v184, v[38:39], off offset:256 nt
	global_load_dword v193, v[38:39], off nt
	global_load_dword v133, v[40:41], off offset:1792 nt
	global_load_dword v143, v[40:41], off offset:1536 nt
	global_load_dword v153, v[40:41], off offset:1280 nt
	global_load_dword v161, v[40:41], off offset:1024 nt
	global_load_dword v170, v[40:41], off offset:768 nt
	global_load_dword v178, v[40:41], off offset:512 nt
	global_load_dword v186, v[40:41], off offset:256 nt
	global_load_dword v196, v[40:41], off nt
	global_load_dwordx2 v[28:29], v[60:61], off offset:3584 nt
	global_load_dwordx2 v[34:35], v[60:61], off offset:3072 nt
	global_load_dwordx2 v[38:39], v[60:61], off offset:2560 nt
	global_load_dwordx2 v[44:45], v[60:61], off offset:2048 nt
	global_load_dwordx2 v[48:49], v[60:61], off offset:1536 nt
	global_load_dwordx2 v[52:53], v[60:61], off offset:1024 nt
	global_load_dwordx2 v[58:59], v[60:61], off offset:512 nt
	global_load_dwordx2 v[62:63], v[60:61], off nt
	ds_bpermute_b32 v68, v109, v19
	v_cvt_pk_f32_fp8_e32 v[54:55], v192
	ds_bpermute_b32 v67, v110, v19
	v_cvt_pk_f32_fp8_sdwa v[60:61], v192 src0_sel:WORD_1
	s_waitcnt vmcnt(63)
	v_lshlrev_b32_e32 v41, 16, v65
	v_mov_b32_e32 v84, v54
	s_waitcnt lgkmcnt(1)
	v_pk_mul_f32 v[84:85], v[84:85], v[68:69] op_sel:[0,1] op_sel_hi:[1,0]
	v_mov_b32_e32 v83, v60
	v_mov_b32_e32 v72, v55
	v_pk_fma_f32 v[82:83], v[82:83], v[68:69], v[84:85]
	v_mov_b32_e32 v84, v78
	v_mov_b32_e32 v85, v76
	s_waitcnt lgkmcnt(0)
	v_pk_mul_f32 v[86:87], v[86:87], v[66:67] op_sel:[0,1] op_sel_hi:[1,0]
	v_mov_b32_e32 v60, v71
	v_pk_mul_f32 v[54:55], v[72:73], v[68:69] op_sel:[0,1] op_sel_hi:[1,0]
	v_pk_fma_f32 v[84:85], v[84:85], v[66:67], v[86:87]
	v_pk_fma_f32 v[54:55], v[60:61], v[68:69], v[54:55]
	v_mov_b32_e32 v76, v79
	v_pk_mul_f32 v[60:61], v[80:81], v[66:67] op_sel:[0,1] op_sel_hi:[1,0]
	v_lshlrev_b32_e32 v40, 16, v64
	v_pk_add_f32 v[82:83], v[82:83], v[84:85]
	v_pk_fma_f32 v[60:61], v[76:77], v[66:67], v[60:61]
	v_and_b32_e32 v65, 0xffff0000, v65
	v_and_b32_e32 v64, 0xffff0000, v64
	v_pk_add_f32 v[40:41], v[82:83], v[40:41]
	v_pk_add_f32 v[54:55], v[54:55], v[60:61]
	v_and_b32_sdwa v61, v40, v129 dst_sel:DWORD dst_unused:UNUSED_PAD src0_sel:WORD_1 src1_sel:DWORD
	v_pk_add_f32 v[54:55], v[54:55], v[64:65]
	v_add3_u32 v64, v40, v61, s4
	v_and_b32_sdwa v61, v55, v129 dst_sel:DWORD dst_unused:UNUSED_PAD src0_sel:WORD_1 src1_sel:DWORD
	v_and_b32_sdwa v65, v54, v129 dst_sel:DWORD dst_unused:UNUSED_PAD src0_sel:WORD_1 src1_sel:DWORD
	v_and_b32_sdwa v60, v41, v129 dst_sel:DWORD dst_unused:UNUSED_PAD src0_sel:WORD_1 src1_sel:DWORD
	v_add3_u32 v61, v55, v61, s4
	v_add3_u32 v65, v54, v65, s4
	v_add3_u32 v60, v41, v60, s4
	v_and_b32_e32 v61, 0xffff0000, v61
	v_and_b32_e32 v65, 0xffff0000, v65
	v_or_b32_sdwa v61, v61, v60 dst_sel:DWORD dst_unused:UNUSED_PAD src0_sel:DWORD src1_sel:WORD_1
	v_or_b32_sdwa v60, v65, v64 dst_sel:DWORD dst_unused:UNUSED_PAD src0_sel:DWORD src1_sel:WORD_1
	global_store_dwordx2 v[30:31], v[60:61], off
	v_pk_mul_f32 v[60:61], v[54:55], v[54:55]
	s_nop 0
	v_pk_fma_f32 v[70:71], v[40:41], v[40:41], v[60:61]
	v_cvt_pk_f32_fp8_e32 v[60:61], v185
	v_cvt_pk_f32_fp8_sdwa v[74:75], v187 src0_sel:WORD_1
	v_cvt_pk_f32_fp8_sdwa v[64:65], v185 src0_sel:WORD_1
	v_cvt_pk_f32_fp8_e32 v[72:73], v187
	v_cvt_pk_f32_fp8_e32 v[76:77], v188
	s_waitcnt vmcnt(63)
	v_cvt_pk_f32_fp8_sdwa v[82:83], v189 src0_sel:WORD_1
	v_cvt_pk_f32_fp8_sdwa v[78:79], v188 src0_sel:WORD_1
	v_cvt_pk_f32_fp8_e32 v[80:81], v189
	v_mov_b32_e32 v188, v60
	v_mov_b32_e32 v189, v74
	v_lshlrev_b32_e32 v85, 16, v57
	v_lshlrev_b32_e32 v84, 16, v56
	v_and_b32_e32 v87, 0xffff0000, v57
	v_and_b32_e32 v86, 0xffff0000, v56
	v_mov_b32_e32 v56, v72
	v_mov_b32_e32 v57, v64
	v_pk_mul_f32 v[188:189], v[188:189], v[68:69] op_sel:[0,1] op_sel_hi:[1,0]
	v_mov_b32_e32 v194, v76
	v_mov_b32_e32 v195, v82
	v_mov_b32_e32 v74, v61
	v_pk_fma_f32 v[56:57], v[56:57], v[68:69], v[188:189]
	v_mov_b32_e32 v188, v80
	v_mov_b32_e32 v189, v78
	v_pk_mul_f32 v[194:195], v[194:195], v[66:67] op_sel:[0,1] op_sel_hi:[1,0]
	v_mov_b32_e32 v64, v73
	v_pk_mul_f32 v[60:61], v[74:75], v[68:69] op_sel:[0,1] op_sel_hi:[1,0]
	v_mov_b32_e32 v82, v77
	v_pk_fma_f32 v[188:189], v[188:189], v[66:67], v[194:195]
	v_pk_fma_f32 v[60:61], v[64:65], v[68:69], v[60:61]
	v_mov_b32_e32 v78, v81
	v_pk_mul_f32 v[64:65], v[82:83], v[66:67] op_sel:[0,1] op_sel_hi:[1,0]
	v_pk_add_f32 v[56:57], v[56:57], v[188:189]
	v_pk_fma_f32 v[64:65], v[78:79], v[66:67], v[64:65]
	v_pk_add_f32 v[56:57], v[56:57], v[84:85]
	v_pk_add_f32 v[60:61], v[60:61], v[64:65]
	v_and_b32_sdwa v65, v56, v129 dst_sel:DWORD dst_unused:UNUSED_PAD src0_sel:WORD_1 src1_sel:DWORD
	v_pk_add_f32 v[60:61], v[60:61], v[86:87]
	v_add3_u32 v72, v56, v65, s4
	v_and_b32_sdwa v65, v61, v129 dst_sel:DWORD dst_unused:UNUSED_PAD src0_sel:WORD_1 src1_sel:DWORD
	v_and_b32_sdwa v73, v60, v129 dst_sel:DWORD dst_unused:UNUSED_PAD src0_sel:WORD_1 src1_sel:DWORD
	v_and_b32_sdwa v64, v57, v129 dst_sel:DWORD dst_unused:UNUSED_PAD src0_sel:WORD_1 src1_sel:DWORD
	v_add3_u32 v65, v61, v65, s4
	v_add3_u32 v73, v60, v73, s4
	v_add3_u32 v64, v57, v64, s4
	v_and_b32_e32 v65, 0xffff0000, v65
	v_and_b32_e32 v73, 0xffff0000, v73
	v_or_b32_sdwa v65, v65, v64 dst_sel:DWORD dst_unused:UNUSED_PAD src0_sel:DWORD src1_sel:WORD_1
	v_or_b32_sdwa v64, v73, v72 dst_sel:DWORD dst_unused:UNUSED_PAD src0_sel:DWORD src1_sel:WORD_1
	global_store_dwordx2 v[30:31], v[64:65], off offset:512
	v_pk_mul_f32 v[64:65], v[60:61], v[60:61]
	s_nop 0
	v_pk_fma_f32 v[76:77], v[56:57], v[56:57], v[64:65]
	v_cvt_pk_f32_fp8_e32 v[64:65], v177
	v_cvt_pk_f32_fp8_sdwa v[78:79], v179 src0_sel:WORD_1
	v_cvt_pk_f32_fp8_sdwa v[72:73], v177 src0_sel:WORD_1
	v_cvt_pk_f32_fp8_e32 v[74:75], v179
	v_cvt_pk_f32_fp8_e32 v[80:81], v180
	s_waitcnt vmcnt(63)
	v_cvt_pk_f32_fp8_sdwa v[86:87], v181 src0_sel:WORD_1
	v_cvt_pk_f32_fp8_sdwa v[82:83], v180 src0_sel:WORD_1
	v_cvt_pk_f32_fp8_e32 v[84:85], v181
	v_mov_b32_e32 v194, v64
	v_mov_b32_e32 v195, v78
	v_lshlrev_b32_e32 v181, 16, v51
	v_lshlrev_b32_e32 v180, 16, v50
	v_and_b32_e32 v189, 0xffff0000, v51
	v_and_b32_e32 v188, 0xffff0000, v50
	v_mov_b32_e32 v50, v74
	v_mov_b32_e32 v51, v72
	v_pk_mul_f32 v[194:195], v[194:195], v[68:69] op_sel:[0,1] op_sel_hi:[1,0]
	v_mov_b32_e32 v200, v80
	v_mov_b32_e32 v201, v86
	v_mov_b32_e32 v78, v65
	v_pk_fma_f32 v[50:51], v[50:51], v[68:69], v[194:195]
	v_mov_b32_e32 v194, v84
	v_mov_b32_e32 v195, v82
	v_pk_mul_f32 v[200:201], v[200:201], v[66:67] op_sel:[0,1] op_sel_hi:[1,0]
	v_mov_b32_e32 v72, v75
	v_pk_mul_f32 v[64:65], v[78:79], v[68:69] op_sel:[0,1] op_sel_hi:[1,0]
	v_mov_b32_e32 v86, v81
	v_pk_fma_f32 v[194:195], v[194:195], v[66:67], v[200:201]
	v_pk_fma_f32 v[64:65], v[72:73], v[68:69], v[64:65]
	v_mov_b32_e32 v82, v85
	v_pk_mul_f32 v[72:73], v[86:87], v[66:67] op_sel:[0,1] op_sel_hi:[1,0]
	v_pk_add_f32 v[50:51], v[50:51], v[194:195]
	v_pk_fma_f32 v[72:73], v[82:83], v[66:67], v[72:73]
	v_pk_add_f32 v[50:51], v[50:51], v[180:181]
	v_pk_add_f32 v[64:65], v[64:65], v[72:73]
	v_and_b32_sdwa v73, v50, v129 dst_sel:DWORD dst_unused:UNUSED_PAD src0_sel:WORD_1 src1_sel:DWORD
	v_pk_add_f32 v[64:65], v[64:65], v[188:189]
	v_add3_u32 v74, v50, v73, s4
	v_and_b32_sdwa v73, v65, v129 dst_sel:DWORD dst_unused:UNUSED_PAD src0_sel:WORD_1 src1_sel:DWORD
	v_and_b32_sdwa v75, v64, v129 dst_sel:DWORD dst_unused:UNUSED_PAD src0_sel:WORD_1 src1_sel:DWORD
	v_and_b32_sdwa v72, v51, v129 dst_sel:DWORD dst_unused:UNUSED_PAD src0_sel:WORD_1 src1_sel:DWORD
	v_add3_u32 v73, v65, v73, s4
	v_add3_u32 v75, v64, v75, s4
	v_add3_u32 v72, v51, v72, s4
	v_and_b32_e32 v73, 0xffff0000, v73
	v_and_b32_e32 v75, 0xffff0000, v75
	v_or_b32_sdwa v73, v73, v72 dst_sel:DWORD dst_unused:UNUSED_PAD src0_sel:DWORD src1_sel:WORD_1
	v_or_b32_sdwa v72, v75, v74 dst_sel:DWORD dst_unused:UNUSED_PAD src0_sel:DWORD src1_sel:WORD_1
	global_store_dwordx2 v[30:31], v[72:73], off offset:1024
	v_pk_mul_f32 v[72:73], v[64:65], v[64:65]
	s_nop 0
	v_pk_fma_f32 v[80:81], v[50:51], v[50:51], v[72:73]
	v_cvt_pk_f32_fp8_e32 v[72:73], v169
	v_cvt_pk_f32_fp8_sdwa v[82:83], v171 src0_sel:WORD_1
	v_cvt_pk_f32_fp8_sdwa v[74:75], v169 src0_sel:WORD_1
	v_cvt_pk_f32_fp8_e32 v[78:79], v171
	v_cvt_pk_f32_fp8_e32 v[84:85], v172
	v_cvt_pk_f32_fp8_sdwa v[86:87], v172 src0_sel:WORD_1
	s_waitcnt vmcnt(63)
	v_cvt_pk_f32_fp8_e32 v[180:181], v173
	v_cvt_pk_f32_fp8_sdwa v[172:173], v173 src0_sel:WORD_1
	v_mov_b32_e32 v200, v72
	v_mov_b32_e32 v201, v82
	v_lshlrev_b32_e32 v189, 16, v47
	v_lshlrev_b32_e32 v188, 16, v46
	v_and_b32_e32 v195, 0xffff0000, v47
	v_and_b32_e32 v194, 0xffff0000, v46
	v_mov_b32_e32 v46, v78
	v_mov_b32_e32 v47, v74
	v_pk_mul_f32 v[200:201], v[200:201], v[68:69] op_sel:[0,1] op_sel_hi:[1,0]
	v_mov_b32_e32 v202, v84
	v_mov_b32_e32 v203, v172
	v_mov_b32_e32 v82, v73
	v_pk_fma_f32 v[46:47], v[46:47], v[68:69], v[200:201]
	v_mov_b32_e32 v200, v180
	v_mov_b32_e32 v201, v86
	v_pk_mul_f32 v[202:203], v[202:203], v[66:67] op_sel:[0,1] op_sel_hi:[1,0]
	v_mov_b32_e32 v74, v79
	v_pk_mul_f32 v[72:73], v[82:83], v[68:69] op_sel:[0,1] op_sel_hi:[1,0]
	v_mov_b32_e32 v172, v85
	v_pk_fma_f32 v[200:201], v[200:201], v[66:67], v[202:203]
	v_pk_fma_f32 v[72:73], v[74:75], v[68:69], v[72:73]
	v_mov_b32_e32 v86, v181
	v_pk_mul_f32 v[74:75], v[172:173], v[66:67] op_sel:[0,1] op_sel_hi:[1,0]
	v_pk_add_f32 v[46:47], v[46:47], v[200:201]
	v_pk_fma_f32 v[74:75], v[86:87], v[66:67], v[74:75]
	v_pk_add_f32 v[46:47], v[46:47], v[188:189]
	v_pk_add_f32 v[72:73], v[72:73], v[74:75]
	v_and_b32_sdwa v75, v46, v129 dst_sel:DWORD dst_unused:UNUSED_PAD src0_sel:WORD_1 src1_sel:DWORD
	v_pk_add_f32 v[72:73], v[72:73], v[194:195]
	v_add3_u32 v78, v46, v75, s4
	v_and_b32_sdwa v75, v73, v129 dst_sel:DWORD dst_unused:UNUSED_PAD src0_sel:WORD_1 src1_sel:DWORD
	v_and_b32_sdwa v79, v72, v129 dst_sel:DWORD dst_unused:UNUSED_PAD src0_sel:WORD_1 src1_sel:DWORD
	v_and_b32_sdwa v74, v47, v129 dst_sel:DWORD dst_unused:UNUSED_PAD src0_sel:WORD_1 src1_sel:DWORD
	v_add3_u32 v75, v73, v75, s4
	v_add3_u32 v79, v72, v79, s4
	v_add3_u32 v74, v47, v74, s4
	v_and_b32_e32 v75, 0xffff0000, v75
	v_and_b32_e32 v79, 0xffff0000, v79
	v_or_b32_sdwa v75, v75, v74 dst_sel:DWORD dst_unused:UNUSED_PAD src0_sel:DWORD src1_sel:WORD_1
	v_or_b32_sdwa v74, v79, v78 dst_sel:DWORD dst_unused:UNUSED_PAD src0_sel:DWORD src1_sel:WORD_1
	global_store_dwordx2 v[30:31], v[74:75], off offset:1536
	v_pk_mul_f32 v[74:75], v[72:73], v[72:73]
	s_nop 0
	v_pk_fma_f32 v[86:87], v[46:47], v[46:47], v[74:75]
	v_cvt_pk_f32_fp8_e32 v[74:75], v162
	v_cvt_pk_f32_fp8_sdwa v[84:85], v163 src0_sel:WORD_1
	v_cvt_pk_f32_fp8_sdwa v[78:79], v162 src0_sel:WORD_1
	v_cvt_pk_f32_fp8_e32 v[82:83], v163
	v_cvt_pk_f32_fp8_e32 v[162:163], v164
	v_cvt_pk_f32_fp8_sdwa v[172:173], v164 src0_sel:WORD_1
	s_waitcnt vmcnt(63)
	v_cvt_pk_f32_fp8_e32 v[180:181], v165
	v_cvt_pk_f32_fp8_sdwa v[164:165], v165 src0_sel:WORD_1
	v_mov_b32_e32 v200, v74
	v_mov_b32_e32 v201, v84
	v_lshlrev_b32_e32 v189, 16, v43
	v_lshlrev_b32_e32 v188, 16, v42
	v_and_b32_e32 v195, 0xffff0000, v43
	v_and_b32_e32 v194, 0xffff0000, v42
	v_mov_b32_e32 v42, v82
	v_mov_b32_e32 v43, v78
	v_pk_mul_f32 v[200:201], v[200:201], v[68:69] op_sel:[0,1] op_sel_hi:[1,0]
	v_mov_b32_e32 v202, v162
	v_mov_b32_e32 v203, v164
	v_mov_b32_e32 v84, v75
	v_pk_fma_f32 v[42:43], v[42:43], v[68:69], v[200:201]
	v_mov_b32_e32 v200, v180
	v_mov_b32_e32 v201, v172
	v_pk_mul_f32 v[202:203], v[202:203], v[66:67] op_sel:[0,1] op_sel_hi:[1,0]
	v_mov_b32_e32 v78, v83
	v_pk_mul_f32 v[74:75], v[84:85], v[68:69] op_sel:[0,1] op_sel_hi:[1,0]
	v_mov_b32_e32 v164, v163
	v_pk_fma_f32 v[200:201], v[200:201], v[66:67], v[202:203]
	v_pk_fma_f32 v[74:75], v[78:79], v[68:69], v[74:75]
	v_mov_b32_e32 v172, v181
	v_pk_mul_f32 v[78:79], v[164:165], v[66:67] op_sel:[0,1] op_sel_hi:[1,0]
	v_pk_add_f32 v[42:43], v[42:43], v[200:201]
	v_pk_fma_f32 v[78:79], v[172:173], v[66:67], v[78:79]
	v_pk_add_f32 v[42:43], v[42:43], v[188:189]
	v_pk_add_f32 v[74:75], v[74:75], v[78:79]
	v_and_b32_sdwa v79, v42, v129 dst_sel:DWORD dst_unused:UNUSED_PAD src0_sel:WORD_1 src1_sel:DWORD
	v_pk_add_f32 v[74:75], v[74:75], v[194:195]
	v_add3_u32 v82, v42, v79, s4
	v_and_b32_sdwa v79, v75, v129 dst_sel:DWORD dst_unused:UNUSED_PAD src0_sel:WORD_1 src1_sel:DWORD
	v_and_b32_sdwa v83, v74, v129 dst_sel:DWORD dst_unused:UNUSED_PAD src0_sel:WORD_1 src1_sel:DWORD
	v_and_b32_sdwa v78, v43, v129 dst_sel:DWORD dst_unused:UNUSED_PAD src0_sel:WORD_1 src1_sel:DWORD
	v_add3_u32 v79, v75, v79, s4
	v_add3_u32 v83, v74, v83, s4
	v_add3_u32 v78, v43, v78, s4
	v_and_b32_e32 v79, 0xffff0000, v79
	v_and_b32_e32 v83, 0xffff0000, v83
	v_or_b32_sdwa v79, v79, v78 dst_sel:DWORD dst_unused:UNUSED_PAD src0_sel:DWORD src1_sel:WORD_1
	v_or_b32_sdwa v78, v83, v82 dst_sel:DWORD dst_unused:UNUSED_PAD src0_sel:DWORD src1_sel:WORD_1
	global_store_dwordx2 v[30:31], v[78:79], off offset:2048
	v_pk_mul_f32 v[78:79], v[74:75], v[74:75]
	s_nop 0
	v_pk_fma_f32 v[162:163], v[42:43], v[42:43], v[78:79]
	v_cvt_pk_f32_fp8_e32 v[78:79], v154
	v_cvt_pk_f32_fp8_sdwa v[82:83], v154 src0_sel:WORD_1
	v_cvt_pk_f32_fp8_e32 v[84:85], v155
	v_cvt_pk_f32_fp8_sdwa v[154:155], v155 src0_sel:WORD_1
	v_cvt_pk_f32_fp8_e32 v[164:165], v156
	v_cvt_pk_f32_fp8_sdwa v[172:173], v156 src0_sel:WORD_1
	s_waitcnt vmcnt(63)
	v_cvt_pk_f32_fp8_e32 v[180:181], v157
	v_cvt_pk_f32_fp8_sdwa v[156:157], v157 src0_sel:WORD_1
	v_mov_b32_e32 v200, v78
	v_mov_b32_e32 v201, v154
	v_lshlrev_b32_e32 v189, 16, v37
	v_lshlrev_b32_e32 v188, 16, v36
	v_and_b32_e32 v195, 0xffff0000, v37
	v_and_b32_e32 v194, 0xffff0000, v36
	v_mov_b32_e32 v36, v84
	v_mov_b32_e32 v37, v82
	v_pk_mul_f32 v[200:201], v[200:201], v[68:69] op_sel:[0,1] op_sel_hi:[1,0]
	v_mov_b32_e32 v202, v164
	v_mov_b32_e32 v203, v156
	v_mov_b32_e32 v154, v79
	v_pk_fma_f32 v[36:37], v[36:37], v[68:69], v[200:201]
	v_mov_b32_e32 v200, v180
	v_mov_b32_e32 v201, v172
	v_pk_mul_f32 v[202:203], v[202:203], v[66:67] op_sel:[0,1] op_sel_hi:[1,0]
	v_mov_b32_e32 v82, v85
	v_pk_mul_f32 v[78:79], v[154:155], v[68:69] op_sel:[0,1] op_sel_hi:[1,0]
	v_mov_b32_e32 v156, v165
	v_pk_fma_f32 v[200:201], v[200:201], v[66:67], v[202:203]
	v_pk_fma_f32 v[78:79], v[82:83], v[68:69], v[78:79]
	v_mov_b32_e32 v172, v181
	v_pk_mul_f32 v[82:83], v[156:157], v[66:67] op_sel:[0,1] op_sel_hi:[1,0]
	v_pk_add_f32 v[36:37], v[36:37], v[200:201]
	v_pk_fma_f32 v[82:83], v[172:173], v[66:67], v[82:83]
	v_pk_add_f32 v[36:37], v[36:37], v[188:189]
	v_pk_add_f32 v[78:79], v[78:79], v[82:83]
	v_and_b32_sdwa v83, v36, v129 dst_sel:DWORD dst_unused:UNUSED_PAD src0_sel:WORD_1 src1_sel:DWORD
	v_pk_add_f32 v[78:79], v[78:79], v[194:195]
	v_add3_u32 v84, v36, v83, s4
	v_and_b32_sdwa v83, v79, v129 dst_sel:DWORD dst_unused:UNUSED_PAD src0_sel:WORD_1 src1_sel:DWORD
	v_and_b32_sdwa v85, v78, v129 dst_sel:DWORD dst_unused:UNUSED_PAD src0_sel:WORD_1 src1_sel:DWORD
	v_and_b32_sdwa v82, v37, v129 dst_sel:DWORD dst_unused:UNUSED_PAD src0_sel:WORD_1 src1_sel:DWORD
	v_add3_u32 v83, v79, v83, s4
	v_add3_u32 v85, v78, v85, s4
	v_add3_u32 v82, v37, v82, s4
	v_and_b32_e32 v83, 0xffff0000, v83
	v_and_b32_e32 v85, 0xffff0000, v85
	v_or_b32_sdwa v83, v83, v82 dst_sel:DWORD dst_unused:UNUSED_PAD src0_sel:DWORD src1_sel:WORD_1
	v_or_b32_sdwa v82, v85, v84 dst_sel:DWORD dst_unused:UNUSED_PAD src0_sel:DWORD src1_sel:WORD_1
	global_store_dwordx2 v[30:31], v[82:83], off offset:2560
	v_pk_mul_f32 v[82:83], v[78:79], v[78:79]
	s_nop 0
	v_pk_fma_f32 v[154:155], v[36:37], v[36:37], v[82:83]
	v_cvt_pk_f32_fp8_e32 v[84:85], v145
	v_cvt_pk_f32_fp8_sdwa v[164:165], v146 src0_sel:WORD_1
	v_cvt_pk_f32_fp8_sdwa v[144:145], v145 src0_sel:WORD_1
	v_cvt_pk_f32_fp8_e32 v[156:157], v146
	v_cvt_pk_f32_fp8_e32 v[172:173], v147
	s_waitcnt vmcnt(63)
	v_cvt_pk_f32_fp8_sdwa v[188:189], v148 src0_sel:WORD_1
	v_cvt_pk_f32_fp8_sdwa v[146:147], v147 src0_sel:WORD_1
	v_cvt_pk_f32_fp8_e32 v[180:181], v148
	v_mov_b32_e32 v200, v84
	v_mov_b32_e32 v201, v164
	v_mov_b32_e32 v194, v156
	v_mov_b32_e32 v195, v144
	v_pk_mul_f32 v[200:201], v[200:201], v[68:69] op_sel:[0,1] op_sel_hi:[1,0]
	v_mov_b32_e32 v202, v172
	v_mov_b32_e32 v203, v188
	v_mov_b32_e32 v164, v85
	v_pk_fma_f32 v[194:195], v[194:195], v[68:69], v[200:201]
	v_mov_b32_e32 v200, v180
	v_mov_b32_e32 v201, v146
	v_pk_mul_f32 v[202:203], v[202:203], v[66:67] op_sel:[0,1] op_sel_hi:[1,0]
	v_mov_b32_e32 v144, v157
	v_pk_mul_f32 v[84:85], v[164:165], v[68:69] op_sel:[0,1] op_sel_hi:[1,0]
	v_mov_b32_e32 v188, v173
	v_pk_fma_f32 v[200:201], v[200:201], v[66:67], v[202:203]
	v_pk_fma_f32 v[84:85], v[144:145], v[68:69], v[84:85]
	v_mov_b32_e32 v146, v181
	v_pk_mul_f32 v[144:145], v[188:189], v[66:67] op_sel:[0,1] op_sel_hi:[1,0]
	v_lshlrev_b32_e32 v83, 16, v33
	v_lshlrev_b32_e32 v82, 16, v32
	v_pk_add_f32 v[194:195], v[194:195], v[200:201]
	v_pk_fma_f32 v[144:145], v[146:147], v[66:67], v[144:145]
	v_and_b32_e32 v33, 0xffff0000, v33
	v_and_b32_e32 v32, 0xffff0000, v32
	v_pk_add_f32 v[82:83], v[194:195], v[82:83]
	v_pk_add_f32 v[84:85], v[84:85], v[144:145]
	s_nop 0
	v_pk_add_f32 v[84:85], v[84:85], v[32:33]
	v_and_b32_sdwa v33, v82, v129 dst_sel:DWORD dst_unused:UNUSED_PAD src0_sel:WORD_1 src1_sel:DWORD
	v_add3_u32 v134, v82, v33, s4
	v_and_b32_sdwa v33, v85, v129 dst_sel:DWORD dst_unused:UNUSED_PAD src0_sel:WORD_1 src1_sel:DWORD
	v_and_b32_sdwa v136, v84, v129 dst_sel:DWORD dst_unused:UNUSED_PAD src0_sel:WORD_1 src1_sel:DWORD
	v_and_b32_sdwa v32, v83, v129 dst_sel:DWORD dst_unused:UNUSED_PAD src0_sel:WORD_1 src1_sel:DWORD
	v_add3_u32 v33, v85, v33, s4
	v_add3_u32 v136, v84, v136, s4
	v_add3_u32 v32, v83, v32, s4
	v_and_b32_e32 v33, 0xffff0000, v33
	v_and_b32_e32 v136, 0xffff0000, v136
	v_or_b32_sdwa v33, v33, v32 dst_sel:DWORD dst_unused:UNUSED_PAD src0_sel:DWORD src1_sel:WORD_1
	v_or_b32_sdwa v32, v136, v134 dst_sel:DWORD dst_unused:UNUSED_PAD src0_sel:DWORD src1_sel:WORD_1
	global_store_dwordx2 v[30:31], v[32:33], off offset:3072
	v_pk_mul_f32 v[32:33], v[84:85], v[84:85]
	s_nop 0
	v_pk_fma_f32 v[144:145], v[82:83], v[82:83], v[32:33]
	v_cvt_pk_f32_fp8_e32 v[32:33], v132
	v_cvt_pk_f32_fp8_e32 v[156:157], v135
	v_cvt_pk_f32_fp8_sdwa v[134:135], v135 src0_sel:WORD_1
	v_cvt_pk_f32_fp8_sdwa v[146:147], v132 src0_sel:WORD_1
	v_cvt_pk_f32_fp8_e32 v[164:165], v137
	s_waitcnt vmcnt(63)
	v_cvt_pk_f32_fp8_sdwa v[180:181], v138 src0_sel:WORD_1
	v_cvt_pk_f32_fp8_sdwa v[136:137], v137 src0_sel:WORD_1
	v_cvt_pk_f32_fp8_e32 v[172:173], v138
	v_mov_b32_e32 v200, v32
	v_mov_b32_e32 v201, v134
	v_lshlrev_b32_e32 v189, 16, v27
	v_lshlrev_b32_e32 v188, 16, v26
	v_and_b32_e32 v195, 0xffff0000, v27
	v_and_b32_e32 v194, 0xffff0000, v26
	v_mov_b32_e32 v26, v156
	v_mov_b32_e32 v27, v146
	v_pk_mul_f32 v[200:201], v[200:201], v[68:69] op_sel:[0,1] op_sel_hi:[1,0]
	v_mov_b32_e32 v202, v164
	v_mov_b32_e32 v203, v180
	v_mov_b32_e32 v134, v33
	v_pk_fma_f32 v[26:27], v[26:27], v[68:69], v[200:201]
	v_mov_b32_e32 v200, v172
	v_mov_b32_e32 v201, v136
	v_pk_mul_f32 v[202:203], v[202:203], v[66:67] op_sel:[0,1] op_sel_hi:[1,0]
	v_mov_b32_e32 v146, v157
	v_pk_mul_f32 v[32:33], v[134:135], v[68:69] op_sel:[0,1] op_sel_hi:[1,0]
	v_mov_b32_e32 v180, v165
	v_pk_fma_f32 v[200:201], v[200:201], v[66:67], v[202:203]
	v_pk_fma_f32 v[32:33], v[146:147], v[68:69], v[32:33]
	v_mov_b32_e32 v136, v173
	v_pk_mul_f32 v[68:69], v[180:181], v[66:67] op_sel:[0,1] op_sel_hi:[1,0]
	v_pk_add_f32 v[26:27], v[26:27], v[200:201]
	v_pk_fma_f32 v[66:67], v[136:137], v[66:67], v[68:69]
	v_pk_add_f32 v[26:27], v[26:27], v[188:189]
	v_pk_add_f32 v[32:33], v[32:33], v[66:67]
	v_and_b32_sdwa v67, v26, v129 dst_sel:DWORD dst_unused:UNUSED_PAD src0_sel:WORD_1 src1_sel:DWORD
	v_pk_add_f32 v[32:33], v[32:33], v[194:195]
	v_add3_u32 v68, v26, v67, s4
	v_and_b32_sdwa v67, v33, v129 dst_sel:DWORD dst_unused:UNUSED_PAD src0_sel:WORD_1 src1_sel:DWORD
	v_and_b32_sdwa v69, v32, v129 dst_sel:DWORD dst_unused:UNUSED_PAD src0_sel:WORD_1 src1_sel:DWORD
	v_and_b32_sdwa v66, v27, v129 dst_sel:DWORD dst_unused:UNUSED_PAD src0_sel:WORD_1 src1_sel:DWORD
	v_add3_u32 v67, v33, v67, s4
	v_add3_u32 v69, v32, v69, s4
	v_add3_u32 v66, v27, v66, s4
	v_and_b32_e32 v67, 0xffff0000, v67
	v_and_b32_e32 v69, 0xffff0000, v69
	v_or_b32_sdwa v67, v67, v66 dst_sel:DWORD dst_unused:UNUSED_PAD src0_sel:DWORD src1_sel:WORD_1
	v_or_b32_sdwa v66, v69, v68 dst_sel:DWORD dst_unused:UNUSED_PAD src0_sel:DWORD src1_sel:WORD_1
	global_store_dwordx2 v[30:31], v[66:67], off offset:3584
	v_add_f32_e32 v66, v76, v77
	v_add_f32_e32 v67, v70, v71
	v_add_f32_e32 v66, v67, v66
	v_add_f32_e32 v67, v80, v81
	v_add_f32_e32 v66, v66, v67
	v_add_f32_e32 v67, v86, v87
	v_add_f32_e32 v66, v66, v67
	v_add_f32_e32 v67, v162, v163
	v_pk_mul_f32 v[30:31], v[32:33], v[32:33]
	v_add_f32_e32 v66, v66, v67
	v_add_f32_e32 v67, v154, v155
	v_pk_fma_f32 v[30:31], v[26:27], v[26:27], v[30:31]
	v_add_f32_e32 v66, v66, v67
	v_add_f32_e32 v67, v144, v145
	v_add_f32_e32 v66, v66, v67
	v_add_f32_e32 v30, v30, v31
	v_add_f32_e32 v30, v66, v30
	v_mov_b64_e32 v[66:67], v[212:213]
	v_mov_b64_e32 v[68:69], v[214:215]
	ds_bpermute_b32 v31, v1, v30
	s_waitcnt lgkmcnt(0)
	v_add_f32_e32 v30, v30, v31
	ds_bpermute_b32 v31, v90, v30
	s_waitcnt lgkmcnt(0)
	v_add_f32_e32 v30, v30, v31
	ds_bpermute_b32 v31, v91, v30
	s_waitcnt lgkmcnt(0)
	v_add_f32_e32 v30, v30, v31
	ds_bpermute_b32 v31, v92, v30
	s_waitcnt lgkmcnt(0)
	v_add_f32_e32 v30, v30, v31
	ds_bpermute_b32 v31, v93, v30
	s_waitcnt lgkmcnt(0)
	v_add_f32_e32 v30, v30, v31
	ds_bpermute_b32 v31, v94, v30
	s_waitcnt lgkmcnt(0)
	v_add_f32_e32 v30, v30, v31
	v_fmamk_f32 v30, v30, 0x3a000000, v127
	v_mul_f32_e32 v31, 0x4f800000, v30
	v_cmp_gt_f32_e32 vcc, s19, v30
	s_nop 1
	v_cndmask_b32_e32 v30, v30, v31, vcc
	v_sqrt_f32_e32 v31, v30
	s_nop 0
	v_add_u32_e32 v70, -1, v31
	v_add_u32_e32 v71, 1, v31
	v_fma_f32 v76, -v70, v31, v30
	v_fma_f32 v77, -v71, v31, v30
	v_cmp_ge_f32_e64 s[8:9], 0, v76
	s_nop 1
	v_cndmask_b32_e64 v31, v31, v70, s[8:9]
	v_cmp_lt_f32_e64 s[8:9], 0, v77
	s_nop 1
	v_cndmask_b32_e64 v31, v31, v71, s[8:9]
	v_mul_f32_e32 v70, 0x37800000, v31
	v_cndmask_b32_e32 v31, v31, v70, vcc
	v_cmp_class_f32_e32 vcc, v30, v128
	v_mov_b32_e32 v71, 0
	s_nop 0
	v_cndmask_b32_e32 v30, v31, v30, vcc
	v_div_scale_f32 v31, s[0:1], v30, v30, 1.0
	v_rcp_f32_e32 v70, v31
	v_div_scale_f32 v76, vcc, 1.0, v30, 1.0
	v_fma_f32 v77, -v31, v70, 1.0
	v_fmac_f32_e32 v70, v77, v70
	v_mul_f32_e32 v77, v76, v70
	v_fma_f32 v80, -v31, v77, v76
	v_fmac_f32_e32 v77, v80, v70
	v_fma_f32 v31, -v31, v77, v76
	v_div_fmas_f32 v31, v31, v70, v77
	v_div_fixup_f32 v70, v31, v30, 1.0
	v_mul_f32_e32 v30, v70, v40
	v_mul_f32_e32 v31, v70, v54

	v_mul_f32_e32 v30, v66, v30
	v_mul_f32_e32 v31, v67, v31
	v_cvt_pk_fp8_f32 v71, v30, v31
	v_mul_f32_e32 v40, v70, v41
	v_mul_f32_e32 v30, v70, v55
	v_mul_f32_e32 v31, v68, v40
	v_mul_f32_e32 v30, v69, v30
	v_cvt_pk_fp8_f32 v71, v31, v30 op_sel:[0,0,1]
	v_mul_f32_e32 v31, v70, v56
	v_mul_f32_e32 v40, v70, v60
	v_mov_b32_e32 v30, 0
	global_store_dword v[24:25], v71, off offset:2048
	v_mov_b64_e32 v[66:67], v[216:217]
	v_mov_b64_e32 v[68:69], v[218:219]
	v_mul_f32_e32 v41, v70, v57
	v_mul_f32_e32 v37, v70, v37
	v_mul_f32_e32 v26, v70, v26
	v_mul_f32_e32 v32, v70, v32
	v_mul_f32_e32 v27, v70, v27
	s_waitcnt vmcnt(41)
	v_cvt_pk_f32_fp8_e32 v[76:77], v190

	v_mul_f32_e32 v31, v66, v31
	v_mul_f32_e32 v40, v67, v40
	v_cvt_pk_fp8_f32 v30, v31, v40
	v_mul_f32_e32 v31, v70, v61
	v_mul_f32_e32 v40, v68, v41
	v_mul_f32_e32 v31, v69, v31
	v_cvt_pk_fp8_f32 v30, v40, v31 op_sel:[0,0,1]
	v_mul_f32_e32 v31, v70, v50
	v_mul_f32_e32 v40, v70, v64
	v_mul_f32_e32 v41, v70, v51
	global_store_dword v[24:25], v30, off offset:2304
	v_mov_b64_e32 v[54:55], v[220:221]
	v_mov_b64_e32 v[56:57], v[222:223]
	v_mov_b32_e32 v30, 0
	v_mov_b32_e32 v68, 0
	ds_bpermute_b32 v50, v118, v130
	s_waitcnt lgkmcnt(0)
	v_ashrrev_i32_e32 v51, 31, v50
	v_lshlrev_b64 v[50:51], 11, v[50:51]
	v_lshl_add_u64 v[50:51], v[4:5], 0, v[50:51]

	v_mul_f32_e32 v31, v54, v31
	v_mul_f32_e32 v40, v55, v40
	v_cvt_pk_fp8_f32 v30, v31, v40
	v_mul_f32_e32 v31, v70, v65
	v_mul_f32_e32 v40, v56, v41
	v_mul_f32_e32 v31, v57, v31
	v_cvt_pk_fp8_f32 v30, v40, v31 op_sel:[0,0,1]
	v_mul_f32_e32 v31, v70, v46
	v_mul_f32_e32 v40, v70, v72
	v_mul_f32_e32 v41, v70, v47
	global_store_dword v[24:25], v30, off offset:2560
	v_mov_b64_e32 v[54:55], v[224:225]
	v_mov_b64_e32 v[56:57], v[226:227]
	v_mov_b32_e32 v30, 0
	ds_bpermute_b32 v46, v117, v130
	s_waitcnt lgkmcnt(0)
	v_ashrrev_i32_e32 v47, 31, v46
	v_lshlrev_b64 v[46:47], 11, v[46:47]
	v_lshl_add_u64 v[64:65], v[4:5], 0, v[46:47]

	v_mul_f32_e32 v31, v54, v31
	v_mul_f32_e32 v40, v55, v40
	v_cvt_pk_fp8_f32 v30, v31, v40
	v_mul_f32_e32 v31, v70, v73
	v_mul_f32_e32 v40, v56, v41
	v_mul_f32_e32 v31, v57, v31
	v_cvt_pk_fp8_f32 v30, v40, v31 op_sel:[0,0,1]
	v_mul_f32_e32 v31, v70, v42
	v_mul_f32_e32 v40, v70, v74
	v_mul_f32_e32 v41, v70, v43
	global_store_dword v[24:25], v30, off offset:2816
	v_mov_b64_e32 v[54:55], v[228:229]
	v_mov_b64_e32 v[56:57], v[230:231]
	v_mov_b32_e32 v30, 0
	s_waitcnt vmcnt(36)
	v_cvt_pk_f32_fp8_e32 v[72:73], v191

	v_mul_f32_e32 v31, v54, v31
	v_mul_f32_e32 v40, v55, v40
	v_cvt_pk_fp8_f32 v30, v31, v40
	v_mul_f32_e32 v31, v70, v75
	v_mul_f32_e32 v40, v56, v41
	v_mul_f32_e32 v31, v57, v31
	v_cvt_pk_fp8_f32 v30, v40, v31 op_sel:[0,0,1]
	v_mul_f32_e32 v31, v70, v36
	v_mul_f32_e32 v36, v70, v78
	ds_bpermute_b32 v54, v119, v130
	global_store_dword v[24:25], v30, off offset:3072
	v_mov_b64_e32 v[40:41], v[232:233]
	v_mov_b64_e32 v[42:43], v[234:235]
	v_mov_b32_e32 v30, 0
	v_cvt_pk_f32_fp8_sdwa v[74:75], v191 src0_sel:WORD_1
	s_waitcnt lgkmcnt(0)
	v_ashrrev_i32_e32 v55, 31, v54
	v_lshlrev_b64 v[54:55], 11, v[54:55]
	v_lshl_add_u64 v[66:67], v[4:5], 0, v[54:55]

	v_mul_f32_e32 v31, v40, v31
	v_mul_f32_e32 v36, v41, v36
	v_cvt_pk_fp8_f32 v30, v31, v36
	v_mul_f32_e32 v31, v70, v79
	v_mul_f32_e32 v36, v42, v37
	v_mul_f32_e32 v31, v43, v31
	v_cvt_pk_fp8_f32 v30, v36, v31 op_sel:[0,0,1]
	v_mul_f32_e32 v31, v70, v82
	v_mul_f32_e32 v36, v70, v84
	v_mul_f32_e32 v37, v70, v83
	global_store_dword v[24:25], v30, off offset:3328
	v_mov_b64_e32 v[40:41], v[236:237]
	v_mov_b64_e32 v[42:43], v[238:239]
	v_mov_b32_e32 v30, 0
	v_cvt_pk_f32_fp8_sdwa v[78:79], v190 src0_sel:WORD_1
	v_mov_b32_e32 v84, v72

	v_mul_f32_e32 v31, v40, v31
	v_mul_f32_e32 v36, v41, v36
	v_cvt_pk_fp8_f32 v30, v31, v36
	v_mul_f32_e32 v31, v70, v85
	v_mul_f32_e32 v36, v42, v37
	v_mul_f32_e32 v31, v43, v31
	v_cvt_pk_fp8_f32 v30, v36, v31 op_sel:[0,0,1]
	ds_bpermute_b32 v36, v116, v130
	v_mov_b32_e32 v85, v78
	v_mov_b32_e32 v78, v73
	global_store_dword v[24:25], v30, off offset:3584
	v_mov_b64_e32 v[40:41], v[240:241]
	v_mov_b64_e32 v[42:43], v[242:243]
	v_add_co_u32_e32 v30, vcc, s34, v20
	s_waitcnt lgkmcnt(0)
	v_ashrrev_i32_e32 v37, 31, v36
	v_addc_co_u32_e32 v31, vcc, 0, v21, vcc
	v_lshlrev_b64 v[36:37], 11, v[36:37]
	v_add_co_u32_e32 v56, vcc, s37, v20
	v_lshl_add_u64 v[60:61], v[4:5], 0, v[36:37]
	s_nop 0
	v_addc_co_u32_e32 v57, vcc, 0, v21, vcc
	v_add_co_u32_e32 v72, vcc, s35, v20

	v_mul_f32_e32 v26, v40, v26
	v_mul_f32_e32 v32, v41, v32
	v_cvt_pk_fp8_f32 v68, v26, v32
	v_mul_f32_e32 v26, v70, v33
	v_mul_f32_e32 v27, v42, v27
	v_mul_f32_e32 v26, v43, v26
	v_cvt_pk_fp8_f32 v68, v27, v26 op_sel:[0,0,1]
	s_waitcnt vmcnt(31)
	v_cvt_pk_f32_fp8_sdwa v[70:71], v193 src0_sel:WORD_1
	v_addc_co_u32_e32 v73, vcc, 0, v21, vcc
	global_store_dword v[24:25], v68, off offset:3840
	global_load_dwordx2 v[54:55], v[30:31], off offset:512 nt
	global_load_dwordx2 v[46:47], v[30:31], off offset:1024 nt
	global_load_dwordx2 v[42:43], v[30:31], off offset:1536 nt
	global_load_dwordx2 v[40:41], v[30:31], off offset:2048 nt
	global_load_dwordx2 v[36:37], v[30:31], off offset:2560 nt
	global_load_dwordx2 v[32:33], v[30:31], off offset:3072 nt
	global_load_dwordx2 v[26:27], v[30:31], off offset:3584 nt
	global_load_dword v188, v[60:61], off nt
	global_load_dword v180, v[60:61], off offset:256 nt
	global_load_dword v172, v[60:61], off offset:512 nt
	global_load_dword v164, v[60:61], off offset:768 nt
	global_load_dword v156, v[60:61], off offset:1024 nt
	global_load_dword v147, v[60:61], off offset:1280 nt
	global_load_dword v142, v[60:61], off offset:1536 nt
	global_load_dword v132, v[60:61], off offset:1792 nt
	global_load_dword v189, v[64:65], off nt
	global_load_dword v181, v[64:65], off offset:256 nt
	global_load_dword v173, v[64:65], off offset:512 nt
	global_load_dword v165, v[64:65], off offset:768 nt
	global_load_dword v157, v[64:65], off offset:1024 nt
	global_load_dword v152, v[64:65], off offset:1280 nt
	global_load_dword v144, v[64:65], off offset:1536 nt
	global_load_dword v134, v[64:65], off offset:1792 nt
	global_load_dword v192, v[50:51], off nt
	global_load_dword v185, v[50:51], off offset:256 nt
	global_load_dword v177, v[50:51], off offset:512 nt
	global_load_dword v169, v[50:51], off offset:768 nt
	global_load_dword v162, v[50:51], off offset:1024 nt
	global_load_dword v154, v[50:51], off offset:1280 nt
	global_load_dword v145, v[50:51], off offset:1536 nt
	global_load_dword v135, v[50:51], off offset:1792 nt
	global_load_dword v194, v[66:67], off nt
	global_load_dwordx2 v[60:61], v[56:57], off offset:-4096 nt
	global_load_dword v187, v[66:67], off offset:256 nt
	global_load_dword v179, v[66:67], off offset:512 nt
	global_load_dword v171, v[66:67], off offset:768 nt
	global_load_dword v163, v[66:67], off offset:1024 nt
	global_load_dword v155, v[66:67], off offset:1280 nt
	global_load_dword v146, v[66:67], off offset:1536 nt
	global_load_dword v136, v[66:67], off offset:1792 nt
	ds_bpermute_b32 v67, v112, v19
	ds_bpermute_b32 v66, v113, v19
	s_waitcnt vmcnt(63)
	v_cvt_pk_f32_fp8_e32 v[30:31], v196
	ds_bpermute_b32 v65, v114, v19
	ds_bpermute_b32 v64, v115, v19
	v_cvt_pk_f32_fp8_sdwa v[50:51], v196 src0_sel:WORD_1
	v_cvt_pk_f32_fp8_e32 v[68:69], v193
	v_mov_b32_e32 v82, v30
	v_mov_b32_e32 v83, v70
	v_mov_b32_e32 v70, v31
	v_mov_b32_e32 v80, v68
	v_mov_b32_e32 v81, v50
	s_waitcnt lgkmcnt(2)
	v_pk_mul_f32 v[82:83], v[82:83], v[66:67] op_sel:[0,1] op_sel_hi:[1,0]
	v_mov_b32_e32 v50, v69
	v_pk_mul_f32 v[30:31], v[70:71], v[66:67] op_sel:[0,1] op_sel_hi:[1,0]
	v_pk_fma_f32 v[80:81], v[80:81], v[66:67], v[82:83]
	v_mov_b32_e32 v83, v74
	v_pk_fma_f32 v[30:31], v[50:51], v[66:67], v[30:31]
	v_mov_b32_e32 v74, v77
	s_waitcnt lgkmcnt(0)
	v_pk_mul_f32 v[50:51], v[78:79], v[64:65] op_sel:[0,1] op_sel_hi:[1,0]
	v_mov_b32_e32 v82, v76
	v_pk_mul_f32 v[84:85], v[84:85], v[64:65] op_sel:[0,1] op_sel_hi:[1,0]
	v_pk_fma_f32 v[50:51], v[74:75], v[64:65], v[50:51]
	s_waitcnt vmcnt(56)
	v_lshlrev_b32_e32 v25, 16, v63
	v_lshlrev_b32_e32 v24, 16, v62
	v_and_b32_e32 v63, 0xffff0000, v63
	v_and_b32_e32 v62, 0xffff0000, v62
	v_pk_fma_f32 v[82:83], v[82:83], v[64:65], v[84:85]
	v_pk_add_f32 v[30:31], v[30:31], v[50:51]
	v_pk_add_f32 v[80:81], v[80:81], v[82:83]
	v_pk_add_f32 v[50:51], v[30:31], v[62:63]
	v_pk_add_f32 v[24:25], v[80:81], v[24:25]
	v_and_b32_sdwa v62, v51, v129 dst_sel:DWORD dst_unused:UNUSED_PAD src0_sel:WORD_1 src1_sel:DWORD
	v_and_b32_sdwa v30, v25, v129 dst_sel:DWORD dst_unused:UNUSED_PAD src0_sel:WORD_1 src1_sel:DWORD
	v_and_b32_sdwa v63, v50, v129 dst_sel:DWORD dst_unused:UNUSED_PAD src0_sel:WORD_1 src1_sel:DWORD
	v_add3_u32 v62, v51, v62, s4
	v_and_b32_sdwa v31, v24, v129 dst_sel:DWORD dst_unused:UNUSED_PAD src0_sel:WORD_1 src1_sel:DWORD
	v_add3_u32 v30, v25, v30, s4
	v_add3_u32 v63, v50, v63, s4
	v_and_b32_e32 v62, 0xffff0000, v62
	v_add3_u32 v31, v24, v31, s4
	v_and_b32_e32 v68, 0xffff0000, v63
	v_or_b32_sdwa v63, v62, v30 dst_sel:DWORD dst_unused:UNUSED_PAD src0_sel:DWORD src1_sel:WORD_1
	v_add_co_u32_e32 v30, vcc, s38, v20
	v_or_b32_sdwa v62, v68, v31 dst_sel:DWORD dst_unused:UNUSED_PAD src0_sel:DWORD src1_sel:WORD_1
	s_nop 0
	v_addc_co_u32_e32 v31, vcc, 0, v21, vcc
	global_store_dwordx2 v[30:31], v[62:63], off offset:-4096
	v_pk_mul_f32 v[62:63], v[50:51], v[50:51]
	s_nop 0
	v_pk_fma_f32 v[74:75], v[24:25], v[24:25], v[62:63]
	v_cvt_pk_f32_fp8_e32 v[62:63], v186
	v_cvt_pk_f32_fp8_sdwa v[76:77], v184 src0_sel:WORD_1
	v_cvt_pk_f32_fp8_sdwa v[68:69], v186 src0_sel:WORD_1
	v_cvt_pk_f32_fp8_e32 v[70:71], v184
	v_cvt_pk_f32_fp8_e32 v[78:79], v183
	v_cvt_pk_f32_fp8_sdwa v[84:85], v182 src0_sel:WORD_1
	v_cvt_pk_f32_fp8_sdwa v[80:81], v183 src0_sel:WORD_1
	v_cvt_pk_f32_fp8_e32 v[82:83], v182
	v_mov_b32_e32 v190, v62
	v_mov_b32_e32 v191, v76
	v_lshlrev_b32_e32 v87, 16, v59
	v_lshlrev_b32_e32 v86, 16, v58
	v_and_b32_e32 v183, 0xffff0000, v59
	v_and_b32_e32 v182, 0xffff0000, v58
	v_mov_b32_e32 v58, v70
	v_mov_b32_e32 v59, v68
	v_pk_mul_f32 v[190:191], v[190:191], v[66:67] op_sel:[0,1] op_sel_hi:[1,0]
	v_mov_b32_e32 v196, v78
	v_mov_b32_e32 v197, v84
	v_mov_b32_e32 v76, v63
	v_pk_fma_f32 v[58:59], v[58:59], v[66:67], v[190:191]
	v_mov_b32_e32 v190, v82
	v_mov_b32_e32 v191, v80
	v_pk_mul_f32 v[196:197], v[196:197], v[64:65] op_sel:[0,1] op_sel_hi:[1,0]
	v_mov_b32_e32 v68, v71
	v_pk_mul_f32 v[62:63], v[76:77], v[66:67] op_sel:[0,1] op_sel_hi:[1,0]
	v_mov_b32_e32 v84, v79
	v_pk_fma_f32 v[190:191], v[190:191], v[64:65], v[196:197]
	v_pk_fma_f32 v[62:63], v[68:69], v[66:67], v[62:63]
	v_mov_b32_e32 v80, v83
	v_pk_mul_f32 v[68:69], v[84:85], v[64:65] op_sel:[0,1] op_sel_hi:[1,0]
	v_pk_add_f32 v[58:59], v[58:59], v[190:191]
	v_pk_fma_f32 v[68:69], v[80:81], v[64:65], v[68:69]
	v_pk_add_f32 v[58:59], v[58:59], v[86:87]
	v_pk_add_f32 v[62:63], v[62:63], v[68:69]
	v_and_b32_sdwa v69, v58, v129 dst_sel:DWORD dst_unused:UNUSED_PAD src0_sel:WORD_1 src1_sel:DWORD
	v_pk_add_f32 v[62:63], v[62:63], v[182:183]
	v_add3_u32 v70, v58, v69, s4
	v_and_b32_sdwa v69, v63, v129 dst_sel:DWORD dst_unused:UNUSED_PAD src0_sel:WORD_1 src1_sel:DWORD
	v_and_b32_sdwa v71, v62, v129 dst_sel:DWORD dst_unused:UNUSED_PAD src0_sel:WORD_1 src1_sel:DWORD
	v_and_b32_sdwa v68, v59, v129 dst_sel:DWORD dst_unused:UNUSED_PAD src0_sel:WORD_1 src1_sel:DWORD
	v_add3_u32 v69, v63, v69, s4
	v_add3_u32 v71, v62, v71, s4
	v_add3_u32 v68, v59, v68, s4
	v_and_b32_e32 v69, 0xffff0000, v69
	v_and_b32_e32 v71, 0xffff0000, v71
	v_or_b32_sdwa v69, v69, v68 dst_sel:DWORD dst_unused:UNUSED_PAD src0_sel:DWORD src1_sel:WORD_1
	v_or_b32_sdwa v68, v71, v70 dst_sel:DWORD dst_unused:UNUSED_PAD src0_sel:DWORD src1_sel:WORD_1
	global_store_dwordx2 v[72:73], v[68:69], off offset:512
	v_pk_mul_f32 v[68:69], v[62:63], v[62:63]
	s_nop 0
	v_pk_fma_f32 v[80:81], v[58:59], v[58:59], v[68:69]
	v_cvt_pk_f32_fp8_e32 v[68:69], v178
	v_cvt_pk_f32_fp8_sdwa v[78:79], v176 src0_sel:WORD_1
	v_cvt_pk_f32_fp8_sdwa v[70:71], v178 src0_sel:WORD_1
	v_cvt_pk_f32_fp8_e32 v[76:77], v176
	v_cvt_pk_f32_fp8_e32 v[82:83], v175
	v_cvt_pk_f32_fp8_sdwa v[84:85], v175 src0_sel:WORD_1
	v_cvt_pk_f32_fp8_e32 v[86:87], v174
	v_cvt_pk_f32_fp8_sdwa v[174:175], v174 src0_sel:WORD_1
	v_mov_b32_e32 v196, v68
	v_mov_b32_e32 v197, v78
	v_lshlrev_b32_e32 v183, 16, v53
	v_lshlrev_b32_e32 v182, 16, v52
	v_and_b32_e32 v191, 0xffff0000, v53
	v_and_b32_e32 v190, 0xffff0000, v52
	v_mov_b32_e32 v52, v76
	v_mov_b32_e32 v53, v70
	v_pk_mul_f32 v[196:197], v[196:197], v[66:67] op_sel:[0,1] op_sel_hi:[1,0]
	v_mov_b32_e32 v200, v82
	v_mov_b32_e32 v201, v174
	v_mov_b32_e32 v78, v69
	v_pk_fma_f32 v[52:53], v[52:53], v[66:67], v[196:197]
	v_mov_b32_e32 v196, v86
	v_mov_b32_e32 v197, v84
	v_pk_mul_f32 v[200:201], v[200:201], v[64:65] op_sel:[0,1] op_sel_hi:[1,0]
	v_mov_b32_e32 v70, v77
	v_pk_mul_f32 v[68:69], v[78:79], v[66:67] op_sel:[0,1] op_sel_hi:[1,0]
	v_mov_b32_e32 v174, v83
	v_pk_fma_f32 v[196:197], v[196:197], v[64:65], v[200:201]
	v_pk_fma_f32 v[68:69], v[70:71], v[66:67], v[68:69]
	v_mov_b32_e32 v84, v87
	v_pk_mul_f32 v[70:71], v[174:175], v[64:65] op_sel:[0,1] op_sel_hi:[1,0]
	v_pk_add_f32 v[52:53], v[52:53], v[196:197]
	v_pk_fma_f32 v[70:71], v[84:85], v[64:65], v[70:71]
	v_pk_add_f32 v[52:53], v[52:53], v[182:183]
	v_pk_add_f32 v[68:69], v[68:69], v[70:71]
	v_and_b32_sdwa v71, v52, v129 dst_sel:DWORD dst_unused:UNUSED_PAD src0_sel:WORD_1 src1_sel:DWORD
	v_pk_add_f32 v[68:69], v[68:69], v[190:191]
	v_add3_u32 v76, v52, v71, s4
	v_and_b32_sdwa v71, v69, v129 dst_sel:DWORD dst_unused:UNUSED_PAD src0_sel:WORD_1 src1_sel:DWORD
	v_and_b32_sdwa v77, v68, v129 dst_sel:DWORD dst_unused:UNUSED_PAD src0_sel:WORD_1 src1_sel:DWORD
	v_and_b32_sdwa v70, v53, v129 dst_sel:DWORD dst_unused:UNUSED_PAD src0_sel:WORD_1 src1_sel:DWORD
	v_add3_u32 v71, v69, v71, s4
	v_add3_u32 v77, v68, v77, s4
	v_add3_u32 v70, v53, v70, s4
	v_and_b32_e32 v71, 0xffff0000, v71
	v_and_b32_e32 v77, 0xffff0000, v77
	v_or_b32_sdwa v71, v71, v70 dst_sel:DWORD dst_unused:UNUSED_PAD src0_sel:DWORD src1_sel:WORD_1
	v_or_b32_sdwa v70, v77, v76 dst_sel:DWORD dst_unused:UNUSED_PAD src0_sel:DWORD src1_sel:WORD_1
	global_store_dwordx2 v[72:73], v[70:71], off offset:1024
	v_pk_mul_f32 v[70:71], v[68:69], v[68:69]
	s_nop 0
	v_pk_fma_f32 v[84:85], v[52:53], v[52:53], v[70:71]
	v_cvt_pk_f32_fp8_e32 v[76:77], v170
	v_cvt_pk_f32_fp8_sdwa v[86:87], v168 src0_sel:WORD_1
	v_cvt_pk_f32_fp8_sdwa v[78:79], v170 src0_sel:WORD_1
	v_cvt_pk_f32_fp8_e32 v[82:83], v168
	v_cvt_pk_f32_fp8_e32 v[174:175], v167
	v_cvt_pk_f32_fp8_sdwa v[182:183], v167 src0_sel:WORD_1
	v_cvt_pk_f32_fp8_e32 v[190:191], v166
	v_cvt_pk_f32_fp8_sdwa v[166:167], v166 src0_sel:WORD_1
	v_mov_b32_e32 v200, v76
	v_mov_b32_e32 v201, v86
	v_mov_b32_e32 v196, v82
	v_mov_b32_e32 v197, v78
	v_pk_mul_f32 v[200:201], v[200:201], v[66:67] op_sel:[0,1] op_sel_hi:[1,0]
	v_mov_b32_e32 v202, v174
	v_mov_b32_e32 v203, v166
	v_mov_b32_e32 v86, v77
	v_pk_fma_f32 v[196:197], v[196:197], v[66:67], v[200:201]
	v_mov_b32_e32 v200, v190
	v_mov_b32_e32 v201, v182
	v_pk_mul_f32 v[202:203], v[202:203], v[64:65] op_sel:[0,1] op_sel_hi:[1,0]
	v_mov_b32_e32 v78, v83
	v_pk_mul_f32 v[76:77], v[86:87], v[66:67] op_sel:[0,1] op_sel_hi:[1,0]
	v_mov_b32_e32 v166, v175
	v_pk_fma_f32 v[200:201], v[200:201], v[64:65], v[202:203]
	v_pk_fma_f32 v[76:77], v[78:79], v[66:67], v[76:77]
	v_mov_b32_e32 v182, v191
	v_pk_mul_f32 v[78:79], v[166:167], v[64:65] op_sel:[0,1] op_sel_hi:[1,0]
	v_lshlrev_b32_e32 v71, 16, v49
	v_lshlrev_b32_e32 v70, 16, v48
	v_pk_add_f32 v[196:197], v[196:197], v[200:201]
	v_pk_fma_f32 v[78:79], v[182:183], v[64:65], v[78:79]
	v_and_b32_e32 v49, 0xffff0000, v49
	v_and_b32_e32 v48, 0xffff0000, v48
	v_pk_add_f32 v[70:71], v[196:197], v[70:71]
	v_pk_add_f32 v[76:77], v[76:77], v[78:79]
	s_nop 0
	v_pk_add_f32 v[76:77], v[76:77], v[48:49]
	v_and_b32_sdwa v49, v70, v129 dst_sel:DWORD dst_unused:UNUSED_PAD src0_sel:WORD_1 src1_sel:DWORD
	v_add3_u32 v78, v70, v49, s4
	v_and_b32_sdwa v49, v77, v129 dst_sel:DWORD dst_unused:UNUSED_PAD src0_sel:WORD_1 src1_sel:DWORD
	v_and_b32_sdwa v79, v76, v129 dst_sel:DWORD dst_unused:UNUSED_PAD src0_sel:WORD_1 src1_sel:DWORD
	v_and_b32_sdwa v48, v71, v129 dst_sel:DWORD dst_unused:UNUSED_PAD src0_sel:WORD_1 src1_sel:DWORD
	v_add3_u32 v49, v77, v49, s4
	v_add3_u32 v79, v76, v79, s4
	v_add3_u32 v48, v71, v48, s4
	v_and_b32_e32 v49, 0xffff0000, v49
	v_and_b32_e32 v79, 0xffff0000, v79
	v_or_b32_sdwa v49, v49, v48 dst_sel:DWORD dst_unused:UNUSED_PAD src0_sel:DWORD src1_sel:WORD_1
	v_or_b32_sdwa v48, v79, v78 dst_sel:DWORD dst_unused:UNUSED_PAD src0_sel:DWORD src1_sel:WORD_1
	global_store_dwordx2 v[72:73], v[48:49], off offset:1536
	v_pk_mul_f32 v[48:49], v[76:77], v[76:77]
	s_nop 0
	v_pk_fma_f32 v[48:49], v[70:71], v[70:71], v[48:49]
	v_cvt_pk_f32_fp8_e32 v[78:79], v161
	v_cvt_pk_f32_fp8_sdwa v[82:83], v161 src0_sel:WORD_1
	v_cvt_pk_f32_fp8_e32 v[86:87], v160
	v_cvt_pk_f32_fp8_sdwa v[160:161], v160 src0_sel:WORD_1
	v_cvt_pk_f32_fp8_e32 v[166:167], v159
	v_cvt_pk_f32_fp8_sdwa v[174:175], v159 src0_sel:WORD_1
	v_cvt_pk_f32_fp8_e32 v[182:183], v158
	v_cvt_pk_f32_fp8_sdwa v[158:159], v158 src0_sel:WORD_1
	v_mov_b32_e32 v200, v78
	v_mov_b32_e32 v201, v160
	v_lshlrev_b32_e32 v191, 16, v45
	v_lshlrev_b32_e32 v190, 16, v44
	v_and_b32_e32 v197, 0xffff0000, v45
	v_and_b32_e32 v196, 0xffff0000, v44
	v_mov_b32_e32 v44, v86
	v_mov_b32_e32 v45, v82
	v_pk_mul_f32 v[200:201], v[200:201], v[66:67] op_sel:[0,1] op_sel_hi:[1,0]
	v_mov_b32_e32 v202, v166
	v_mov_b32_e32 v203, v158
	v_mov_b32_e32 v160, v79
	v_pk_fma_f32 v[44:45], v[44:45], v[66:67], v[200:201]
	v_mov_b32_e32 v200, v182
	v_mov_b32_e32 v201, v174
	v_pk_mul_f32 v[202:203], v[202:203], v[64:65] op_sel:[0,1] op_sel_hi:[1,0]
	v_mov_b32_e32 v82, v87
	v_pk_mul_f32 v[78:79], v[160:161], v[66:67] op_sel:[0,1] op_sel_hi:[1,0]
	v_mov_b32_e32 v158, v167
	v_pk_fma_f32 v[200:201], v[200:201], v[64:65], v[202:203]
	v_pk_fma_f32 v[78:79], v[82:83], v[66:67], v[78:79]
	v_mov_b32_e32 v174, v183
	v_pk_mul_f32 v[82:83], v[158:159], v[64:65] op_sel:[0,1] op_sel_hi:[1,0]
	v_pk_add_f32 v[44:45], v[44:45], v[200:201]
	v_pk_fma_f32 v[82:83], v[174:175], v[64:65], v[82:83]
	v_pk_add_f32 v[44:45], v[44:45], v[190:191]
	v_pk_add_f32 v[78:79], v[78:79], v[82:83]
	v_and_b32_sdwa v83, v44, v129 dst_sel:DWORD dst_unused:UNUSED_PAD src0_sel:WORD_1 src1_sel:DWORD
	v_pk_add_f32 v[78:79], v[78:79], v[196:197]
	v_add3_u32 v86, v44, v83, s4
	v_and_b32_sdwa v83, v79, v129 dst_sel:DWORD dst_unused:UNUSED_PAD src0_sel:WORD_1 src1_sel:DWORD
	v_and_b32_sdwa v87, v78, v129 dst_sel:DWORD dst_unused:UNUSED_PAD src0_sel:WORD_1 src1_sel:DWORD
	v_and_b32_sdwa v82, v45, v129 dst_sel:DWORD dst_unused:UNUSED_PAD src0_sel:WORD_1 src1_sel:DWORD
	v_add3_u32 v83, v79, v83, s4
	v_add3_u32 v87, v78, v87, s4
	v_add3_u32 v82, v45, v82, s4
	v_and_b32_e32 v83, 0xffff0000, v83
	v_and_b32_e32 v87, 0xffff0000, v87
	v_or_b32_sdwa v83, v83, v82 dst_sel:DWORD dst_unused:UNUSED_PAD src0_sel:DWORD src1_sel:WORD_1
	v_or_b32_sdwa v82, v87, v86 dst_sel:DWORD dst_unused:UNUSED_PAD src0_sel:DWORD src1_sel:WORD_1
	global_store_dwordx2 v[72:73], v[82:83], off offset:2048
	v_pk_mul_f32 v[82:83], v[78:79], v[78:79]
	s_nop 0
	v_pk_fma_f32 v[158:159], v[44:45], v[44:45], v[82:83]
	v_cvt_pk_f32_fp8_e32 v[82:83], v153
	v_cvt_pk_f32_fp8_sdwa v[166:167], v151 src0_sel:WORD_1
	v_cvt_pk_f32_fp8_sdwa v[86:87], v153 src0_sel:WORD_1
	v_cvt_pk_f32_fp8_e32 v[160:161], v151
	v_cvt_pk_f32_fp8_e32 v[174:175], v150
	v_cvt_pk_f32_fp8_e32 v[182:183], v149
	v_cvt_pk_f32_fp8_sdwa v[148:149], v149 src0_sel:WORD_1
	v_cvt_pk_f32_fp8_sdwa v[150:151], v150 src0_sel:WORD_1
	v_mov_b32_e32 v200, v82
	v_mov_b32_e32 v201, v166
	v_lshlrev_b32_e32 v191, 16, v39
	v_lshlrev_b32_e32 v190, 16, v38
	v_and_b32_e32 v197, 0xffff0000, v39
	v_and_b32_e32 v196, 0xffff0000, v38
	v_mov_b32_e32 v38, v160
	v_mov_b32_e32 v39, v86
	v_pk_mul_f32 v[200:201], v[200:201], v[66:67] op_sel:[0,1] op_sel_hi:[1,0]
	v_mov_b32_e32 v202, v174
	v_mov_b32_e32 v203, v148
	v_mov_b32_e32 v166, v83
	v_pk_fma_f32 v[38:39], v[38:39], v[66:67], v[200:201]
	v_mov_b32_e32 v200, v182
	v_mov_b32_e32 v201, v150
	v_pk_mul_f32 v[202:203], v[202:203], v[64:65] op_sel:[0,1] op_sel_hi:[1,0]
	v_mov_b32_e32 v86, v161
	v_pk_mul_f32 v[82:83], v[166:167], v[66:67] op_sel:[0,1] op_sel_hi:[1,0]
	v_mov_b32_e32 v148, v175
	v_pk_fma_f32 v[200:201], v[200:201], v[64:65], v[202:203]
	v_pk_fma_f32 v[82:83], v[86:87], v[66:67], v[82:83]
	v_mov_b32_e32 v150, v183
	v_pk_mul_f32 v[86:87], v[148:149], v[64:65] op_sel:[0,1] op_sel_hi:[1,0]
	v_pk_add_f32 v[38:39], v[38:39], v[200:201]
	v_pk_fma_f32 v[86:87], v[150:151], v[64:65], v[86:87]
	v_pk_add_f32 v[38:39], v[38:39], v[190:191]
	v_pk_add_f32 v[82:83], v[82:83], v[86:87]
	v_and_b32_sdwa v87, v38, v129 dst_sel:DWORD dst_unused:UNUSED_PAD src0_sel:WORD_1 src1_sel:DWORD
	v_pk_add_f32 v[82:83], v[82:83], v[196:197]
	v_add3_u32 v137, v38, v87, s4
	v_and_b32_sdwa v87, v83, v129 dst_sel:DWORD dst_unused:UNUSED_PAD src0_sel:WORD_1 src1_sel:DWORD
	v_and_b32_sdwa v138, v82, v129 dst_sel:DWORD dst_unused:UNUSED_PAD src0_sel:WORD_1 src1_sel:DWORD
	v_and_b32_sdwa v86, v39, v129 dst_sel:DWORD dst_unused:UNUSED_PAD src0_sel:WORD_1 src1_sel:DWORD
	v_add3_u32 v87, v83, v87, s4
	v_add3_u32 v138, v82, v138, s4
	v_add3_u32 v86, v39, v86, s4
	v_and_b32_e32 v87, 0xffff0000, v87
	v_and_b32_e32 v138, 0xffff0000, v138
	v_or_b32_sdwa v87, v87, v86 dst_sel:DWORD dst_unused:UNUSED_PAD src0_sel:DWORD src1_sel:WORD_1
	v_or_b32_sdwa v86, v138, v137 dst_sel:DWORD dst_unused:UNUSED_PAD src0_sel:DWORD src1_sel:WORD_1
	global_store_dwordx2 v[72:73], v[86:87], off offset:2560
	v_pk_mul_f32 v[86:87], v[82:83], v[82:83]
	s_nop 0
	v_pk_fma_f32 v[148:149], v[38:39], v[38:39], v[86:87]
	v_cvt_pk_f32_fp8_e32 v[86:87], v143
	v_cvt_pk_f32_fp8_sdwa v[166:167], v141 src0_sel:WORD_1
	v_cvt_pk_f32_fp8_sdwa v[150:151], v143 src0_sel:WORD_1
	v_cvt_pk_f32_fp8_e32 v[160:161], v141
	v_cvt_pk_f32_fp8_e32 v[174:175], v140
	v_cvt_pk_f32_fp8_e32 v[182:183], v139
	v_cvt_pk_f32_fp8_sdwa v[138:139], v139 src0_sel:WORD_1
	v_cvt_pk_f32_fp8_sdwa v[140:141], v140 src0_sel:WORD_1
	v_mov_b32_e32 v200, v86
	v_mov_b32_e32 v201, v166
	v_lshlrev_b32_e32 v191, 16, v35
	v_lshlrev_b32_e32 v190, 16, v34
	v_and_b32_e32 v197, 0xffff0000, v35
	v_and_b32_e32 v196, 0xffff0000, v34
	v_mov_b32_e32 v34, v160
	v_mov_b32_e32 v35, v150
	v_pk_mul_f32 v[200:201], v[200:201], v[66:67] op_sel:[0,1] op_sel_hi:[1,0]
	v_mov_b32_e32 v203, v138
	v_mov_b32_e32 v166, v87
	v_mov_b32_e32 v138, v175
	v_pk_fma_f32 v[34:35], v[34:35], v[66:67], v[200:201]
	v_mov_b32_e32 v201, v140
	v_mov_b32_e32 v202, v174
	v_mov_b32_e32 v150, v161
	v_pk_mul_f32 v[86:87], v[166:167], v[66:67] op_sel:[0,1] op_sel_hi:[1,0]
	v_mov_b32_e32 v140, v183
	v_pk_mul_f32 v[138:139], v[138:139], v[64:65] op_sel:[0,1] op_sel_hi:[1,0]
	v_mov_b32_e32 v200, v182
	v_pk_mul_f32 v[202:203], v[202:203], v[64:65] op_sel:[0,1] op_sel_hi:[1,0]
	v_pk_fma_f32 v[86:87], v[150:151], v[66:67], v[86:87]
	v_pk_fma_f32 v[138:139], v[140:141], v[64:65], v[138:139]
	v_pk_fma_f32 v[200:201], v[200:201], v[64:65], v[202:203]
	v_pk_add_f32 v[86:87], v[86:87], v[138:139]
	v_pk_add_f32 v[34:35], v[34:35], v[200:201]
	v_pk_add_f32 v[86:87], v[86:87], v[196:197]
	v_pk_add_f32 v[34:35], v[34:35], v[190:191]
	v_and_b32_sdwa v139, v87, v129 dst_sel:DWORD dst_unused:UNUSED_PAD src0_sel:WORD_1 src1_sel:DWORD
	v_and_b32_sdwa v140, v86, v129 dst_sel:DWORD dst_unused:UNUSED_PAD src0_sel:WORD_1 src1_sel:DWORD
	v_and_b32_sdwa v137, v35, v129 dst_sel:DWORD dst_unused:UNUSED_PAD src0_sel:WORD_1 src1_sel:DWORD
	v_and_b32_sdwa v138, v34, v129 dst_sel:DWORD dst_unused:UNUSED_PAD src0_sel:WORD_1 src1_sel:DWORD
	v_add3_u32 v139, v87, v139, s4
	v_add3_u32 v140, v86, v140, s4
	v_add3_u32 v138, v34, v138, s4
	v_add3_u32 v137, v35, v137, s4
	v_and_b32_e32 v139, 0xffff0000, v139
	v_and_b32_e32 v140, 0xffff0000, v140
	v_or_b32_sdwa v139, v139, v137 dst_sel:DWORD dst_unused:UNUSED_PAD src0_sel:DWORD src1_sel:WORD_1
	v_or_b32_sdwa v138, v140, v138 dst_sel:DWORD dst_unused:UNUSED_PAD src0_sel:DWORD src1_sel:WORD_1
	global_store_dwordx2 v[72:73], v[138:139], off offset:3072
	v_pk_mul_f32 v[138:139], v[86:87], v[86:87]
	s_nop 0
	v_pk_fma_f32 v[138:139], v[34:35], v[34:35], v[138:139]
	v_cvt_pk_f32_fp8_e32 v[140:141], v133
	v_cvt_pk_f32_fp8_sdwa v[166:167], v131 src0_sel:WORD_1
	v_cvt_pk_f32_fp8_sdwa v[150:151], v133 src0_sel:WORD_1
	v_cvt_pk_f32_fp8_e32 v[160:161], v131
	v_cvt_pk_f32_fp8_e32 v[174:175], v89
	v_cvt_pk_f32_fp8_sdwa v[182:183], v89 src0_sel:WORD_1
	v_cvt_pk_f32_fp8_e32 v[190:191], v88
	v_cvt_pk_f32_fp8_sdwa v[88:89], v88 src0_sel:WORD_1
	v_mov_b32_e32 v202, v140
	v_mov_b32_e32 v203, v166
	v_lshlrev_b32_e32 v197, 16, v29
	v_lshlrev_b32_e32 v196, 16, v28
	v_and_b32_e32 v201, 0xffff0000, v29
	v_and_b32_e32 v200, 0xffff0000, v28
	v_mov_b32_e32 v28, v160
	v_mov_b32_e32 v29, v150
	v_pk_mul_f32 v[202:203], v[202:203], v[66:67] op_sel:[0,1] op_sel_hi:[1,0]
	v_mov_b32_e32 v204, v174
	v_mov_b32_e32 v205, v88
	v_pk_fma_f32 v[28:29], v[28:29], v[66:67], v[202:203]
	v_mov_b32_e32 v202, v190
	v_mov_b32_e32 v203, v182
	v_pk_mul_f32 v[204:205], v[204:205], v[64:65] op_sel:[0,1] op_sel_hi:[1,0]
	v_mov_b32_e32 v166, v141
	v_mov_b32_e32 v88, v175
	v_pk_fma_f32 v[202:203], v[202:203], v[64:65], v[204:205]
	v_mov_b32_e32 v150, v161
	v_pk_mul_f32 v[140:141], v[166:167], v[66:67] op_sel:[0,1] op_sel_hi:[1,0]
	v_mov_b32_e32 v182, v191
	v_pk_mul_f32 v[88:89], v[88:89], v[64:65] op_sel:[0,1] op_sel_hi:[1,0]
	v_pk_add_f32 v[28:29], v[28:29], v[202:203]
	v_pk_fma_f32 v[66:67], v[150:151], v[66:67], v[140:141]
	v_pk_fma_f32 v[64:65], v[182:183], v[64:65], v[88:89]
	v_pk_add_f32 v[28:29], v[28:29], v[196:197]
	v_pk_add_f32 v[64:65], v[66:67], v[64:65]
	v_and_b32_sdwa v67, v28, v129 dst_sel:DWORD dst_unused:UNUSED_PAD src0_sel:WORD_1 src1_sel:DWORD
	v_pk_add_f32 v[64:65], v[64:65], v[200:201]
	v_add3_u32 v88, v28, v67, s4
	v_and_b32_sdwa v67, v65, v129 dst_sel:DWORD dst_unused:UNUSED_PAD src0_sel:WORD_1 src1_sel:DWORD
	v_and_b32_sdwa v89, v64, v129 dst_sel:DWORD dst_unused:UNUSED_PAD src0_sel:WORD_1 src1_sel:DWORD
	v_and_b32_sdwa v66, v29, v129 dst_sel:DWORD dst_unused:UNUSED_PAD src0_sel:WORD_1 src1_sel:DWORD
	v_add3_u32 v67, v65, v67, s4
	v_add3_u32 v89, v64, v89, s4
	v_add3_u32 v66, v29, v66, s4
	v_and_b32_e32 v67, 0xffff0000, v67
	v_and_b32_e32 v89, 0xffff0000, v89
	v_or_b32_sdwa v67, v67, v66 dst_sel:DWORD dst_unused:UNUSED_PAD src0_sel:DWORD src1_sel:WORD_1
	v_or_b32_sdwa v66, v89, v88 dst_sel:DWORD dst_unused:UNUSED_PAD src0_sel:DWORD src1_sel:WORD_1
	global_store_dwordx2 v[72:73], v[66:67], off offset:3584
	v_add_f32_e32 v72, v80, v81
	v_add_f32_e32 v73, v74, v75
	v_add_f32_e32 v72, v73, v72
	v_add_f32_e32 v73, v84, v85
	v_add_f32_e32 v72, v72, v73
	v_add_f32_e32 v48, v48, v49
	v_add_f32_e32 v48, v72, v48
	v_add_f32_e32 v49, v158, v159
	v_pk_mul_f32 v[66:67], v[64:65], v[64:65]
	v_add_f32_e32 v48, v48, v49
	v_add_f32_e32 v49, v148, v149
	v_pk_fma_f32 v[66:67], v[28:29], v[28:29], v[66:67]
	v_add_f32_e32 v48, v48, v49
	v_add_f32_e32 v49, v138, v139
	v_add_f32_e32 v48, v48, v49
	v_add_f32_e32 v49, v66, v67
	v_add_f32_e32 v48, v48, v49
	v_mov_b64_e32 v[72:73], v[212:213]
	v_mov_b64_e32 v[74:75], v[214:215]
	ds_bpermute_b32 v49, v1, v48
	s_waitcnt lgkmcnt(0)
	v_add_f32_e32 v48, v48, v49
	ds_bpermute_b32 v49, v90, v48
	s_waitcnt lgkmcnt(0)
	v_add_f32_e32 v48, v48, v49
	ds_bpermute_b32 v49, v91, v48
	s_waitcnt lgkmcnt(0)
	v_add_f32_e32 v48, v48, v49
	ds_bpermute_b32 v49, v92, v48
	s_waitcnt lgkmcnt(0)
	v_add_f32_e32 v48, v48, v49
	ds_bpermute_b32 v49, v93, v48
	s_waitcnt lgkmcnt(0)
	v_add_f32_e32 v48, v48, v49
	ds_bpermute_b32 v49, v94, v48
	s_waitcnt lgkmcnt(0)
	v_add_f32_e32 v48, v48, v49
	v_fmamk_f32 v48, v48, 0x3a000000, v127
	v_mul_f32_e32 v49, 0x4f800000, v48
	v_cmp_gt_f32_e32 vcc, s19, v48
	s_nop 1
	v_cndmask_b32_e32 v48, v48, v49, vcc
	v_sqrt_f32_e32 v49, v48
	s_nop 0
	v_add_u32_e32 v66, -1, v49
	v_add_u32_e32 v67, 1, v49
	v_fma_f32 v80, -v66, v49, v48
	v_fma_f32 v81, -v67, v49, v48
	v_cmp_ge_f32_e64 s[8:9], 0, v80
	s_nop 1
	v_cndmask_b32_e64 v49, v49, v66, s[8:9]
	v_cmp_lt_f32_e64 s[8:9], 0, v81
	s_nop 1
	v_cndmask_b32_e64 v49, v49, v67, s[8:9]
	v_mul_f32_e32 v66, 0x37800000, v49
	v_cndmask_b32_e32 v49, v49, v66, vcc
	v_cmp_class_f32_e32 vcc, v48, v128
	v_mov_b32_e32 v67, 0
	s_nop 0
	v_cndmask_b32_e32 v48, v49, v48, vcc
	v_div_scale_f32 v49, s[0:1], v48, v48, 1.0
	v_rcp_f32_e32 v66, v49
	v_div_scale_f32 v80, vcc, 1.0, v48, 1.0
	v_fma_f32 v81, -v49, v66, 1.0
	v_fmac_f32_e32 v66, v81, v66
	v_mul_f32_e32 v81, v80, v66
	v_fma_f32 v84, -v49, v81, v80
	v_fmac_f32_e32 v81, v84, v66
	v_fma_f32 v49, -v49, v81, v80
	v_div_fmas_f32 v49, v49, v66, v81
	v_div_fixup_f32 v66, v49, v48, 1.0
	v_mul_f32_e32 v24, v66, v24
	v_mul_f32_e32 v48, v66, v50

	v_mul_f32_e32 v24, v72, v24
	v_mul_f32_e32 v48, v73, v48
	v_cvt_pk_fp8_f32 v67, v24, v48
	v_mul_f32_e32 v25, v66, v25
	v_mul_f32_e32 v24, v66, v51
	v_mul_f32_e32 v25, v74, v25
	v_mul_f32_e32 v24, v75, v24
	v_cvt_pk_fp8_f32 v67, v25, v24 op_sel:[0,0,1]
	v_add_co_u32_e32 v24, vcc, s41, v22
	v_mul_f32_e32 v58, v66, v58
	s_nop 0
	v_addc_co_u32_e32 v25, vcc, 0, v23, vcc
	global_store_dword v[24:25], v67, off offset:-4096
	v_mov_b64_e32 v[48:49], v[216:217]
	v_mov_b64_e32 v[50:51], v[218:219]
	v_mul_f32_e32 v62, v66, v62
	v_mov_b32_e32 v67, 0
	v_mul_f32_e32 v59, v66, v59
	v_mul_f32_e32 v45, v66, v45
	v_mul_f32_e32 v39, v66, v39
	v_mul_f32_e32 v35, v66, v35
	v_mul_f32_e32 v28, v66, v28
	v_mul_f32_e32 v29, v66, v29
	s_waitcnt vmcnt(17)
	v_cvt_pk_f32_fp8_sdwa v[80:81], v194 src0_sel:WORD_1

	v_mul_f32_e32 v48, v48, v58
	v_mul_f32_e32 v49, v49, v62
	v_cvt_pk_fp8_f32 v67, v48, v49
	v_mul_f32_e32 v48, v66, v63
	v_mul_f32_e32 v49, v50, v59
	v_mul_f32_e32 v48, v51, v48
	v_cvt_pk_fp8_f32 v67, v49, v48 op_sel:[0,0,1]
	v_add_co_u32_e32 v48, vcc, s36, v22
	v_mul_f32_e32 v50, v66, v68
	s_nop 0
	v_addc_co_u32_e32 v49, vcc, 0, v23, vcc
	global_store_dword v[48:49], v67, off offset:256
	v_mov_b64_e32 v[72:73], v[220:221]
	v_mov_b64_e32 v[74:75], v[222:223]
	v_mul_f32_e32 v23, v66, v52
	v_mov_b32_e32 v22, 0
	v_mul_f32_e32 v51, v66, v53
	v_mul_f32_e32 v58, v66, v76
	v_mul_f32_e32 v59, v66, v71
	ds_bpermute_b32 v67, v116, v19
	v_cvt_pk_f32_fp8_e32 v[62:63], v188
	v_mov_b32_e32 v84, v62

	v_mul_f32_e32 v23, v72, v23
	v_mul_f32_e32 v50, v73, v50
	v_cvt_pk_fp8_f32 v22, v23, v50
	v_mul_f32_e32 v23, v66, v69
	v_mul_f32_e32 v50, v74, v51
	v_mul_f32_e32 v23, v75, v23
	v_cvt_pk_fp8_f32 v22, v50, v23 op_sel:[0,0,1]
	v_mul_f32_e32 v23, v66, v70
	v_cvt_pk_f32_fp8_sdwa v[72:73], v189 src0_sel:WORD_1
	v_cvt_pk_f32_fp8_sdwa v[68:69], v188 src0_sel:WORD_1
	global_store_dword v[48:49], v22, off offset:512
	v_mov_b64_e32 v[50:51], v[224:225]
	v_mov_b64_e32 v[52:53], v[226:227]
	v_mov_b32_e32 v22, 0
	v_cvt_pk_f32_fp8_e32 v[70:71], v189
	v_cvt_pk_f32_fp8_e32 v[74:75], v192
	v_mov_b32_e32 v85, v72
	v_mov_b32_e32 v72, v63

	v_mul_f32_e32 v23, v50, v23
	v_mul_f32_e32 v50, v51, v58
	v_cvt_pk_fp8_f32 v22, v23, v50
	v_mul_f32_e32 v23, v66, v77
	v_mul_f32_e32 v50, v52, v59
	v_mul_f32_e32 v23, v53, v23
	v_cvt_pk_fp8_f32 v22, v50, v23 op_sel:[0,0,1]
	v_mul_f32_e32 v23, v66, v44
	v_mul_f32_e32 v44, v66, v78
	v_mul_f32_e32 v59, v66, v64
	global_store_dword v[48:49], v22, off offset:768
	v_mov_b64_e32 v[50:51], v[228:229]
	v_mov_b64_e32 v[52:53], v[230:231]
	v_mov_b32_e32 v22, 0
	v_mov_b32_e32 v58, 0
	ds_bpermute_b32 v64, v119, v19
	v_cvt_pk_f32_fp8_sdwa v[76:77], v192 src0_sel:WORD_1

	v_mul_f32_e32 v23, v50, v23
	v_mul_f32_e32 v44, v51, v44
	v_cvt_pk_fp8_f32 v22, v23, v44
	v_mul_f32_e32 v23, v66, v79
	v_mul_f32_e32 v44, v52, v45
	v_mul_f32_e32 v23, v53, v23
	v_cvt_pk_fp8_f32 v22, v44, v23 op_sel:[0,0,1]
	v_mul_f32_e32 v23, v66, v38
	v_mul_f32_e32 v38, v66, v82
	ds_bpermute_b32 v44, v123, v130
	global_store_dword v[48:49], v22, off offset:1024
	v_mov_b64_e32 v[50:51], v[232:233]
	v_mov_b64_e32 v[52:53], v[234:235]
	v_mov_b32_e32 v22, 0
	v_cvt_pk_f32_fp8_e32 v[78:79], v194
	s_waitcnt lgkmcnt(0)
	v_ashrrev_i32_e32 v45, 31, v44
	v_lshlrev_b64 v[44:45], 11, v[44:45]
	v_mov_b32_e32 v82, v70

	v_mul_f32_e32 v23, v50, v23
	v_mul_f32_e32 v38, v51, v38
	v_cvt_pk_fp8_f32 v22, v23, v38
	v_mul_f32_e32 v23, v66, v83
	v_mul_f32_e32 v38, v52, v39
	v_mul_f32_e32 v23, v53, v23
	v_cvt_pk_fp8_f32 v22, v38, v23 op_sel:[0,0,1]
	v_mul_f32_e32 v23, v66, v34
	v_mul_f32_e32 v34, v66, v86
	ds_bpermute_b32 v38, v122, v130
	global_store_dword v[48:49], v22, off offset:1280
	v_mov_b64_e32 v[50:51], v[236:237]
	v_mov_b64_e32 v[52:53], v[238:239]
	v_mov_b32_e32 v22, 0
	v_mov_b32_e32 v83, v68
	s_waitcnt lgkmcnt(0)
	v_ashrrev_i32_e32 v39, 31, v38
	v_lshlrev_b64 v[38:39], 11, v[38:39]
	v_mov_b32_e32 v86, v74
	v_mov_b32_e32 v68, v71

	v_mul_f32_e32 v23, v50, v23
	v_mul_f32_e32 v34, v51, v34
	v_cvt_pk_fp8_f32 v22, v23, v34
	v_mul_f32_e32 v23, v66, v87
	v_mul_f32_e32 v34, v52, v35
	v_mul_f32_e32 v23, v53, v23
	v_cvt_pk_fp8_f32 v22, v34, v23 op_sel:[0,0,1]
	ds_bpermute_b32 v34, v121, v130
	v_mov_b32_e32 v87, v80
	v_mov_b32_e32 v80, v75
	global_store_dword v[48:49], v22, off offset:1536
	v_mov_b64_e32 v[50:51], v[240:241]
	v_mov_b64_e32 v[52:53], v[242:243]
	ds_bpermute_b32 v22, v120, v130
	s_waitcnt lgkmcnt(1)
	v_ashrrev_i32_e32 v35, 31, v34
	v_lshlrev_b64 v[34:35], 11, v[34:35]
	s_waitcnt lgkmcnt(0)
	v_ashrrev_i32_e32 v23, 31, v22
	v_lshlrev_b64 v[22:23], 11, v[22:23]
	v_lshl_add_u64 v[22:23], v[4:5], 0, v[22:23]

	v_mul_f32_e32 v28, v50, v28
	v_mul_f32_e32 v50, v51, v59
	v_cvt_pk_fp8_f32 v58, v28, v50
	v_mul_f32_e32 v28, v66, v65
	v_mul_f32_e32 v29, v52, v29
	v_mul_f32_e32 v28, v53, v28
	v_cvt_pk_fp8_f32 v58, v29, v28 op_sel:[0,0,1]
	v_lshl_add_u64 v[28:29], v[4:5], 0, v[34:35]
	v_lshl_add_u64 v[34:35], v[4:5], 0, v[38:39]
	v_lshl_add_u64 v[38:39], v[4:5], 0, v[44:45]
	global_store_dword v[48:49], v58, off offset:1792
	global_load_dword v183, v[22:23], off nt
	global_load_dword v175, v[22:23], off offset:256 nt
	global_load_dword v167, v[22:23], off offset:512 nt
	global_load_dword v159, v[22:23], off offset:768 nt
	global_load_dword v150, v[22:23], off offset:1024 nt
	global_load_dword v141, v[22:23], off offset:1280 nt
	global_load_dword v137, v[22:23], off offset:1536 nt
	global_load_dword v88, v[22:23], off offset:1792 nt
	global_load_dword v184, v[28:29], off nt
	global_load_dword v176, v[28:29], off offset:256 nt
	global_load_dword v168, v[28:29], off offset:512 nt
	global_load_dword v160, v[28:29], off offset:768 nt
	global_load_dword v151, v[28:29], off offset:1024 nt
	global_load_dword v143, v[28:29], off offset:1280 nt
	global_load_dword v138, v[28:29], off offset:1536 nt
	global_load_dword v89, v[28:29], off offset:1792 nt
	global_load_dword v186, v[34:35], off nt
	global_load_dword v178, v[34:35], off offset:256 nt
	global_load_dword v170, v[34:35], off offset:512 nt
	global_load_dword v161, v[34:35], off offset:768 nt
	global_load_dword v153, v[34:35], off offset:1024 nt
	global_load_dword v148, v[34:35], off offset:1280 nt
	global_load_dword v139, v[34:35], off offset:1536 nt
	global_load_dword v131, v[34:35], off offset:1792 nt
	global_load_dword v190, v[38:39], off nt
	global_load_dword v182, v[38:39], off offset:256 nt
	global_load_dword v174, v[38:39], off offset:512 nt
	global_load_dword v166, v[38:39], off offset:768 nt
	global_load_dword v158, v[38:39], off offset:1024 nt
	global_load_dword v149, v[38:39], off offset:1280 nt
	global_load_dword v140, v[38:39], off offset:1536 nt
	global_load_dword v133, v[38:39], off offset:1792 nt
	global_load_dwordx2 v[22:23], v[56:57], off offset:3584 nt
	global_load_dwordx2 v[28:29], v[56:57], off offset:3072 nt
	global_load_dwordx2 v[34:35], v[56:57], off offset:2560 nt
	s_nop 0
	global_load_dwordx2 v[38:39], v[56:57], off offset:2048 nt
	global_load_dwordx2 v[44:45], v[56:57], off offset:1536 nt
	global_load_dwordx2 v[50:51], v[56:57], off offset:1024 nt
	global_load_dwordx2 v[52:53], v[56:57], off offset:512 nt
	s_nop 0
	global_load_dwordx2 v[56:57], v[56:57], off nt
	ds_bpermute_b32 v66, v117, v19
	ds_bpermute_b32 v65, v118, v19
	s_waitcnt vmcnt(63)
	v_lshlrev_b32_e32 v59, 16, v61
	v_lshlrev_b32_e32 v58, 16, v60
	v_and_b32_e32 v61, 0xffff0000, v61
	s_waitcnt lgkmcnt(1)
	v_pk_mul_f32 v[84:85], v[84:85], v[66:67] op_sel:[0,1] op_sel_hi:[1,0]
	s_waitcnt lgkmcnt(0)
	v_pk_mul_f32 v[86:87], v[86:87], v[64:65] op_sel:[0,1] op_sel_hi:[1,0]
	v_pk_fma_f32 v[82:83], v[82:83], v[66:67], v[84:85]
	v_mov_b32_e32 v84, v78
	v_mov_b32_e32 v85, v76
	v_pk_mul_f32 v[62:63], v[72:73], v[66:67] op_sel:[0,1] op_sel_hi:[1,0]
	v_pk_fma_f32 v[84:85], v[84:85], v[64:65], v[86:87]
	v_pk_fma_f32 v[62:63], v[68:69], v[66:67], v[62:63]
	v_mov_b32_e32 v76, v79
	v_pk_mul_f32 v[68:69], v[80:81], v[64:65] op_sel:[0,1] op_sel_hi:[1,0]
	v_pk_add_f32 v[82:83], v[82:83], v[84:85]
	v_pk_fma_f32 v[68:69], v[76:77], v[64:65], v[68:69]
	v_and_b32_e32 v60, 0xffff0000, v60
	v_pk_add_f32 v[58:59], v[82:83], v[58:59]
	v_pk_add_f32 v[62:63], v[62:63], v[68:69]
	s_nop 0
	v_pk_add_f32 v[60:61], v[62:63], v[60:61]
	v_and_b32_sdwa v63, v58, v129 dst_sel:DWORD dst_unused:UNUSED_PAD src0_sel:WORD_1 src1_sel:DWORD
	v_add3_u32 v68, v58, v63, s4
	v_and_b32_sdwa v63, v61, v129 dst_sel:DWORD dst_unused:UNUSED_PAD src0_sel:WORD_1 src1_sel:DWORD
	v_and_b32_sdwa v69, v60, v129 dst_sel:DWORD dst_unused:UNUSED_PAD src0_sel:WORD_1 src1_sel:DWORD
	v_and_b32_sdwa v62, v59, v129 dst_sel:DWORD dst_unused:UNUSED_PAD src0_sel:WORD_1 src1_sel:DWORD
	v_add3_u32 v63, v61, v63, s4
	v_add3_u32 v69, v60, v69, s4
	v_add3_u32 v62, v59, v62, s4
	v_and_b32_e32 v63, 0xffff0000, v63
	v_and_b32_e32 v69, 0xffff0000, v69
	v_or_b32_sdwa v63, v63, v62 dst_sel:DWORD dst_unused:UNUSED_PAD src0_sel:DWORD src1_sel:WORD_1
	v_or_b32_sdwa v62, v69, v68 dst_sel:DWORD dst_unused:UNUSED_PAD src0_sel:DWORD src1_sel:WORD_1
	global_store_dwordx2 v[30:31], v[62:63], off
	v_pk_mul_f32 v[62:63], v[60:61], v[60:61]
	s_nop 0
	v_pk_fma_f32 v[70:71], v[58:59], v[58:59], v[62:63]
	v_cvt_pk_f32_fp8_e32 v[62:63], v180
	v_cvt_pk_f32_fp8_sdwa v[74:75], v181 src0_sel:WORD_1
	v_cvt_pk_f32_fp8_sdwa v[68:69], v180 src0_sel:WORD_1
	v_cvt_pk_f32_fp8_e32 v[72:73], v181
	v_cvt_pk_f32_fp8_e32 v[76:77], v185
	s_waitcnt vmcnt(63)
	v_cvt_pk_f32_fp8_sdwa v[82:83], v187 src0_sel:WORD_1
	v_cvt_pk_f32_fp8_sdwa v[78:79], v185 src0_sel:WORD_1
	v_cvt_pk_f32_fp8_e32 v[80:81], v187
	v_mov_b32_e32 v180, v62
	v_mov_b32_e32 v181, v74
	v_lshlrev_b32_e32 v85, 16, v55
	v_lshlrev_b32_e32 v84, 16, v54
	v_and_b32_e32 v87, 0xffff0000, v55
	v_and_b32_e32 v86, 0xffff0000, v54
	v_mov_b32_e32 v54, v72
	v_mov_b32_e32 v55, v68
	v_pk_mul_f32 v[180:181], v[180:181], v[66:67] op_sel:[0,1] op_sel_hi:[1,0]
	v_mov_b32_e32 v188, v76
	v_mov_b32_e32 v189, v82
	v_mov_b32_e32 v74, v63
	v_pk_fma_f32 v[54:55], v[54:55], v[66:67], v[180:181]
	v_mov_b32_e32 v180, v80
	v_mov_b32_e32 v181, v78
	v_pk_mul_f32 v[188:189], v[188:189], v[64:65] op_sel:[0,1] op_sel_hi:[1,0]
	v_mov_b32_e32 v68, v73
	v_pk_mul_f32 v[62:63], v[74:75], v[66:67] op_sel:[0,1] op_sel_hi:[1,0]
	v_mov_b32_e32 v82, v77
	v_pk_fma_f32 v[180:181], v[180:181], v[64:65], v[188:189]
	v_pk_fma_f32 v[62:63], v[68:69], v[66:67], v[62:63]
	v_mov_b32_e32 v78, v81
	v_pk_mul_f32 v[68:69], v[82:83], v[64:65] op_sel:[0,1] op_sel_hi:[1,0]
	v_pk_add_f32 v[54:55], v[54:55], v[180:181]
	v_pk_fma_f32 v[68:69], v[78:79], v[64:65], v[68:69]
	v_pk_add_f32 v[54:55], v[54:55], v[84:85]
	v_pk_add_f32 v[62:63], v[62:63], v[68:69]
	v_and_b32_sdwa v69, v54, v129 dst_sel:DWORD dst_unused:UNUSED_PAD src0_sel:WORD_1 src1_sel:DWORD
	v_pk_add_f32 v[62:63], v[62:63], v[86:87]
	v_add3_u32 v72, v54, v69, s4
	v_and_b32_sdwa v69, v63, v129 dst_sel:DWORD dst_unused:UNUSED_PAD src0_sel:WORD_1 src1_sel:DWORD
	v_and_b32_sdwa v73, v62, v129 dst_sel:DWORD dst_unused:UNUSED_PAD src0_sel:WORD_1 src1_sel:DWORD
	v_and_b32_sdwa v68, v55, v129 dst_sel:DWORD dst_unused:UNUSED_PAD src0_sel:WORD_1 src1_sel:DWORD
	v_add3_u32 v69, v63, v69, s4
	v_add3_u32 v73, v62, v73, s4
	v_add3_u32 v68, v55, v68, s4
	v_and_b32_e32 v69, 0xffff0000, v69
	v_and_b32_e32 v73, 0xffff0000, v73
	v_or_b32_sdwa v69, v69, v68 dst_sel:DWORD dst_unused:UNUSED_PAD src0_sel:DWORD src1_sel:WORD_1
	v_or_b32_sdwa v68, v73, v72 dst_sel:DWORD dst_unused:UNUSED_PAD src0_sel:DWORD src1_sel:WORD_1
	global_store_dwordx2 v[30:31], v[68:69], off offset:512
	v_pk_mul_f32 v[68:69], v[62:63], v[62:63]
	s_nop 0
	v_pk_fma_f32 v[76:77], v[54:55], v[54:55], v[68:69]
	v_cvt_pk_f32_fp8_e32 v[68:69], v172
	v_cvt_pk_f32_fp8_sdwa v[78:79], v173 src0_sel:WORD_1
	v_cvt_pk_f32_fp8_sdwa v[72:73], v172 src0_sel:WORD_1
	v_cvt_pk_f32_fp8_e32 v[74:75], v173
	v_cvt_pk_f32_fp8_e32 v[80:81], v177
	s_waitcnt vmcnt(63)
	v_cvt_pk_f32_fp8_sdwa v[86:87], v179 src0_sel:WORD_1
	v_cvt_pk_f32_fp8_sdwa v[82:83], v177 src0_sel:WORD_1
	v_cvt_pk_f32_fp8_e32 v[84:85], v179
	v_mov_b32_e32 v188, v68
	v_mov_b32_e32 v189, v78
	v_lshlrev_b32_e32 v173, 16, v47
	v_lshlrev_b32_e32 v172, 16, v46
	v_and_b32_e32 v181, 0xffff0000, v47
	v_and_b32_e32 v180, 0xffff0000, v46
	v_mov_b32_e32 v46, v74
	v_mov_b32_e32 v47, v72
	v_pk_mul_f32 v[188:189], v[188:189], v[66:67] op_sel:[0,1] op_sel_hi:[1,0]
	v_mov_b32_e32 v192, v80
	v_mov_b32_e32 v193, v86
	v_mov_b32_e32 v78, v69
	v_pk_fma_f32 v[46:47], v[46:47], v[66:67], v[188:189]
	v_mov_b32_e32 v188, v84
	v_mov_b32_e32 v189, v82
	v_pk_mul_f32 v[192:193], v[192:193], v[64:65] op_sel:[0,1] op_sel_hi:[1,0]
	v_mov_b32_e32 v72, v75
	v_pk_mul_f32 v[68:69], v[78:79], v[66:67] op_sel:[0,1] op_sel_hi:[1,0]
	v_mov_b32_e32 v86, v81
	v_pk_fma_f32 v[188:189], v[188:189], v[64:65], v[192:193]
	v_pk_fma_f32 v[68:69], v[72:73], v[66:67], v[68:69]
	v_mov_b32_e32 v82, v85
	v_pk_mul_f32 v[72:73], v[86:87], v[64:65] op_sel:[0,1] op_sel_hi:[1,0]
	v_pk_add_f32 v[46:47], v[46:47], v[188:189]
	v_pk_fma_f32 v[72:73], v[82:83], v[64:65], v[72:73]
	v_pk_add_f32 v[46:47], v[46:47], v[172:173]
	v_pk_add_f32 v[68:69], v[68:69], v[72:73]
	v_and_b32_sdwa v73, v46, v129 dst_sel:DWORD dst_unused:UNUSED_PAD src0_sel:WORD_1 src1_sel:DWORD
	v_pk_add_f32 v[68:69], v[68:69], v[180:181]
	v_add3_u32 v74, v46, v73, s4
	v_and_b32_sdwa v73, v69, v129 dst_sel:DWORD dst_unused:UNUSED_PAD src0_sel:WORD_1 src1_sel:DWORD
	v_and_b32_sdwa v75, v68, v129 dst_sel:DWORD dst_unused:UNUSED_PAD src0_sel:WORD_1 src1_sel:DWORD
	v_and_b32_sdwa v72, v47, v129 dst_sel:DWORD dst_unused:UNUSED_PAD src0_sel:WORD_1 src1_sel:DWORD
	v_add3_u32 v73, v69, v73, s4
	v_add3_u32 v75, v68, v75, s4
	v_add3_u32 v72, v47, v72, s4
	v_and_b32_e32 v73, 0xffff0000, v73
	v_and_b32_e32 v75, 0xffff0000, v75
	v_or_b32_sdwa v73, v73, v72 dst_sel:DWORD dst_unused:UNUSED_PAD src0_sel:DWORD src1_sel:WORD_1
	v_or_b32_sdwa v72, v75, v74 dst_sel:DWORD dst_unused:UNUSED_PAD src0_sel:DWORD src1_sel:WORD_1
	global_store_dwordx2 v[30:31], v[72:73], off offset:1024
	v_pk_mul_f32 v[72:73], v[68:69], v[68:69]
	s_nop 0
	v_pk_fma_f32 v[80:81], v[46:47], v[46:47], v[72:73]
	v_cvt_pk_f32_fp8_e32 v[72:73], v164
	v_cvt_pk_f32_fp8_sdwa v[82:83], v165 src0_sel:WORD_1
	v_cvt_pk_f32_fp8_sdwa v[74:75], v164 src0_sel:WORD_1
	v_cvt_pk_f32_fp8_e32 v[78:79], v165
	v_cvt_pk_f32_fp8_e32 v[84:85], v169
	s_waitcnt vmcnt(63)
	v_cvt_pk_f32_fp8_sdwa v[172:173], v171 src0_sel:WORD_1
	v_cvt_pk_f32_fp8_sdwa v[86:87], v169 src0_sel:WORD_1
	v_cvt_pk_f32_fp8_e32 v[164:165], v171
	v_mov_b32_e32 v192, v72
	v_mov_b32_e32 v193, v82
	v_lshlrev_b32_e32 v181, 16, v43
	v_lshlrev_b32_e32 v180, 16, v42
	v_and_b32_e32 v189, 0xffff0000, v43
	v_and_b32_e32 v188, 0xffff0000, v42
	v_mov_b32_e32 v42, v78
	v_mov_b32_e32 v43, v74
	v_pk_mul_f32 v[192:193], v[192:193], v[66:67] op_sel:[0,1] op_sel_hi:[1,0]
	v_mov_b32_e32 v194, v84
	v_mov_b32_e32 v195, v172
	v_mov_b32_e32 v82, v73
	v_pk_fma_f32 v[42:43], v[42:43], v[66:67], v[192:193]
	v_mov_b32_e32 v192, v164
	v_mov_b32_e32 v193, v86
	v_pk_mul_f32 v[194:195], v[194:195], v[64:65] op_sel:[0,1] op_sel_hi:[1,0]
	v_mov_b32_e32 v74, v79
	v_pk_mul_f32 v[72:73], v[82:83], v[66:67] op_sel:[0,1] op_sel_hi:[1,0]
	v_mov_b32_e32 v172, v85
	v_pk_fma_f32 v[192:193], v[192:193], v[64:65], v[194:195]
	v_pk_fma_f32 v[72:73], v[74:75], v[66:67], v[72:73]
	v_mov_b32_e32 v86, v165
	v_pk_mul_f32 v[74:75], v[172:173], v[64:65] op_sel:[0,1] op_sel_hi:[1,0]
	v_pk_add_f32 v[42:43], v[42:43], v[192:193]
	v_pk_fma_f32 v[74:75], v[86:87], v[64:65], v[74:75]
	v_pk_add_f32 v[42:43], v[42:43], v[180:181]
	v_pk_add_f32 v[72:73], v[72:73], v[74:75]
	v_and_b32_sdwa v75, v42, v129 dst_sel:DWORD dst_unused:UNUSED_PAD src0_sel:WORD_1 src1_sel:DWORD
	v_pk_add_f32 v[72:73], v[72:73], v[188:189]
	v_add3_u32 v78, v42, v75, s4
	v_and_b32_sdwa v75, v73, v129 dst_sel:DWORD dst_unused:UNUSED_PAD src0_sel:WORD_1 src1_sel:DWORD
	v_and_b32_sdwa v79, v72, v129 dst_sel:DWORD dst_unused:UNUSED_PAD src0_sel:WORD_1 src1_sel:DWORD
	v_and_b32_sdwa v74, v43, v129 dst_sel:DWORD dst_unused:UNUSED_PAD src0_sel:WORD_1 src1_sel:DWORD
	v_add3_u32 v75, v73, v75, s4
	v_add3_u32 v79, v72, v79, s4
	v_add3_u32 v74, v43, v74, s4
	v_and_b32_e32 v75, 0xffff0000, v75
	v_and_b32_e32 v79, 0xffff0000, v79
	v_or_b32_sdwa v75, v75, v74 dst_sel:DWORD dst_unused:UNUSED_PAD src0_sel:DWORD src1_sel:WORD_1
	v_or_b32_sdwa v74, v79, v78 dst_sel:DWORD dst_unused:UNUSED_PAD src0_sel:DWORD src1_sel:WORD_1
	global_store_dwordx2 v[30:31], v[74:75], off offset:1536
	v_pk_mul_f32 v[74:75], v[72:73], v[72:73]
	s_nop 0
	v_pk_fma_f32 v[86:87], v[42:43], v[42:43], v[74:75]
	v_cvt_pk_f32_fp8_e32 v[74:75], v156
	v_cvt_pk_f32_fp8_sdwa v[84:85], v157 src0_sel:WORD_1
	v_cvt_pk_f32_fp8_sdwa v[78:79], v156 src0_sel:WORD_1
	v_cvt_pk_f32_fp8_e32 v[82:83], v157
	v_cvt_pk_f32_fp8_e32 v[156:157], v162
	v_cvt_pk_f32_fp8_sdwa v[164:165], v162 src0_sel:WORD_1
	s_waitcnt vmcnt(63)
	v_cvt_pk_f32_fp8_e32 v[172:173], v163
	v_cvt_pk_f32_fp8_sdwa v[162:163], v163 src0_sel:WORD_1
	v_mov_b32_e32 v192, v74
	v_mov_b32_e32 v193, v84
	v_lshlrev_b32_e32 v181, 16, v41
	v_lshlrev_b32_e32 v180, 16, v40
	v_and_b32_e32 v189, 0xffff0000, v41
	v_and_b32_e32 v188, 0xffff0000, v40
	v_mov_b32_e32 v40, v82
	v_mov_b32_e32 v41, v78
	v_pk_mul_f32 v[192:193], v[192:193], v[66:67] op_sel:[0,1] op_sel_hi:[1,0]
	v_mov_b32_e32 v194, v156
	v_mov_b32_e32 v195, v162
	v_mov_b32_e32 v84, v75
	v_pk_fma_f32 v[40:41], v[40:41], v[66:67], v[192:193]
	v_mov_b32_e32 v192, v172
	v_mov_b32_e32 v193, v164
	v_pk_mul_f32 v[194:195], v[194:195], v[64:65] op_sel:[0,1] op_sel_hi:[1,0]
	v_mov_b32_e32 v78, v83
	v_pk_mul_f32 v[74:75], v[84:85], v[66:67] op_sel:[0,1] op_sel_hi:[1,0]
	v_mov_b32_e32 v162, v157
	v_pk_fma_f32 v[192:193], v[192:193], v[64:65], v[194:195]
	v_pk_fma_f32 v[74:75], v[78:79], v[66:67], v[74:75]
	v_mov_b32_e32 v164, v173
	v_pk_mul_f32 v[78:79], v[162:163], v[64:65] op_sel:[0,1] op_sel_hi:[1,0]
	v_pk_add_f32 v[40:41], v[40:41], v[192:193]
	v_pk_fma_f32 v[78:79], v[164:165], v[64:65], v[78:79]
	v_pk_add_f32 v[40:41], v[40:41], v[180:181]
	v_pk_add_f32 v[74:75], v[74:75], v[78:79]
	v_and_b32_sdwa v79, v40, v129 dst_sel:DWORD dst_unused:UNUSED_PAD src0_sel:WORD_1 src1_sel:DWORD
	v_pk_add_f32 v[74:75], v[74:75], v[188:189]
	v_add3_u32 v82, v40, v79, s4
	v_and_b32_sdwa v79, v75, v129 dst_sel:DWORD dst_unused:UNUSED_PAD src0_sel:WORD_1 src1_sel:DWORD
	v_and_b32_sdwa v83, v74, v129 dst_sel:DWORD dst_unused:UNUSED_PAD src0_sel:WORD_1 src1_sel:DWORD
	v_and_b32_sdwa v78, v41, v129 dst_sel:DWORD dst_unused:UNUSED_PAD src0_sel:WORD_1 src1_sel:DWORD
	v_add3_u32 v79, v75, v79, s4
	v_add3_u32 v83, v74, v83, s4
	v_add3_u32 v78, v41, v78, s4
	v_and_b32_e32 v79, 0xffff0000, v79
	v_and_b32_e32 v83, 0xffff0000, v83
	v_or_b32_sdwa v79, v79, v78 dst_sel:DWORD dst_unused:UNUSED_PAD src0_sel:DWORD src1_sel:WORD_1
	v_or_b32_sdwa v78, v83, v82 dst_sel:DWORD dst_unused:UNUSED_PAD src0_sel:DWORD src1_sel:WORD_1
	global_store_dwordx2 v[30:31], v[78:79], off offset:2048
	v_pk_mul_f32 v[78:79], v[74:75], v[74:75]
	s_nop 0
	v_pk_fma_f32 v[156:157], v[40:41], v[40:41], v[78:79]
	v_cvt_pk_f32_fp8_e32 v[78:79], v147
	v_cvt_pk_f32_fp8_sdwa v[162:163], v152 src0_sel:WORD_1
	v_cvt_pk_f32_fp8_sdwa v[82:83], v147 src0_sel:WORD_1
	v_cvt_pk_f32_fp8_e32 v[84:85], v152
	v_cvt_pk_f32_fp8_e32 v[164:165], v154
	v_cvt_pk_f32_fp8_sdwa v[172:173], v154 src0_sel:WORD_1
	s_waitcnt vmcnt(63)
	v_cvt_pk_f32_fp8_e32 v[180:181], v155
	v_cvt_pk_f32_fp8_sdwa v[154:155], v155 src0_sel:WORD_1
	v_mov_b32_e32 v194, v78
	v_mov_b32_e32 v195, v162
	v_lshlrev_b32_e32 v189, 16, v37
	v_lshlrev_b32_e32 v188, 16, v36
	v_and_b32_e32 v193, 0xffff0000, v37
	v_and_b32_e32 v192, 0xffff0000, v36
	v_mov_b32_e32 v36, v84
	v_mov_b32_e32 v37, v82
	v_pk_mul_f32 v[194:195], v[194:195], v[66:67] op_sel:[0,1] op_sel_hi:[1,0]
	v_mov_b32_e32 v196, v164
	v_mov_b32_e32 v197, v154
	v_mov_b32_e32 v162, v79
	v_pk_fma_f32 v[36:37], v[36:37], v[66:67], v[194:195]
	v_mov_b32_e32 v194, v180
	v_mov_b32_e32 v195, v172
	v_pk_mul_f32 v[196:197], v[196:197], v[64:65] op_sel:[0,1] op_sel_hi:[1,0]
	v_mov_b32_e32 v82, v85
	v_pk_mul_f32 v[78:79], v[162:163], v[66:67] op_sel:[0,1] op_sel_hi:[1,0]
	v_mov_b32_e32 v154, v165
	v_pk_fma_f32 v[194:195], v[194:195], v[64:65], v[196:197]
	v_pk_fma_f32 v[78:79], v[82:83], v[66:67], v[78:79]
	v_mov_b32_e32 v172, v181
	v_pk_mul_f32 v[82:83], v[154:155], v[64:65] op_sel:[0,1] op_sel_hi:[1,0]
	v_pk_add_f32 v[36:37], v[36:37], v[194:195]
	v_pk_fma_f32 v[82:83], v[172:173], v[64:65], v[82:83]
	v_pk_add_f32 v[36:37], v[36:37], v[188:189]
	v_pk_add_f32 v[78:79], v[78:79], v[82:83]
	v_and_b32_sdwa v83, v36, v129 dst_sel:DWORD dst_unused:UNUSED_PAD src0_sel:WORD_1 src1_sel:DWORD
	v_pk_add_f32 v[78:79], v[78:79], v[192:193]
	v_add3_u32 v84, v36, v83, s4
	v_and_b32_sdwa v83, v79, v129 dst_sel:DWORD dst_unused:UNUSED_PAD src0_sel:WORD_1 src1_sel:DWORD
	v_and_b32_sdwa v85, v78, v129 dst_sel:DWORD dst_unused:UNUSED_PAD src0_sel:WORD_1 src1_sel:DWORD
	v_and_b32_sdwa v82, v37, v129 dst_sel:DWORD dst_unused:UNUSED_PAD src0_sel:WORD_1 src1_sel:DWORD
	v_add3_u32 v83, v79, v83, s4
	v_add3_u32 v85, v78, v85, s4
	v_add3_u32 v82, v37, v82, s4
	v_and_b32_e32 v83, 0xffff0000, v83
	v_and_b32_e32 v85, 0xffff0000, v85
	v_or_b32_sdwa v83, v83, v82 dst_sel:DWORD dst_unused:UNUSED_PAD src0_sel:DWORD src1_sel:WORD_1
	v_or_b32_sdwa v82, v85, v84 dst_sel:DWORD dst_unused:UNUSED_PAD src0_sel:DWORD src1_sel:WORD_1
	global_store_dwordx2 v[30:31], v[82:83], off offset:2560
	v_pk_mul_f32 v[82:83], v[78:79], v[78:79]
	s_nop 0
	v_pk_fma_f32 v[154:155], v[36:37], v[36:37], v[82:83]
	v_cvt_pk_f32_fp8_e32 v[84:85], v142
	v_cvt_pk_f32_fp8_sdwa v[172:173], v144 src0_sel:WORD_1
	v_cvt_pk_f32_fp8_sdwa v[162:163], v142 src0_sel:WORD_1
	v_cvt_pk_f32_fp8_e32 v[164:165], v144
	v_cvt_pk_f32_fp8_e32 v[180:181], v145
	s_waitcnt vmcnt(63)
	v_cvt_pk_f32_fp8_e32 v[188:189], v146
	v_cvt_pk_f32_fp8_sdwa v[146:147], v146 src0_sel:WORD_1
	v_cvt_pk_f32_fp8_sdwa v[144:145], v145 src0_sel:WORD_1
	v_mov_b32_e32 v194, v84
	v_mov_b32_e32 v195, v172
	v_mov_b32_e32 v192, v164
	v_mov_b32_e32 v193, v162
	v_pk_mul_f32 v[194:195], v[194:195], v[66:67] op_sel:[0,1] op_sel_hi:[1,0]
	v_mov_b32_e32 v196, v180
	v_mov_b32_e32 v197, v146
	v_pk_fma_f32 v[192:193], v[192:193], v[66:67], v[194:195]
	v_mov_b32_e32 v194, v188
	v_mov_b32_e32 v195, v144
	v_pk_mul_f32 v[196:197], v[196:197], v[64:65] op_sel:[0,1] op_sel_hi:[1,0]
	v_mov_b32_e32 v172, v85
	v_mov_b32_e32 v146, v181
	v_pk_fma_f32 v[194:195], v[194:195], v[64:65], v[196:197]
	v_mov_b32_e32 v162, v165
	v_pk_mul_f32 v[84:85], v[172:173], v[66:67] op_sel:[0,1] op_sel_hi:[1,0]
	v_mov_b32_e32 v144, v189
	v_pk_mul_f32 v[146:147], v[146:147], v[64:65] op_sel:[0,1] op_sel_hi:[1,0]
	v_lshlrev_b32_e32 v83, 16, v33
	v_lshlrev_b32_e32 v82, 16, v32
	v_pk_add_f32 v[192:193], v[192:193], v[194:195]
	v_pk_fma_f32 v[84:85], v[162:163], v[66:67], v[84:85]
	v_pk_fma_f32 v[144:145], v[144:145], v[64:65], v[146:147]
	v_and_b32_e32 v33, 0xffff0000, v33
	v_and_b32_e32 v32, 0xffff0000, v32
	v_pk_add_f32 v[82:83], v[192:193], v[82:83]
	v_pk_add_f32 v[84:85], v[84:85], v[144:145]
	s_nop 0
	v_pk_add_f32 v[84:85], v[84:85], v[32:33]
	v_and_b32_sdwa v33, v82, v129 dst_sel:DWORD dst_unused:UNUSED_PAD src0_sel:WORD_1 src1_sel:DWORD
	v_add3_u32 v142, v82, v33, s4
	v_and_b32_sdwa v33, v85, v129 dst_sel:DWORD dst_unused:UNUSED_PAD src0_sel:WORD_1 src1_sel:DWORD
	v_and_b32_sdwa v144, v84, v129 dst_sel:DWORD dst_unused:UNUSED_PAD src0_sel:WORD_1 src1_sel:DWORD
	v_and_b32_sdwa v32, v83, v129 dst_sel:DWORD dst_unused:UNUSED_PAD src0_sel:WORD_1 src1_sel:DWORD
	v_add3_u32 v33, v85, v33, s4
	v_add3_u32 v144, v84, v144, s4
	v_add3_u32 v32, v83, v32, s4
	v_and_b32_e32 v33, 0xffff0000, v33
	v_and_b32_e32 v144, 0xffff0000, v144
	v_or_b32_sdwa v33, v33, v32 dst_sel:DWORD dst_unused:UNUSED_PAD src0_sel:DWORD src1_sel:WORD_1
	v_or_b32_sdwa v32, v144, v142 dst_sel:DWORD dst_unused:UNUSED_PAD src0_sel:DWORD src1_sel:WORD_1
	global_store_dwordx2 v[30:31], v[32:33], off offset:3072
	v_pk_mul_f32 v[32:33], v[84:85], v[84:85]
	s_nop 0
	v_pk_fma_f32 v[144:145], v[82:83], v[82:83], v[32:33]
	v_cvt_pk_f32_fp8_e32 v[32:33], v132
	v_cvt_pk_f32_fp8_sdwa v[164:165], v134 src0_sel:WORD_1
	v_cvt_pk_f32_fp8_sdwa v[146:147], v132 src0_sel:WORD_1
	v_cvt_pk_f32_fp8_e32 v[162:163], v134
	v_cvt_pk_f32_fp8_e32 v[172:173], v135
	s_waitcnt vmcnt(63)
	v_cvt_pk_f32_fp8_sdwa v[188:189], v136 src0_sel:WORD_1
	v_cvt_pk_f32_fp8_sdwa v[134:135], v135 src0_sel:WORD_1
	v_cvt_pk_f32_fp8_e32 v[180:181], v136
	v_mov_b32_e32 v196, v32
	v_mov_b32_e32 v197, v164
	v_lshlrev_b32_e32 v193, 16, v27
	v_lshlrev_b32_e32 v192, 16, v26
	v_and_b32_e32 v195, 0xffff0000, v27
	v_and_b32_e32 v194, 0xffff0000, v26
	v_mov_b32_e32 v26, v162
	v_mov_b32_e32 v27, v146
	v_pk_mul_f32 v[196:197], v[196:197], v[66:67] op_sel:[0,1] op_sel_hi:[1,0]
	v_mov_b32_e32 v200, v172
	v_mov_b32_e32 v201, v188
	v_mov_b32_e32 v164, v33
	v_pk_fma_f32 v[26:27], v[26:27], v[66:67], v[196:197]
	v_mov_b32_e32 v196, v180
	v_mov_b32_e32 v197, v134
	v_pk_mul_f32 v[200:201], v[200:201], v[64:65] op_sel:[0,1] op_sel_hi:[1,0]
	v_mov_b32_e32 v146, v163
	v_pk_mul_f32 v[32:33], v[164:165], v[66:67] op_sel:[0,1] op_sel_hi:[1,0]
	v_mov_b32_e32 v188, v173
	v_pk_fma_f32 v[196:197], v[196:197], v[64:65], v[200:201]
	v_pk_fma_f32 v[32:33], v[146:147], v[66:67], v[32:33]
	v_mov_b32_e32 v134, v181
	v_pk_mul_f32 v[66:67], v[188:189], v[64:65] op_sel:[0,1] op_sel_hi:[1,0]
	v_pk_add_f32 v[26:27], v[26:27], v[196:197]
	v_pk_fma_f32 v[64:65], v[134:135], v[64:65], v[66:67]
	v_pk_add_f32 v[26:27], v[26:27], v[192:193]
	v_pk_add_f32 v[32:33], v[32:33], v[64:65]
	v_and_b32_sdwa v65, v26, v129 dst_sel:DWORD dst_unused:UNUSED_PAD src0_sel:WORD_1 src1_sel:DWORD
	v_pk_add_f32 v[32:33], v[32:33], v[194:195]
	v_add3_u32 v66, v26, v65, s4
	v_and_b32_sdwa v65, v33, v129 dst_sel:DWORD dst_unused:UNUSED_PAD src0_sel:WORD_1 src1_sel:DWORD
	v_and_b32_sdwa v67, v32, v129 dst_sel:DWORD dst_unused:UNUSED_PAD src0_sel:WORD_1 src1_sel:DWORD
	v_and_b32_sdwa v64, v27, v129 dst_sel:DWORD dst_unused:UNUSED_PAD src0_sel:WORD_1 src1_sel:DWORD
	v_add3_u32 v65, v33, v65, s4
	v_add3_u32 v67, v32, v67, s4
	v_add3_u32 v64, v27, v64, s4
	v_and_b32_e32 v65, 0xffff0000, v65
	v_and_b32_e32 v67, 0xffff0000, v67
	v_or_b32_sdwa v65, v65, v64 dst_sel:DWORD dst_unused:UNUSED_PAD src0_sel:DWORD src1_sel:WORD_1
	v_or_b32_sdwa v64, v67, v66 dst_sel:DWORD dst_unused:UNUSED_PAD src0_sel:DWORD src1_sel:WORD_1
	global_store_dwordx2 v[30:31], v[64:65], off offset:3584
	v_add_f32_e32 v64, v76, v77
	v_add_f32_e32 v65, v70, v71
	v_add_f32_e32 v64, v65, v64
	v_add_f32_e32 v65, v80, v81
	v_add_f32_e32 v64, v64, v65
	v_add_f32_e32 v65, v86, v87
	v_add_f32_e32 v64, v64, v65
	v_add_f32_e32 v65, v156, v157
	v_pk_mul_f32 v[30:31], v[32:33], v[32:33]
	v_add_f32_e32 v64, v64, v65
	v_add_f32_e32 v65, v154, v155
	v_pk_fma_f32 v[30:31], v[26:27], v[26:27], v[30:31]
	v_add_f32_e32 v64, v64, v65
	v_add_f32_e32 v65, v144, v145
	v_add_f32_e32 v64, v64, v65
	v_add_f32_e32 v30, v30, v31
	v_add_f32_e32 v30, v64, v30
	v_mov_b64_e32 v[64:65], v[212:213]
	v_mov_b64_e32 v[66:67], v[214:215]
	ds_bpermute_b32 v31, v1, v30
	s_waitcnt lgkmcnt(0)
	v_add_f32_e32 v30, v30, v31
	ds_bpermute_b32 v31, v90, v30
	s_waitcnt lgkmcnt(0)
	v_add_f32_e32 v30, v30, v31
	ds_bpermute_b32 v31, v91, v30
	s_waitcnt lgkmcnt(0)
	v_add_f32_e32 v30, v30, v31
	ds_bpermute_b32 v31, v92, v30
	s_waitcnt lgkmcnt(0)
	v_add_f32_e32 v30, v30, v31
	ds_bpermute_b32 v31, v93, v30
	s_waitcnt lgkmcnt(0)
	v_add_f32_e32 v30, v30, v31
	ds_bpermute_b32 v31, v94, v30
	s_waitcnt lgkmcnt(0)
	v_add_f32_e32 v30, v30, v31
	v_fmamk_f32 v30, v30, 0x3a000000, v127
	v_mul_f32_e32 v31, 0x4f800000, v30
	v_cmp_gt_f32_e32 vcc, s19, v30
	s_nop 1
	v_cndmask_b32_e32 v30, v30, v31, vcc
	v_sqrt_f32_e32 v31, v30
	s_nop 0
	v_add_u32_e32 v70, -1, v31
	v_add_u32_e32 v71, 1, v31
	v_fma_f32 v76, -v70, v31, v30
	v_fma_f32 v77, -v71, v31, v30
	v_cmp_ge_f32_e64 s[8:9], 0, v76
	s_nop 1
	v_cndmask_b32_e64 v31, v31, v70, s[8:9]
	v_cmp_lt_f32_e64 s[8:9], 0, v77
	s_nop 1
	v_cndmask_b32_e64 v31, v31, v71, s[8:9]
	v_mul_f32_e32 v70, 0x37800000, v31
	v_cndmask_b32_e32 v31, v31, v70, vcc
	v_cmp_class_f32_e32 vcc, v30, v128
	v_mov_b32_e32 v71, 0
	s_nop 0
	v_cndmask_b32_e32 v30, v31, v30, vcc
	v_div_scale_f32 v31, s[0:1], v30, v30, 1.0
	v_rcp_f32_e32 v70, v31
	v_div_scale_f32 v76, vcc, 1.0, v30, 1.0
	v_fma_f32 v77, -v31, v70, 1.0
	v_fmac_f32_e32 v70, v77, v70
	v_mul_f32_e32 v77, v76, v70
	v_fma_f32 v80, -v31, v77, v76
	v_fmac_f32_e32 v77, v80, v70
	v_fma_f32 v31, -v31, v77, v76
	v_div_fmas_f32 v31, v31, v70, v77
	v_div_fixup_f32 v70, v31, v30, 1.0
	v_mul_f32_e32 v30, v70, v58
	v_mul_f32_e32 v31, v70, v60

	v_mul_f32_e32 v30, v64, v30
	v_mul_f32_e32 v31, v65, v31
	v_cvt_pk_fp8_f32 v71, v30, v31
	v_mul_f32_e32 v58, v70, v59
	v_mul_f32_e32 v30, v70, v61
	v_mul_f32_e32 v31, v66, v58
	v_mul_f32_e32 v30, v67, v30
	v_cvt_pk_fp8_f32 v71, v31, v30 op_sel:[0,0,1]
	v_mul_f32_e32 v31, v70, v54
	v_mul_f32_e32 v54, v70, v62
	v_mov_b32_e32 v30, 0
	global_store_dword v[48:49], v71, off offset:2048
	v_mov_b64_e32 v[58:59], v[216:217]
	v_mov_b64_e32 v[60:61], v[218:219]
	v_mul_f32_e32 v55, v70, v55
	v_mul_f32_e32 v47, v70, v47
	v_mul_f32_e32 v43, v70, v43
	v_mul_f32_e32 v41, v70, v41
	v_mul_f32_e32 v37, v70, v37
	v_mul_f32_e32 v26, v70, v26
	v_mov_b32_e32 v66, 0
	v_mul_f32_e32 v27, v70, v27
	s_waitcnt vmcnt(24)
	v_cvt_pk_f32_fp8_sdwa v[76:77], v190 src0_sel:WORD_1

	v_mul_f32_e32 v31, v58, v31
	v_mul_f32_e32 v54, v59, v54
	v_cvt_pk_fp8_f32 v30, v31, v54
	v_mul_f32_e32 v31, v70, v63
	v_mul_f32_e32 v54, v60, v55
	v_mul_f32_e32 v31, v61, v31
	v_cvt_pk_fp8_f32 v30, v54, v31 op_sel:[0,0,1]
	v_mul_f32_e32 v31, v70, v46
	v_mul_f32_e32 v46, v70, v68
	ds_bpermute_b32 v54, v126, v130
	global_store_dword v[48:49], v30, off offset:2304
	v_mov_b64_e32 v[58:59], v[220:221]
	v_mov_b64_e32 v[60:61], v[222:223]
	v_mov_b32_e32 v30, 0
	s_waitcnt lgkmcnt(0)
	v_ashrrev_i32_e32 v55, 31, v54
	v_lshlrev_b64 v[54:55], 11, v[54:55]
	v_lshl_add_u64 v[54:55], v[4:5], 0, v[54:55]

	v_mul_f32_e32 v31, v58, v31
	v_mul_f32_e32 v46, v59, v46
	v_cvt_pk_fp8_f32 v30, v31, v46
	v_mul_f32_e32 v31, v70, v69
	v_mul_f32_e32 v46, v60, v47
	v_mul_f32_e32 v31, v61, v31
	v_cvt_pk_fp8_f32 v30, v46, v31 op_sel:[0,0,1]
	v_mul_f32_e32 v31, v70, v42
	v_mul_f32_e32 v42, v70, v72
	ds_bpermute_b32 v46, v125, v130
	global_store_dword v[48:49], v30, off offset:2560
	v_mov_b64_e32 v[58:59], v[224:225]
	v_mov_b64_e32 v[60:61], v[226:227]
	v_mov_b32_e32 v30, 0
	v_cvt_pk_f32_fp8_sdwa v[68:69], v184 src0_sel:WORD_1
	s_waitcnt lgkmcnt(0)
	v_ashrrev_i32_e32 v47, 31, v46
	v_lshlrev_b64 v[46:47], 11, v[46:47]
	v_lshl_add_u64 v[64:65], v[4:5], 0, v[46:47]
	v_mov_b32_e32 v81, v68

	v_mul_f32_e32 v31, v58, v31
	v_mul_f32_e32 v42, v59, v42
	v_cvt_pk_fp8_f32 v30, v31, v42
	v_mul_f32_e32 v31, v70, v73
	v_mul_f32_e32 v42, v60, v43
	v_mul_f32_e32 v31, v61, v31
	v_cvt_pk_fp8_f32 v30, v42, v31 op_sel:[0,0,1]
	v_mul_f32_e32 v31, v70, v40
	v_mul_f32_e32 v40, v70, v74
	v_cvt_pk_f32_fp8_sdwa v[72:73], v186 src0_sel:WORD_1
	global_store_dword v[48:49], v30, off offset:2816
	v_mov_b64_e32 v[58:59], v[228:229]
	v_mov_b64_e32 v[60:61], v[230:231]
	v_mov_b32_e32 v30, 0

	v_mul_f32_e32 v31, v58, v31
	v_mul_f32_e32 v40, v59, v40
	v_cvt_pk_fp8_f32 v30, v31, v40
	v_mul_f32_e32 v31, v70, v75
	v_mul_f32_e32 v40, v60, v41
	v_mul_f32_e32 v31, v61, v31
	v_cvt_pk_fp8_f32 v30, v40, v31 op_sel:[0,0,1]
	v_mul_f32_e32 v31, v70, v36
	v_mul_f32_e32 v36, v70, v78
	v_add_co_u32_e32 v58, vcc, s39, v20
	global_store_dword v[48:49], v30, off offset:3072
	v_mov_b64_e32 v[40:41], v[232:233]
	v_mov_b64_e32 v[42:43], v[234:235]
	v_mov_b32_e32 v30, 0
	v_addc_co_u32_e32 v59, vcc, 0, v21, vcc
	v_cvt_pk_f32_fp8_e32 v[74:75], v190

	v_mul_f32_e32 v31, v40, v31
	v_mul_f32_e32 v36, v41, v36
	v_cvt_pk_fp8_f32 v30, v31, v36
	v_mul_f32_e32 v31, v70, v79
	v_mul_f32_e32 v36, v42, v37
	v_mul_f32_e32 v31, v43, v31
	v_cvt_pk_fp8_f32 v30, v36, v31 op_sel:[0,0,1]
	v_mul_f32_e32 v31, v70, v82
	v_mul_f32_e32 v36, v70, v84
	v_mul_f32_e32 v37, v70, v83
	global_store_dword v[48:49], v30, off offset:3328
	v_mov_b64_e32 v[40:41], v[236:237]
	v_mov_b64_e32 v[42:43], v[238:239]
	v_mov_b32_e32 v30, 0
	v_mov_b32_e32 v83, v76

	v_mul_f32_e32 v31, v40, v31
	v_mul_f32_e32 v36, v41, v36
	v_cvt_pk_fp8_f32 v30, v31, v36
	v_mul_f32_e32 v31, v70, v85
	v_mul_f32_e32 v36, v42, v37
	v_mul_f32_e32 v31, v43, v31
	v_cvt_pk_fp8_f32 v30, v36, v31 op_sel:[0,0,1]
	ds_bpermute_b32 v36, v124, v130
	global_store_dword v[48:49], v30, off offset:3584
	v_mov_b64_e32 v[40:41], v[240:241]
	v_mov_b64_e32 v[42:43], v[242:243]
	ds_bpermute_b32 v30, v96, v130
	s_waitcnt lgkmcnt(1)
	v_ashrrev_i32_e32 v37, 31, v36
	v_lshlrev_b64 v[36:37], 11, v[36:37]
	v_lshl_add_u64 v[62:63], v[4:5], 0, v[36:37]
	s_waitcnt lgkmcnt(0)
	v_ashrrev_i32_e32 v31, 31, v30
	v_lshlrev_b64 v[30:31], 11, v[30:31]
	v_lshl_add_u64 v[60:61], v[4:5], 0, v[30:31]
	v_mul_f32_e32 v30, v70, v32

	v_mul_f32_e32 v26, v40, v26
	v_mul_f32_e32 v30, v41, v30
	v_cvt_pk_fp8_f32 v66, v26, v30
	v_mul_f32_e32 v26, v70, v33
	v_mul_f32_e32 v27, v42, v27
	v_mul_f32_e32 v26, v43, v26
	v_cvt_pk_fp8_f32 v66, v27, v26 op_sel:[0,0,1]
	v_cvt_pk_f32_fp8_e32 v[70:71], v186
	global_store_dword v[48:49], v66, off offset:3840
	global_load_dwordx2 v[48:49], v[58:59], off nt
	s_nop 0
	global_load_dwordx2 v[46:47], v[58:59], off offset:512 nt
	global_load_dwordx2 v[42:43], v[58:59], off offset:1024 nt
	global_load_dwordx2 v[40:41], v[58:59], off offset:1536 nt
	global_load_dwordx2 v[36:37], v[58:59], off offset:2048 nt
	global_load_dwordx2 v[32:33], v[58:59], off offset:2560 nt
	global_load_dwordx2 v[30:31], v[58:59], off offset:3072 nt
	global_load_dwordx2 v[26:27], v[58:59], off offset:3584 nt
	global_load_dword v181, v[60:61], off nt
	global_load_dword v173, v[60:61], off offset:256 nt
	global_load_dword v165, v[60:61], off offset:512 nt
	global_load_dword v157, v[60:61], off offset:768 nt
	global_load_dword v152, v[60:61], off offset:1024 nt
	global_load_dword v144, v[60:61], off offset:1280 nt
	global_load_dword v134, v[60:61], off offset:1536 nt
	global_load_dword v86, v[60:61], off offset:1792 nt
	global_load_dword v185, v[62:63], off nt
	global_load_dword v177, v[62:63], off offset:256 nt
	global_load_dword v169, v[62:63], off offset:512 nt
	global_load_dword v162, v[62:63], off offset:768 nt
	global_load_dword v154, v[62:63], off offset:1024 nt
	global_load_dword v145, v[62:63], off offset:1280 nt
	global_load_dword v135, v[62:63], off offset:1536 nt
	global_load_dword v87, v[62:63], off offset:1792 nt
	global_load_dword v187, v[64:65], off nt
	global_load_dword v179, v[64:65], off offset:256 nt
	global_load_dword v171, v[64:65], off offset:512 nt
	global_load_dword v163, v[64:65], off offset:768 nt
	global_load_dword v155, v[64:65], off offset:1024 nt
	global_load_dword v146, v[64:65], off offset:1280 nt
	global_load_dword v136, v[64:65], off offset:1536 nt
	global_load_dword v130, v[64:65], off offset:1792 nt
	global_load_dword v188, v[54:55], off nt
	global_load_dword v180, v[54:55], off offset:256 nt
	global_load_dword v172, v[54:55], off offset:512 nt
	global_load_dword v164, v[54:55], off offset:768 nt
	global_load_dword v156, v[54:55], off offset:1024 nt
	global_load_dword v147, v[54:55], off offset:1280 nt
	global_load_dword v142, v[54:55], off offset:1536 nt
	global_load_dword v132, v[54:55], off offset:1792 nt
	ds_bpermute_b32 v63, v120, v19
	ds_bpermute_b32 v62, v121, v19
	v_cvt_pk_f32_fp8_e32 v[58:59], v183
	ds_bpermute_b32 v61, v122, v19
	ds_bpermute_b32 v60, v123, v19
	v_cvt_pk_f32_fp8_sdwa v[64:65], v183 src0_sel:WORD_1
	v_cvt_pk_f32_fp8_e32 v[66:67], v184
	v_mov_b32_e32 v80, v58
	s_waitcnt lgkmcnt(2)
	v_pk_mul_f32 v[80:81], v[80:81], v[62:63] op_sel:[0,1] op_sel_hi:[1,0]
	v_mov_b32_e32 v79, v64
	v_mov_b32_e32 v78, v66
	v_mov_b32_e32 v82, v70
	v_mov_b32_e32 v68, v59
	v_pk_fma_f32 v[78:79], v[78:79], v[62:63], v[80:81]
	v_mov_b32_e32 v80, v74
	v_mov_b32_e32 v81, v72
	s_waitcnt lgkmcnt(0)
	v_pk_mul_f32 v[82:83], v[82:83], v[60:61] op_sel:[0,1] op_sel_hi:[1,0]
	v_mov_b32_e32 v64, v67
	v_pk_mul_f32 v[58:59], v[68:69], v[62:63] op_sel:[0,1] op_sel_hi:[1,0]
	v_mov_b32_e32 v76, v71
	v_pk_fma_f32 v[80:81], v[80:81], v[60:61], v[82:83]
	v_pk_fma_f32 v[58:59], v[64:65], v[62:63], v[58:59]
	v_mov_b32_e32 v72, v75
	v_pk_mul_f32 v[64:65], v[76:77], v[60:61] op_sel:[0,1] op_sel_hi:[1,0]
	s_waitcnt vmcnt(56)
	v_lshlrev_b32_e32 v55, 16, v57
	v_lshlrev_b32_e32 v54, 16, v56
	v_pk_add_f32 v[78:79], v[78:79], v[80:81]
	v_pk_fma_f32 v[64:65], v[72:73], v[60:61], v[64:65]
	v_and_b32_e32 v57, 0xffff0000, v57
	v_and_b32_e32 v56, 0xffff0000, v56
	v_pk_add_f32 v[54:55], v[78:79], v[54:55]
	v_pk_add_f32 v[58:59], v[58:59], v[64:65]
	v_add_co_u32_e32 v66, vcc, s40, v20
	v_pk_add_f32 v[56:57], v[58:59], v[56:57]
	v_and_b32_sdwa v59, v54, v129 dst_sel:DWORD dst_unused:UNUSED_PAD src0_sel:WORD_1 src1_sel:DWORD
	v_add3_u32 v64, v54, v59, s4
	v_and_b32_sdwa v59, v57, v129 dst_sel:DWORD dst_unused:UNUSED_PAD src0_sel:WORD_1 src1_sel:DWORD
	v_and_b32_sdwa v65, v56, v129 dst_sel:DWORD dst_unused:UNUSED_PAD src0_sel:WORD_1 src1_sel:DWORD
	v_and_b32_sdwa v58, v55, v129 dst_sel:DWORD dst_unused:UNUSED_PAD src0_sel:WORD_1 src1_sel:DWORD
	v_add3_u32 v59, v57, v59, s4
	v_add3_u32 v65, v56, v65, s4
	v_addc_co_u32_e32 v67, vcc, 0, v21, vcc
	v_add3_u32 v58, v55, v58, s4
	v_and_b32_e32 v59, 0xffff0000, v59
	v_and_b32_e32 v65, 0xffff0000, v65
	v_add_co_u32_e32 v20, vcc, s42, v20
	v_or_b32_sdwa v59, v59, v58 dst_sel:DWORD dst_unused:UNUSED_PAD src0_sel:DWORD src1_sel:WORD_1
	v_or_b32_sdwa v58, v65, v64 dst_sel:DWORD dst_unused:UNUSED_PAD src0_sel:DWORD src1_sel:WORD_1
	v_addc_co_u32_e32 v21, vcc, 0, v21, vcc
	global_store_dwordx2 v[20:21], v[58:59], off offset:-4096
	v_pk_mul_f32 v[58:59], v[56:57], v[56:57]
	s_nop 0
	v_pk_fma_f32 v[68:69], v[54:55], v[54:55], v[58:59]
	v_cvt_pk_f32_fp8_e32 v[58:59], v175
	v_cvt_pk_f32_fp8_sdwa v[72:73], v176 src0_sel:WORD_1
	v_cvt_pk_f32_fp8_sdwa v[64:65], v175 src0_sel:WORD_1
	v_cvt_pk_f32_fp8_e32 v[70:71], v176
	v_cvt_pk_f32_fp8_e32 v[74:75], v178
	v_cvt_pk_f32_fp8_sdwa v[80:81], v182 src0_sel:WORD_1
	v_cvt_pk_f32_fp8_sdwa v[76:77], v178 src0_sel:WORD_1
	v_cvt_pk_f32_fp8_e32 v[78:79], v182
	v_mov_b32_e32 v182, v58
	v_mov_b32_e32 v183, v72
	v_lshlrev_b32_e32 v83, 16, v53
	v_lshlrev_b32_e32 v82, 16, v52
	v_and_b32_e32 v85, 0xffff0000, v53
	v_and_b32_e32 v84, 0xffff0000, v52
	v_mov_b32_e32 v52, v70
	v_mov_b32_e32 v53, v64
	v_pk_mul_f32 v[182:183], v[182:183], v[62:63] op_sel:[0,1] op_sel_hi:[1,0]
	v_mov_b32_e32 v190, v74
	v_mov_b32_e32 v191, v80
	v_mov_b32_e32 v72, v59
	v_pk_fma_f32 v[52:53], v[52:53], v[62:63], v[182:183]
	v_mov_b32_e32 v182, v78
	v_mov_b32_e32 v183, v76
	v_pk_mul_f32 v[190:191], v[190:191], v[60:61] op_sel:[0,1] op_sel_hi:[1,0]
	v_mov_b32_e32 v64, v71
	v_pk_mul_f32 v[58:59], v[72:73], v[62:63] op_sel:[0,1] op_sel_hi:[1,0]
	v_mov_b32_e32 v80, v75
	v_pk_fma_f32 v[182:183], v[182:183], v[60:61], v[190:191]
	v_pk_fma_f32 v[58:59], v[64:65], v[62:63], v[58:59]
	v_mov_b32_e32 v76, v79
	v_pk_mul_f32 v[64:65], v[80:81], v[60:61] op_sel:[0,1] op_sel_hi:[1,0]
	v_pk_add_f32 v[52:53], v[52:53], v[182:183]
	v_pk_fma_f32 v[64:65], v[76:77], v[60:61], v[64:65]
	v_pk_add_f32 v[52:53], v[52:53], v[82:83]
	v_pk_add_f32 v[58:59], v[58:59], v[64:65]
	v_and_b32_sdwa v65, v52, v129 dst_sel:DWORD dst_unused:UNUSED_PAD src0_sel:WORD_1 src1_sel:DWORD
	v_pk_add_f32 v[58:59], v[58:59], v[84:85]
	v_add3_u32 v70, v52, v65, s4
	v_and_b32_sdwa v65, v59, v129 dst_sel:DWORD dst_unused:UNUSED_PAD src0_sel:WORD_1 src1_sel:DWORD
	v_and_b32_sdwa v71, v58, v129 dst_sel:DWORD dst_unused:UNUSED_PAD src0_sel:WORD_1 src1_sel:DWORD
	v_and_b32_sdwa v64, v53, v129 dst_sel:DWORD dst_unused:UNUSED_PAD src0_sel:WORD_1 src1_sel:DWORD
	v_add3_u32 v65, v59, v65, s4
	v_add3_u32 v71, v58, v71, s4
	v_add3_u32 v64, v53, v64, s4
	v_and_b32_e32 v65, 0xffff0000, v65
	v_and_b32_e32 v71, 0xffff0000, v71
	v_or_b32_sdwa v65, v65, v64 dst_sel:DWORD dst_unused:UNUSED_PAD src0_sel:DWORD src1_sel:WORD_1
	v_or_b32_sdwa v64, v71, v70 dst_sel:DWORD dst_unused:UNUSED_PAD src0_sel:DWORD src1_sel:WORD_1
	global_store_dwordx2 v[66:67], v[64:65], off offset:512
	v_pk_mul_f32 v[64:65], v[58:59], v[58:59]
	s_nop 0
	v_pk_fma_f32 v[74:75], v[52:53], v[52:53], v[64:65]
	v_cvt_pk_f32_fp8_e32 v[64:65], v167
	v_cvt_pk_f32_fp8_sdwa v[76:77], v168 src0_sel:WORD_1
	v_cvt_pk_f32_fp8_sdwa v[70:71], v167 src0_sel:WORD_1
	v_cvt_pk_f32_fp8_e32 v[72:73], v168
	v_cvt_pk_f32_fp8_e32 v[78:79], v170
	v_cvt_pk_f32_fp8_sdwa v[84:85], v174 src0_sel:WORD_1
	v_cvt_pk_f32_fp8_sdwa v[80:81], v170 src0_sel:WORD_1
	v_cvt_pk_f32_fp8_e32 v[82:83], v174
	v_mov_b32_e32 v190, v64
	v_mov_b32_e32 v191, v76
	v_lshlrev_b32_e32 v175, 16, v51
	v_lshlrev_b32_e32 v174, 16, v50
	v_and_b32_e32 v183, 0xffff0000, v51
	v_and_b32_e32 v182, 0xffff0000, v50
	v_mov_b32_e32 v50, v72
	v_mov_b32_e32 v51, v70
	v_pk_mul_f32 v[190:191], v[190:191], v[62:63] op_sel:[0,1] op_sel_hi:[1,0]
	v_mov_b32_e32 v192, v78
	v_mov_b32_e32 v193, v84
	v_mov_b32_e32 v76, v65
	v_pk_fma_f32 v[50:51], v[50:51], v[62:63], v[190:191]
	v_mov_b32_e32 v190, v82
	v_mov_b32_e32 v191, v80
	v_pk_mul_f32 v[192:193], v[192:193], v[60:61] op_sel:[0,1] op_sel_hi:[1,0]
	v_mov_b32_e32 v70, v73
	v_pk_mul_f32 v[64:65], v[76:77], v[62:63] op_sel:[0,1] op_sel_hi:[1,0]
	v_mov_b32_e32 v84, v79
	v_pk_fma_f32 v[190:191], v[190:191], v[60:61], v[192:193]
	v_pk_fma_f32 v[64:65], v[70:71], v[62:63], v[64:65]
	v_mov_b32_e32 v80, v83
	v_pk_mul_f32 v[70:71], v[84:85], v[60:61] op_sel:[0,1] op_sel_hi:[1,0]
	v_pk_add_f32 v[50:51], v[50:51], v[190:191]
	v_pk_fma_f32 v[70:71], v[80:81], v[60:61], v[70:71]
	v_pk_add_f32 v[50:51], v[50:51], v[174:175]
	v_pk_add_f32 v[64:65], v[64:65], v[70:71]
	v_and_b32_sdwa v71, v50, v129 dst_sel:DWORD dst_unused:UNUSED_PAD src0_sel:WORD_1 src1_sel:DWORD
	v_pk_add_f32 v[64:65], v[64:65], v[182:183]
	v_add3_u32 v72, v50, v71, s4
	v_and_b32_sdwa v71, v65, v129 dst_sel:DWORD dst_unused:UNUSED_PAD src0_sel:WORD_1 src1_sel:DWORD
	v_and_b32_sdwa v73, v64, v129 dst_sel:DWORD dst_unused:UNUSED_PAD src0_sel:WORD_1 src1_sel:DWORD
	v_and_b32_sdwa v70, v51, v129 dst_sel:DWORD dst_unused:UNUSED_PAD src0_sel:WORD_1 src1_sel:DWORD
	v_add3_u32 v71, v65, v71, s4
	v_add3_u32 v73, v64, v73, s4
	v_add3_u32 v70, v51, v70, s4
	v_and_b32_e32 v71, 0xffff0000, v71
	v_and_b32_e32 v73, 0xffff0000, v73
	v_or_b32_sdwa v71, v71, v70 dst_sel:DWORD dst_unused:UNUSED_PAD src0_sel:DWORD src1_sel:WORD_1
	v_or_b32_sdwa v70, v73, v72 dst_sel:DWORD dst_unused:UNUSED_PAD src0_sel:DWORD src1_sel:WORD_1
	global_store_dwordx2 v[66:67], v[70:71], off offset:1024
	v_pk_mul_f32 v[70:71], v[64:65], v[64:65]
	s_nop 0
	v_pk_fma_f32 v[80:81], v[50:51], v[50:51], v[70:71]
	v_cvt_pk_f32_fp8_e32 v[70:71], v159
	v_cvt_pk_f32_fp8_sdwa v[78:79], v160 src0_sel:WORD_1
	v_cvt_pk_f32_fp8_sdwa v[72:73], v159 src0_sel:WORD_1
	v_cvt_pk_f32_fp8_e32 v[76:77], v160
	v_cvt_pk_f32_fp8_e32 v[82:83], v161
	v_cvt_pk_f32_fp8_sdwa v[84:85], v161 src0_sel:WORD_1
	v_cvt_pk_f32_fp8_e32 v[160:161], v166
	v_cvt_pk_f32_fp8_sdwa v[166:167], v166 src0_sel:WORD_1
	v_mov_b32_e32 v190, v70
	v_mov_b32_e32 v191, v78
	v_lshlrev_b32_e32 v175, 16, v45
	v_lshlrev_b32_e32 v174, 16, v44
	v_and_b32_e32 v183, 0xffff0000, v45
	v_and_b32_e32 v182, 0xffff0000, v44
	v_mov_b32_e32 v44, v76
	v_mov_b32_e32 v45, v72
	v_pk_mul_f32 v[190:191], v[190:191], v[62:63] op_sel:[0,1] op_sel_hi:[1,0]
	v_mov_b32_e32 v192, v82
	v_mov_b32_e32 v193, v166
	v_mov_b32_e32 v78, v71
	v_pk_fma_f32 v[44:45], v[44:45], v[62:63], v[190:191]
	v_mov_b32_e32 v190, v160
	v_mov_b32_e32 v191, v84
	v_pk_mul_f32 v[192:193], v[192:193], v[60:61] op_sel:[0,1] op_sel_hi:[1,0]
	v_mov_b32_e32 v72, v77
	v_pk_mul_f32 v[70:71], v[78:79], v[62:63] op_sel:[0,1] op_sel_hi:[1,0]
	v_mov_b32_e32 v166, v83
	v_pk_fma_f32 v[190:191], v[190:191], v[60:61], v[192:193]
	v_pk_fma_f32 v[70:71], v[72:73], v[62:63], v[70:71]
	v_mov_b32_e32 v84, v161
	v_pk_mul_f32 v[72:73], v[166:167], v[60:61] op_sel:[0,1] op_sel_hi:[1,0]
	v_pk_add_f32 v[44:45], v[44:45], v[190:191]
	v_pk_fma_f32 v[72:73], v[84:85], v[60:61], v[72:73]
	v_pk_add_f32 v[44:45], v[44:45], v[174:175]
	v_pk_add_f32 v[70:71], v[70:71], v[72:73]
	v_and_b32_sdwa v73, v44, v129 dst_sel:DWORD dst_unused:UNUSED_PAD src0_sel:WORD_1 src1_sel:DWORD
	v_pk_add_f32 v[70:71], v[70:71], v[182:183]
	v_add3_u32 v76, v44, v73, s4
	v_and_b32_sdwa v73, v71, v129 dst_sel:DWORD dst_unused:UNUSED_PAD src0_sel:WORD_1 src1_sel:DWORD
	v_and_b32_sdwa v77, v70, v129 dst_sel:DWORD dst_unused:UNUSED_PAD src0_sel:WORD_1 src1_sel:DWORD
	v_and_b32_sdwa v72, v45, v129 dst_sel:DWORD dst_unused:UNUSED_PAD src0_sel:WORD_1 src1_sel:DWORD
	v_add3_u32 v73, v71, v73, s4
	v_add3_u32 v77, v70, v77, s4
	v_add3_u32 v72, v45, v72, s4
	v_and_b32_e32 v73, 0xffff0000, v73
	v_and_b32_e32 v77, 0xffff0000, v77
	v_or_b32_sdwa v73, v73, v72 dst_sel:DWORD dst_unused:UNUSED_PAD src0_sel:DWORD src1_sel:WORD_1
	v_or_b32_sdwa v72, v77, v76 dst_sel:DWORD dst_unused:UNUSED_PAD src0_sel:DWORD src1_sel:WORD_1
	global_store_dwordx2 v[66:67], v[72:73], off offset:1536
	v_pk_mul_f32 v[72:73], v[70:71], v[70:71]
	s_nop 0
	v_pk_fma_f32 v[84:85], v[44:45], v[44:45], v[72:73]
	v_cvt_pk_f32_fp8_e32 v[72:73], v150
	v_cvt_pk_f32_fp8_sdwa v[82:83], v151 src0_sel:WORD_1
	v_cvt_pk_f32_fp8_sdwa v[76:77], v150 src0_sel:WORD_1
	v_cvt_pk_f32_fp8_e32 v[78:79], v151
	v_cvt_pk_f32_fp8_e32 v[150:151], v153
	v_cvt_pk_f32_fp8_e32 v[166:167], v158
	v_cvt_pk_f32_fp8_sdwa v[158:159], v158 src0_sel:WORD_1
	v_cvt_pk_f32_fp8_sdwa v[160:161], v153 src0_sel:WORD_1
	v_mov_b32_e32 v190, v72
	v_mov_b32_e32 v191, v82
	v_lshlrev_b32_e32 v175, 16, v39
	v_lshlrev_b32_e32 v174, 16, v38
	v_and_b32_e32 v183, 0xffff0000, v39
	v_and_b32_e32 v182, 0xffff0000, v38
	v_mov_b32_e32 v38, v78
	v_mov_b32_e32 v39, v76
	v_pk_mul_f32 v[190:191], v[190:191], v[62:63] op_sel:[0,1] op_sel_hi:[1,0]
	v_mov_b32_e32 v192, v150
	v_mov_b32_e32 v193, v158
	v_mov_b32_e32 v82, v73
	v_pk_fma_f32 v[38:39], v[38:39], v[62:63], v[190:191]
	v_mov_b32_e32 v190, v166
	v_mov_b32_e32 v191, v160
	v_pk_mul_f32 v[192:193], v[192:193], v[60:61] op_sel:[0,1] op_sel_hi:[1,0]
	v_mov_b32_e32 v76, v79
	v_pk_mul_f32 v[72:73], v[82:83], v[62:63] op_sel:[0,1] op_sel_hi:[1,0]
	v_mov_b32_e32 v158, v151
	v_pk_fma_f32 v[190:191], v[190:191], v[60:61], v[192:193]
	v_pk_fma_f32 v[72:73], v[76:77], v[62:63], v[72:73]
	v_mov_b32_e32 v160, v167
	v_pk_mul_f32 v[76:77], v[158:159], v[60:61] op_sel:[0,1] op_sel_hi:[1,0]
	v_pk_add_f32 v[38:39], v[38:39], v[190:191]
	v_pk_fma_f32 v[76:77], v[160:161], v[60:61], v[76:77]
	v_pk_add_f32 v[38:39], v[38:39], v[174:175]
	v_pk_add_f32 v[72:73], v[72:73], v[76:77]
	v_and_b32_sdwa v77, v38, v129 dst_sel:DWORD dst_unused:UNUSED_PAD src0_sel:WORD_1 src1_sel:DWORD
	v_pk_add_f32 v[72:73], v[72:73], v[182:183]
	v_add3_u32 v78, v38, v77, s4
	v_and_b32_sdwa v77, v73, v129 dst_sel:DWORD dst_unused:UNUSED_PAD src0_sel:WORD_1 src1_sel:DWORD
	v_and_b32_sdwa v79, v72, v129 dst_sel:DWORD dst_unused:UNUSED_PAD src0_sel:WORD_1 src1_sel:DWORD
	v_and_b32_sdwa v76, v39, v129 dst_sel:DWORD dst_unused:UNUSED_PAD src0_sel:WORD_1 src1_sel:DWORD
	v_add3_u32 v77, v73, v77, s4
	v_add3_u32 v79, v72, v79, s4
	v_add3_u32 v76, v39, v76, s4
	v_and_b32_e32 v77, 0xffff0000, v77
	v_and_b32_e32 v79, 0xffff0000, v79
	v_or_b32_sdwa v77, v77, v76 dst_sel:DWORD dst_unused:UNUSED_PAD src0_sel:DWORD src1_sel:WORD_1
	v_or_b32_sdwa v76, v79, v78 dst_sel:DWORD dst_unused:UNUSED_PAD src0_sel:DWORD src1_sel:WORD_1
	global_store_dwordx2 v[66:67], v[76:77], off offset:2048
	v_pk_mul_f32 v[76:77], v[72:73], v[72:73]
	s_nop 0
	v_pk_fma_f32 v[150:151], v[38:39], v[38:39], v[76:77]
	v_cvt_pk_f32_fp8_e32 v[76:77], v141
	v_cvt_pk_f32_fp8_sdwa v[158:159], v143 src0_sel:WORD_1
	v_cvt_pk_f32_fp8_sdwa v[78:79], v141 src0_sel:WORD_1
	v_cvt_pk_f32_fp8_e32 v[82:83], v143
	v_cvt_pk_f32_fp8_e32 v[160:161], v148
	v_cvt_pk_f32_fp8_sdwa v[166:167], v148 src0_sel:WORD_1
	v_cvt_pk_f32_fp8_e32 v[174:175], v149
	v_cvt_pk_f32_fp8_sdwa v[148:149], v149 src0_sel:WORD_1
	v_mov_b32_e32 v192, v76
	v_mov_b32_e32 v193, v158
	v_lshlrev_b32_e32 v183, 16, v35
	v_lshlrev_b32_e32 v182, 16, v34
	v_and_b32_e32 v191, 0xffff0000, v35
	v_and_b32_e32 v190, 0xffff0000, v34
	v_mov_b32_e32 v34, v82
	v_mov_b32_e32 v35, v78
	v_pk_mul_f32 v[192:193], v[192:193], v[62:63] op_sel:[0,1] op_sel_hi:[1,0]
	v_mov_b32_e32 v194, v160
	v_mov_b32_e32 v195, v148
	v_mov_b32_e32 v158, v77
	v_pk_fma_f32 v[34:35], v[34:35], v[62:63], v[192:193]
	v_mov_b32_e32 v192, v174
	v_mov_b32_e32 v193, v166
	v_pk_mul_f32 v[194:195], v[194:195], v[60:61] op_sel:[0,1] op_sel_hi:[1,0]
	v_mov_b32_e32 v78, v83
	v_pk_mul_f32 v[76:77], v[158:159], v[62:63] op_sel:[0,1] op_sel_hi:[1,0]
	v_mov_b32_e32 v148, v161
	v_pk_fma_f32 v[192:193], v[192:193], v[60:61], v[194:195]
	v_pk_fma_f32 v[76:77], v[78:79], v[62:63], v[76:77]
	v_mov_b32_e32 v166, v175
	v_pk_mul_f32 v[78:79], v[148:149], v[60:61] op_sel:[0,1] op_sel_hi:[1,0]
	v_pk_add_f32 v[34:35], v[34:35], v[192:193]
	v_pk_fma_f32 v[78:79], v[166:167], v[60:61], v[78:79]
	v_pk_add_f32 v[34:35], v[34:35], v[182:183]
	v_pk_add_f32 v[76:77], v[76:77], v[78:79]
	s_nop 0
	v_pk_add_f32 v[78:79], v[76:77], v[190:191]
	v_and_b32_sdwa v77, v34, v129 dst_sel:DWORD dst_unused:UNUSED_PAD src0_sel:WORD_1 src1_sel:DWORD
	v_add3_u32 v82, v34, v77, s4
	v_and_b32_sdwa v77, v79, v129 dst_sel:DWORD dst_unused:UNUSED_PAD src0_sel:WORD_1 src1_sel:DWORD
	v_and_b32_sdwa v83, v78, v129 dst_sel:DWORD dst_unused:UNUSED_PAD src0_sel:WORD_1 src1_sel:DWORD
	v_and_b32_sdwa v76, v35, v129 dst_sel:DWORD dst_unused:UNUSED_PAD src0_sel:WORD_1 src1_sel:DWORD
	v_add3_u32 v77, v79, v77, s4
	v_add3_u32 v83, v78, v83, s4
	v_add3_u32 v76, v35, v76, s4
	v_and_b32_e32 v77, 0xffff0000, v77
	v_and_b32_e32 v83, 0xffff0000, v83
	v_or_b32_sdwa v77, v77, v76 dst_sel:DWORD dst_unused:UNUSED_PAD src0_sel:DWORD src1_sel:WORD_1
	v_or_b32_sdwa v76, v83, v82 dst_sel:DWORD dst_unused:UNUSED_PAD src0_sel:DWORD src1_sel:WORD_1
	global_store_dwordx2 v[66:67], v[76:77], off offset:2560
	v_pk_mul_f32 v[76:77], v[78:79], v[78:79]
	s_nop 0
	v_pk_fma_f32 v[148:149], v[34:35], v[34:35], v[76:77]
	v_cvt_pk_f32_fp8_e32 v[76:77], v137
	v_cvt_pk_f32_fp8_sdwa v[160:161], v138 src0_sel:WORD_1
	v_cvt_pk_f32_fp8_sdwa v[82:83], v137 src0_sel:WORD_1
	v_cvt_pk_f32_fp8_e32 v[158:159], v138
	v_cvt_pk_f32_fp8_e32 v[166:167], v139
	v_cvt_pk_f32_fp8_e32 v[174:175], v140
	v_cvt_pk_f32_fp8_sdwa v[140:141], v140 src0_sel:WORD_1
	v_cvt_pk_f32_fp8_sdwa v[138:139], v139 src0_sel:WORD_1
	v_mov_b32_e32 v192, v76
	v_mov_b32_e32 v193, v160
	v_lshlrev_b32_e32 v183, 16, v29
	v_lshlrev_b32_e32 v182, 16, v28
	v_and_b32_e32 v191, 0xffff0000, v29
	v_and_b32_e32 v190, 0xffff0000, v28
	v_mov_b32_e32 v28, v158
	v_mov_b32_e32 v29, v82
	v_pk_mul_f32 v[192:193], v[192:193], v[62:63] op_sel:[0,1] op_sel_hi:[1,0]
	v_mov_b32_e32 v194, v166
	v_mov_b32_e32 v195, v140
	v_mov_b32_e32 v160, v77
	v_pk_fma_f32 v[28:29], v[28:29], v[62:63], v[192:193]
	v_mov_b32_e32 v192, v174
	v_mov_b32_e32 v193, v138
	v_pk_mul_f32 v[194:195], v[194:195], v[60:61] op_sel:[0,1] op_sel_hi:[1,0]
	v_mov_b32_e32 v82, v159
	v_pk_mul_f32 v[76:77], v[160:161], v[62:63] op_sel:[0,1] op_sel_hi:[1,0]
	v_mov_b32_e32 v140, v167
	v_pk_fma_f32 v[192:193], v[192:193], v[60:61], v[194:195]
	v_pk_fma_f32 v[76:77], v[82:83], v[62:63], v[76:77]
	v_mov_b32_e32 v138, v175
	v_pk_mul_f32 v[82:83], v[140:141], v[60:61] op_sel:[0,1] op_sel_hi:[1,0]
	v_pk_add_f32 v[28:29], v[28:29], v[192:193]
	v_pk_fma_f32 v[82:83], v[138:139], v[60:61], v[82:83]
	v_pk_add_f32 v[28:29], v[28:29], v[182:183]
	v_pk_add_f32 v[76:77], v[76:77], v[82:83]
	s_nop 0
	v_pk_add_f32 v[82:83], v[76:77], v[190:191]
	v_and_b32_sdwa v77, v28, v129 dst_sel:DWORD dst_unused:UNUSED_PAD src0_sel:WORD_1 src1_sel:DWORD
	v_add3_u32 v137, v28, v77, s4
	v_and_b32_sdwa v77, v83, v129 dst_sel:DWORD dst_unused:UNUSED_PAD src0_sel:WORD_1 src1_sel:DWORD
	v_and_b32_sdwa v138, v82, v129 dst_sel:DWORD dst_unused:UNUSED_PAD src0_sel:WORD_1 src1_sel:DWORD
	v_and_b32_sdwa v76, v29, v129 dst_sel:DWORD dst_unused:UNUSED_PAD src0_sel:WORD_1 src1_sel:DWORD
	v_add3_u32 v77, v83, v77, s4
	v_add3_u32 v138, v82, v138, s4
	v_add3_u32 v76, v29, v76, s4
	v_and_b32_e32 v77, 0xffff0000, v77
	v_and_b32_e32 v138, 0xffff0000, v138
	v_or_b32_sdwa v77, v77, v76 dst_sel:DWORD dst_unused:UNUSED_PAD src0_sel:DWORD src1_sel:WORD_1
	v_or_b32_sdwa v76, v138, v137 dst_sel:DWORD dst_unused:UNUSED_PAD src0_sel:DWORD src1_sel:WORD_1
	global_store_dwordx2 v[66:67], v[76:77], off offset:3072
	v_pk_mul_f32 v[76:77], v[82:83], v[82:83]
	s_nop 0
	v_pk_fma_f32 v[138:139], v[28:29], v[28:29], v[76:77]
	v_cvt_pk_f32_fp8_e32 v[140:141], v88
	v_cvt_pk_f32_fp8_sdwa v[158:159], v88 src0_sel:WORD_1
	v_cvt_pk_f32_fp8_e32 v[160:161], v89
	v_cvt_pk_f32_fp8_sdwa v[88:89], v89 src0_sel:WORD_1
	v_cvt_pk_f32_fp8_e32 v[166:167], v131
	v_cvt_pk_f32_fp8_sdwa v[190:191], v133 src0_sel:WORD_1
	v_cvt_pk_f32_fp8_sdwa v[174:175], v131 src0_sel:WORD_1
	v_cvt_pk_f32_fp8_e32 v[182:183], v133
	v_mov_b32_e32 v194, v140
	v_mov_b32_e32 v195, v88
	v_mov_b32_e32 v192, v160
	v_mov_b32_e32 v193, v158
	v_pk_mul_f32 v[194:195], v[194:195], v[62:63] op_sel:[0,1] op_sel_hi:[1,0]
	v_mov_b32_e32 v196, v166
	v_mov_b32_e32 v197, v190
	v_mov_b32_e32 v88, v141
	v_pk_fma_f32 v[192:193], v[192:193], v[62:63], v[194:195]
	v_mov_b32_e32 v194, v182
	v_mov_b32_e32 v195, v174
	v_pk_mul_f32 v[196:197], v[196:197], v[60:61] op_sel:[0,1] op_sel_hi:[1,0]
	v_mov_b32_e32 v158, v161
	v_pk_mul_f32 v[88:89], v[88:89], v[62:63] op_sel:[0,1] op_sel_hi:[1,0]
	v_mov_b32_e32 v190, v167
	v_pk_fma_f32 v[194:195], v[194:195], v[60:61], v[196:197]
	v_pk_fma_f32 v[62:63], v[158:159], v[62:63], v[88:89]
	v_mov_b32_e32 v174, v183
	v_pk_mul_f32 v[88:89], v[190:191], v[60:61] op_sel:[0,1] op_sel_hi:[1,0]
	v_lshlrev_b32_e32 v77, 16, v23
	v_lshlrev_b32_e32 v76, 16, v22
	v_pk_add_f32 v[192:193], v[192:193], v[194:195]
	v_pk_fma_f32 v[60:61], v[174:175], v[60:61], v[88:89]
	v_and_b32_e32 v23, 0xffff0000, v23
	v_and_b32_e32 v22, 0xffff0000, v22
	v_pk_add_f32 v[76:77], v[192:193], v[76:77]
	v_pk_add_f32 v[60:61], v[62:63], v[60:61]
	s_nop 0
	v_pk_add_f32 v[60:61], v[60:61], v[22:23]
	v_and_b32_sdwa v23, v76, v129 dst_sel:DWORD dst_unused:UNUSED_PAD src0_sel:WORD_1 src1_sel:DWORD
	v_add3_u32 v62, v76, v23, s4
	v_and_b32_sdwa v23, v61, v129 dst_sel:DWORD dst_unused:UNUSED_PAD src0_sel:WORD_1 src1_sel:DWORD
	v_and_b32_sdwa v63, v60, v129 dst_sel:DWORD dst_unused:UNUSED_PAD src0_sel:WORD_1 src1_sel:DWORD
	v_and_b32_sdwa v22, v77, v129 dst_sel:DWORD dst_unused:UNUSED_PAD src0_sel:WORD_1 src1_sel:DWORD
	v_add3_u32 v23, v61, v23, s4
	v_add3_u32 v63, v60, v63, s4
	v_add3_u32 v22, v77, v22, s4
	v_and_b32_e32 v23, 0xffff0000, v23
	v_and_b32_e32 v63, 0xffff0000, v63
	v_or_b32_sdwa v23, v23, v22 dst_sel:DWORD dst_unused:UNUSED_PAD src0_sel:DWORD src1_sel:WORD_1
	v_or_b32_sdwa v22, v63, v62 dst_sel:DWORD dst_unused:UNUSED_PAD src0_sel:DWORD src1_sel:WORD_1
	v_add_f32_e32 v62, v74, v75
	v_add_f32_e32 v63, v68, v69
	v_add_f32_e32 v62, v63, v62
	v_add_f32_e32 v63, v80, v81
	v_add_f32_e32 v62, v62, v63
	v_add_f32_e32 v63, v84, v85
	v_add_f32_e32 v62, v62, v63
	v_add_f32_e32 v63, v150, v151
	global_store_dwordx2 v[66:67], v[22:23], off offset:3584
	v_pk_mul_f32 v[22:23], v[60:61], v[60:61]
	v_add_f32_e32 v62, v62, v63
	v_add_f32_e32 v63, v148, v149
	v_pk_fma_f32 v[22:23], v[76:77], v[76:77], v[22:23]
	v_add_f32_e32 v62, v62, v63
	v_add_f32_e32 v63, v138, v139
	v_add_f32_e32 v62, v62, v63
	v_add_f32_e32 v22, v22, v23
	v_add_f32_e32 v22, v62, v22
	v_mov_b64_e32 v[66:67], v[212:213]
	v_mov_b64_e32 v[68:69], v[214:215]
	ds_bpermute_b32 v23, v1, v22
	s_waitcnt lgkmcnt(0)
	v_add_f32_e32 v22, v22, v23
	ds_bpermute_b32 v23, v90, v22
	s_waitcnt lgkmcnt(0)
	v_add_f32_e32 v22, v22, v23
	ds_bpermute_b32 v23, v91, v22
	s_waitcnt lgkmcnt(0)
	v_add_f32_e32 v22, v22, v23
	ds_bpermute_b32 v23, v92, v22
	s_waitcnt lgkmcnt(0)
	v_add_f32_e32 v22, v22, v23
	ds_bpermute_b32 v23, v93, v22
	s_waitcnt lgkmcnt(0)
	v_add_f32_e32 v22, v22, v23
	ds_bpermute_b32 v23, v94, v22
	s_waitcnt lgkmcnt(0)
	v_add_f32_e32 v22, v22, v23
	v_fmamk_f32 v22, v22, 0x3a000000, v127
	v_mul_f32_e32 v23, 0x4f800000, v22
	v_cmp_gt_f32_e32 vcc, s19, v22
	s_nop 1
	v_cndmask_b32_e32 v22, v22, v23, vcc
	v_sqrt_f32_e32 v23, v22
	s_nop 0
	v_add_u32_e32 v62, -1, v23
	v_add_u32_e32 v63, 1, v23
	v_fma_f32 v74, -v62, v23, v22
	v_fma_f32 v75, -v63, v23, v22
	v_cmp_ge_f32_e64 s[8:9], 0, v74
	s_nop 1
	v_cndmask_b32_e64 v23, v23, v62, s[8:9]
	v_cmp_lt_f32_e64 s[8:9], 0, v75
	s_nop 1
	v_cndmask_b32_e64 v23, v23, v63, s[8:9]
	v_mul_f32_e32 v62, 0x37800000, v23
	v_cndmask_b32_e32 v23, v23, v62, vcc
	v_cmp_class_f32_e32 vcc, v22, v128
	v_mov_b32_e32 v63, 0
	s_nop 0
	v_cndmask_b32_e32 v22, v23, v22, vcc
	v_div_scale_f32 v23, s[0:1], v22, v22, 1.0
	v_rcp_f32_e32 v62, v23
	v_div_scale_f32 v74, vcc, 1.0, v22, 1.0
	v_fma_f32 v75, -v23, v62, 1.0
	v_fmac_f32_e32 v62, v75, v62
	v_mul_f32_e32 v75, v74, v62
	v_fma_f32 v80, -v23, v75, v74
	v_fmac_f32_e32 v75, v80, v62
	v_fma_f32 v23, -v23, v75, v74
	v_div_fmas_f32 v23, v23, v62, v75
	v_div_fixup_f32 v80, v23, v22, 1.0
	v_mul_f32_e32 v22, v80, v54
	v_mul_f32_e32 v23, v80, v56

	v_mul_f32_e32 v22, v66, v22
	v_mul_f32_e32 v23, v67, v23
	v_cvt_pk_fp8_f32 v63, v22, v23
	v_mul_f32_e32 v54, v80, v55
	v_mul_f32_e32 v22, v80, v57
	v_mul_f32_e32 v23, v68, v54
	v_mul_f32_e32 v22, v69, v22
	v_cvt_pk_fp8_f32 v63, v23, v22 op_sel:[0,0,1]
	v_mul_f32_e32 v23, v80, v52
	v_mul_f32_e32 v52, v80, v58
	v_mov_b32_e32 v22, 0
	global_store_dword v[24:25], v63, off
	v_mov_b64_e32 v[54:55], v[216:217]
	v_mov_b64_e32 v[56:57], v[218:219]
	v_mul_f32_e32 v53, v80, v53
	v_mul_f32_e32 v51, v80, v51
	v_mul_f32_e32 v45, v80, v45
	v_mul_f32_e32 v39, v80, v39
	v_mul_f32_e32 v35, v80, v35
	v_mul_f32_e32 v29, v80, v29
	s_waitcnt vmcnt(16)
	v_cvt_pk_f32_fp8_e32 v[62:63], v188
	v_lshlrev_b32_e32 v67, 16, v49
	v_lshlrev_b32_e32 v66, 16, v48
	v_and_b32_e32 v49, 0xffff0000, v49
	v_and_b32_e32 v48, 0xffff0000, v48

	v_mul_f32_e32 v23, v54, v23
	v_mul_f32_e32 v52, v55, v52
	v_cvt_pk_fp8_f32 v22, v23, v52
	v_mul_f32_e32 v23, v80, v59
	v_mul_f32_e32 v52, v56, v53
	v_mul_f32_e32 v23, v57, v23
	v_cvt_pk_fp8_f32 v22, v52, v23 op_sel:[0,0,1]
	v_mul_f32_e32 v23, v80, v50
	v_mul_f32_e32 v50, v80, v64
	v_cvt_pk_f32_fp8_e32 v[56:57], v187
	global_store_dword v[24:25], v22, off offset:256
	v_mov_b64_e32 v[52:53], v[220:221]
	v_mov_b64_e32 v[54:55], v[222:223]
	v_mov_b32_e32 v22, 0
	v_cvt_pk_f32_fp8_sdwa v[58:59], v187 src0_sel:WORD_1
	v_mov_b32_e32 v74, v56

	v_mul_f32_e32 v23, v52, v23
	v_mul_f32_e32 v50, v53, v50
	v_cvt_pk_fp8_f32 v22, v23, v50
	v_mul_f32_e32 v23, v80, v65
	v_mul_f32_e32 v50, v54, v51
	v_mul_f32_e32 v23, v55, v23
	v_cvt_pk_fp8_f32 v22, v50, v23 op_sel:[0,0,1]
	v_mul_f32_e32 v23, v80, v44
	v_mul_f32_e32 v44, v80, v70
	v_cvt_pk_f32_fp8_sdwa v[64:65], v188 src0_sel:WORD_1
	global_store_dword v[24:25], v22, off offset:512
	v_mov_b64_e32 v[50:51], v[224:225]
	v_mov_b64_e32 v[52:53], v[226:227]
	v_mov_b32_e32 v22, 0
	v_mov_b32_e32 v75, v64
	v_mov_b32_e32 v64, v57

	v_mul_f32_e32 v23, v50, v23
	v_mul_f32_e32 v44, v51, v44
	v_cvt_pk_fp8_f32 v22, v23, v44
	v_mul_f32_e32 v23, v80, v71
	v_mul_f32_e32 v44, v52, v45
	v_mul_f32_e32 v23, v53, v23
	v_cvt_pk_fp8_f32 v22, v44, v23 op_sel:[0,0,1]
	v_mul_f32_e32 v23, v80, v38
	v_mul_f32_e32 v38, v80, v72
	ds_bpermute_b32 v45, v125, v19
	global_store_dword v[24:25], v22, off offset:768
	v_mov_b64_e32 v[50:51], v[228:229]
	v_mov_b64_e32 v[52:53], v[230:231]
	v_mov_b32_e32 v22, 0
	ds_bpermute_b32 v44, v126, v19
	v_mov_b32_e32 v72, v62
	s_waitcnt lgkmcnt(0)
	v_pk_mul_f32 v[56:57], v[64:65], v[44:45] op_sel:[0,1] op_sel_hi:[1,0]

	v_mul_f32_e32 v23, v50, v23
	v_mul_f32_e32 v38, v51, v38
	v_cvt_pk_fp8_f32 v22, v23, v38
	v_mul_f32_e32 v23, v80, v73
	v_mul_f32_e32 v38, v52, v39
	v_mul_f32_e32 v23, v53, v23
	v_cvt_pk_fp8_f32 v22, v38, v23 op_sel:[0,0,1]
	v_mul_f32_e32 v23, v80, v34
	v_mul_f32_e32 v34, v80, v78
	v_cvt_pk_f32_fp8_sdwa v[38:39], v185 src0_sel:WORD_1
	global_store_dword v[24:25], v22, off offset:1024
	v_mov_b64_e32 v[50:51], v[232:233]
	v_mov_b64_e32 v[52:53], v[234:235]
	v_mov_b32_e32 v22, 0
	v_mov_b32_e32 v71, v38
	v_mov_b32_e32 v73, v58
	v_mov_b32_e32 v58, v63
	v_mov_b32_e32 v78, 0

	v_mul_f32_e32 v23, v50, v23
	v_mul_f32_e32 v34, v51, v34
	v_cvt_pk_fp8_f32 v22, v23, v34
	v_mul_f32_e32 v23, v80, v79
	v_mul_f32_e32 v34, v52, v35
	v_mul_f32_e32 v23, v53, v23
	v_cvt_pk_fp8_f32 v22, v34, v23 op_sel:[0,0,1]
	v_mul_f32_e32 v23, v80, v28
	v_mul_f32_e32 v28, v80, v82
	v_cvt_pk_f32_fp8_e32 v[34:35], v185
	global_store_dword v[24:25], v22, off offset:1280
	v_mov_b64_e32 v[50:51], v[236:237]
	v_mov_b64_e32 v[52:53], v[238:239]
	v_mov_b32_e32 v22, 0
	v_mov_b32_e32 v68, v34

	v_mul_f32_e32 v23, v50, v23
	v_mul_f32_e32 v28, v51, v28
	v_cvt_pk_fp8_f32 v22, v23, v28
	v_mul_f32_e32 v23, v80, v83
	v_mul_f32_e32 v28, v52, v29
	v_mul_f32_e32 v23, v53, v23
	v_cvt_pk_fp8_f32 v22, v28, v23 op_sel:[0,0,1]
	ds_bpermute_b32 v51, v96, v19
	ds_bpermute_b32 v50, v124, v19
	v_cvt_pk_f32_fp8_sdwa v[28:29], v181 src0_sel:WORD_1
	global_store_dword v[24:25], v22, off offset:1536
	v_mov_b64_e32 v[52:53], v[240:241]
	v_mov_b64_e32 v[54:55], v[242:243]
	v_cvt_pk_f32_fp8_e32 v[22:23], v181
	v_mov_b32_e32 v69, v28
	v_mov_b32_e32 v28, v35
	v_pk_mul_f32 v[34:35], v[74:75], v[44:45] op_sel:[0,1] op_sel_hi:[1,0]
	v_mov_b32_e32 v70, v22
	v_mov_b32_e32 v38, v23
	s_waitcnt lgkmcnt(0)
	v_pk_mul_f32 v[22:23], v[70:71], v[50:51] op_sel:[0,1] op_sel_hi:[1,0]
	v_pk_mul_f32 v[38:39], v[38:39], v[50:51] op_sel:[0,1] op_sel_hi:[1,0]
	v_pk_fma_f32 v[22:23], v[68:69], v[50:51], v[22:23]
	v_pk_fma_f32 v[34:35], v[72:73], v[44:45], v[34:35]
	v_pk_fma_f32 v[28:29], v[28:29], v[50:51], v[38:39]
	v_pk_fma_f32 v[38:39], v[58:59], v[44:45], v[56:57]
	v_pk_add_f32 v[22:23], v[22:23], v[34:35]
	v_pk_add_f32 v[34:35], v[28:29], v[38:39]
	v_pk_add_f32 v[28:29], v[22:23], v[66:67]
	v_pk_add_f32 v[22:23], v[34:35], v[48:49]
	v_mul_f32_e32 v49, v80, v76
	v_mul_f32_e32 v56, v80, v60
	v_mul_f32_e32 v57, v80, v77
	v_and_b32_sdwa v39, v23, v129 dst_sel:DWORD dst_unused:UNUSED_PAD src0_sel:WORD_1 src1_sel:DWORD
	v_and_b32_sdwa v48, v22, v129 dst_sel:DWORD dst_unused:UNUSED_PAD src0_sel:WORD_1 src1_sel:DWORD
	v_and_b32_sdwa v19, v29, v129 dst_sel:DWORD dst_unused:UNUSED_PAD src0_sel:WORD_1 src1_sel:DWORD
	v_and_b32_sdwa v38, v28, v129 dst_sel:DWORD dst_unused:UNUSED_PAD src0_sel:WORD_1 src1_sel:DWORD
	v_add3_u32 v39, v23, v39, s4
	v_add3_u32 v48, v22, v48, s4
	v_pk_mul_f32 v[34:35], v[22:23], v[22:23]
	v_add3_u32 v38, v28, v38, s4
	v_add3_u32 v19, v29, v19, s4
	v_and_b32_e32 v39, 0xffff0000, v39
	v_and_b32_e32 v48, 0xffff0000, v48
	v_or_b32_sdwa v39, v39, v19 dst_sel:DWORD dst_unused:UNUSED_PAD src0_sel:DWORD src1_sel:WORD_1
	v_or_b32_sdwa v38, v48, v38 dst_sel:DWORD dst_unused:UNUSED_PAD src0_sel:DWORD src1_sel:WORD_1

	v_mul_f32_e32 v49, v52, v49
	v_mul_f32_e32 v52, v53, v56
	v_cvt_pk_fp8_f32 v78, v49, v52
	v_mul_f32_e32 v49, v80, v61
	v_mul_f32_e32 v52, v54, v57
	v_mul_f32_e32 v49, v55, v49
	v_cvt_pk_fp8_f32 v78, v52, v49 op_sel:[0,0,1]
	global_store_dword v[24:25], v78, off offset:1792
	global_store_dwordx2 v[20:21], v[38:39], off
	v_pk_fma_f32 v[48:49], v[28:29], v[28:29], v[34:35]
	v_cvt_pk_f32_fp8_e32 v[38:39], v173
	v_cvt_pk_f32_fp8_sdwa v[56:57], v177 src0_sel:WORD_1
	v_cvt_pk_f32_fp8_sdwa v[52:53], v173 src0_sel:WORD_1
	v_cvt_pk_f32_fp8_e32 v[54:55], v177
	v_cvt_pk_f32_fp8_e32 v[58:59], v179
	s_waitcnt vmcnt(23)
	v_cvt_pk_f32_fp8_sdwa v[64:65], v180 src0_sel:WORD_1
	v_cvt_pk_f32_fp8_sdwa v[60:61], v179 src0_sel:WORD_1
	v_cvt_pk_f32_fp8_e32 v[62:63], v180
	v_mov_b32_e32 v68, v38
	v_mov_b32_e32 v69, v56
	v_mov_b32_e32 v56, v39
	v_mov_b32_e32 v66, v54
	v_mov_b32_e32 v67, v52
	v_pk_mul_f32 v[68:69], v[68:69], v[50:51] op_sel:[0,1] op_sel_hi:[1,0]
	v_mov_b32_e32 v71, v64
	v_mov_b32_e32 v52, v55
	v_pk_mul_f32 v[38:39], v[56:57], v[50:51] op_sel:[0,1] op_sel_hi:[1,0]
	v_mov_b32_e32 v64, v59
	v_pk_fma_f32 v[66:67], v[66:67], v[50:51], v[68:69]
	v_mov_b32_e32 v69, v60
	v_mov_b32_e32 v70, v58
	v_pk_fma_f32 v[38:39], v[52:53], v[50:51], v[38:39]
	v_mov_b32_e32 v60, v63
	v_pk_mul_f32 v[52:53], v[64:65], v[44:45] op_sel:[0,1] op_sel_hi:[1,0]
	v_mov_b32_e32 v68, v62
	v_pk_mul_f32 v[70:71], v[70:71], v[44:45] op_sel:[0,1] op_sel_hi:[1,0]
	v_pk_fma_f32 v[52:53], v[60:61], v[44:45], v[52:53]
	v_lshlrev_b32_e32 v35, 16, v47
	v_lshlrev_b32_e32 v34, 16, v46
	v_and_b32_e32 v47, 0xffff0000, v47
	v_and_b32_e32 v46, 0xffff0000, v46
	v_pk_fma_f32 v[68:69], v[68:69], v[44:45], v[70:71]
	v_pk_add_f32 v[38:39], v[38:39], v[52:53]
	v_pk_add_f32 v[66:67], v[66:67], v[68:69]
	v_pk_add_f32 v[38:39], v[38:39], v[46:47]
	v_pk_add_f32 v[34:35], v[66:67], v[34:35]
	v_and_b32_sdwa v47, v39, v129 dst_sel:DWORD dst_unused:UNUSED_PAD src0_sel:WORD_1 src1_sel:DWORD
	v_and_b32_sdwa v52, v38, v129 dst_sel:DWORD dst_unused:UNUSED_PAD src0_sel:WORD_1 src1_sel:DWORD
	v_and_b32_sdwa v19, v35, v129 dst_sel:DWORD dst_unused:UNUSED_PAD src0_sel:WORD_1 src1_sel:DWORD
	v_and_b32_sdwa v46, v34, v129 dst_sel:DWORD dst_unused:UNUSED_PAD src0_sel:WORD_1 src1_sel:DWORD
	v_add3_u32 v47, v39, v47, s4
	v_add3_u32 v52, v38, v52, s4
	v_add3_u32 v46, v34, v46, s4
	v_add3_u32 v19, v35, v19, s4
	v_and_b32_e32 v47, 0xffff0000, v47
	v_and_b32_e32 v52, 0xffff0000, v52
	v_or_b32_sdwa v47, v47, v19 dst_sel:DWORD dst_unused:UNUSED_PAD src0_sel:DWORD src1_sel:WORD_1
	v_or_b32_sdwa v46, v52, v46 dst_sel:DWORD dst_unused:UNUSED_PAD src0_sel:DWORD src1_sel:WORD_1
	global_store_dwordx2 v[20:21], v[46:47], off offset:512
	v_pk_mul_f32 v[46:47], v[38:39], v[38:39]
	s_nop 0
	v_pk_fma_f32 v[56:57], v[34:35], v[34:35], v[46:47]
	v_cvt_pk_f32_fp8_e32 v[46:47], v165
	v_cvt_pk_f32_fp8_sdwa v[58:59], v169 src0_sel:WORD_1
	v_cvt_pk_f32_fp8_sdwa v[52:53], v165 src0_sel:WORD_1
	v_cvt_pk_f32_fp8_e32 v[54:55], v169
	v_cvt_pk_f32_fp8_e32 v[60:61], v171
	s_waitcnt vmcnt(23)
	v_cvt_pk_f32_fp8_sdwa v[66:67], v172 src0_sel:WORD_1
	v_cvt_pk_f32_fp8_sdwa v[62:63], v171 src0_sel:WORD_1
	v_cvt_pk_f32_fp8_e32 v[64:65], v172
	v_mov_b32_e32 v72, v46
	v_mov_b32_e32 v73, v58
	v_mov_b32_e32 v58, v47
	v_lshlrev_b32_e32 v69, 16, v43
	v_lshlrev_b32_e32 v68, 16, v42
	v_and_b32_e32 v71, 0xffff0000, v43
	v_and_b32_e32 v70, 0xffff0000, v42
	v_mov_b32_e32 v42, v54
	v_mov_b32_e32 v43, v52
	v_pk_mul_f32 v[72:73], v[72:73], v[50:51] op_sel:[0,1] op_sel_hi:[1,0]
	v_mov_b32_e32 v75, v66
	v_mov_b32_e32 v52, v55
	v_pk_mul_f32 v[46:47], v[58:59], v[50:51] op_sel:[0,1] op_sel_hi:[1,0]
	v_mov_b32_e32 v66, v61
	v_pk_fma_f32 v[42:43], v[42:43], v[50:51], v[72:73]
	v_mov_b32_e32 v73, v62
	v_mov_b32_e32 v74, v60
	v_pk_fma_f32 v[46:47], v[52:53], v[50:51], v[46:47]
	v_mov_b32_e32 v62, v65
	v_pk_mul_f32 v[52:53], v[66:67], v[44:45] op_sel:[0,1] op_sel_hi:[1,0]
	v_mov_b32_e32 v72, v64
	v_pk_mul_f32 v[74:75], v[74:75], v[44:45] op_sel:[0,1] op_sel_hi:[1,0]
	v_pk_fma_f32 v[52:53], v[62:63], v[44:45], v[52:53]
	v_pk_fma_f32 v[72:73], v[72:73], v[44:45], v[74:75]
	v_pk_add_f32 v[46:47], v[46:47], v[52:53]
	v_pk_add_f32 v[42:43], v[42:43], v[72:73]
	v_pk_add_f32 v[46:47], v[46:47], v[70:71]
	v_pk_add_f32 v[42:43], v[42:43], v[68:69]
	v_and_b32_sdwa v53, v47, v129 dst_sel:DWORD dst_unused:UNUSED_PAD src0_sel:WORD_1 src1_sel:DWORD
	v_and_b32_sdwa v54, v46, v129 dst_sel:DWORD dst_unused:UNUSED_PAD src0_sel:WORD_1 src1_sel:DWORD
	v_and_b32_sdwa v19, v43, v129 dst_sel:DWORD dst_unused:UNUSED_PAD src0_sel:WORD_1 src1_sel:DWORD
	v_and_b32_sdwa v52, v42, v129 dst_sel:DWORD dst_unused:UNUSED_PAD src0_sel:WORD_1 src1_sel:DWORD
	v_add3_u32 v53, v47, v53, s4
	v_add3_u32 v54, v46, v54, s4
	v_add3_u32 v52, v42, v52, s4
	v_add3_u32 v19, v43, v19, s4
	v_and_b32_e32 v53, 0xffff0000, v53
	v_and_b32_e32 v54, 0xffff0000, v54
	v_or_b32_sdwa v53, v53, v19 dst_sel:DWORD dst_unused:UNUSED_PAD src0_sel:DWORD src1_sel:WORD_1
	v_or_b32_sdwa v52, v54, v52 dst_sel:DWORD dst_unused:UNUSED_PAD src0_sel:DWORD src1_sel:WORD_1
	global_store_dwordx2 v[20:21], v[52:53], off offset:1024
	v_pk_mul_f32 v[52:53], v[46:47], v[46:47]
	s_nop 0
	v_pk_fma_f32 v[60:61], v[42:43], v[42:43], v[52:53]
	v_cvt_pk_f32_fp8_e32 v[52:53], v157
	v_cvt_pk_f32_fp8_sdwa v[62:63], v162 src0_sel:WORD_1
	v_cvt_pk_f32_fp8_sdwa v[54:55], v157 src0_sel:WORD_1
	v_cvt_pk_f32_fp8_e32 v[58:59], v162
	v_cvt_pk_f32_fp8_e32 v[64:65], v163
	s_waitcnt vmcnt(23)
	v_cvt_pk_f32_fp8_sdwa v[70:71], v164 src0_sel:WORD_1
	v_cvt_pk_f32_fp8_sdwa v[66:67], v163 src0_sel:WORD_1
	v_cvt_pk_f32_fp8_e32 v[68:69], v164
	v_mov_b32_e32 v76, v52
	v_mov_b32_e32 v77, v62
	v_mov_b32_e32 v62, v53
	v_lshlrev_b32_e32 v73, 16, v41
	v_lshlrev_b32_e32 v72, 16, v40
	v_and_b32_e32 v75, 0xffff0000, v41
	v_and_b32_e32 v74, 0xffff0000, v40
	v_mov_b32_e32 v40, v58
	v_mov_b32_e32 v41, v54
	v_pk_mul_f32 v[76:77], v[76:77], v[50:51] op_sel:[0,1] op_sel_hi:[1,0]
	v_mov_b32_e32 v79, v70
	v_mov_b32_e32 v54, v59
	v_pk_mul_f32 v[52:53], v[62:63], v[50:51] op_sel:[0,1] op_sel_hi:[1,0]
	v_mov_b32_e32 v70, v65
	v_pk_fma_f32 v[40:41], v[40:41], v[50:51], v[76:77]
	v_mov_b32_e32 v77, v66
	v_mov_b32_e32 v78, v64
	v_pk_fma_f32 v[52:53], v[54:55], v[50:51], v[52:53]
	v_mov_b32_e32 v66, v69
	v_pk_mul_f32 v[54:55], v[70:71], v[44:45] op_sel:[0,1] op_sel_hi:[1,0]
	v_mov_b32_e32 v76, v68
	v_pk_mul_f32 v[78:79], v[78:79], v[44:45] op_sel:[0,1] op_sel_hi:[1,0]
	v_pk_fma_f32 v[54:55], v[66:67], v[44:45], v[54:55]
	v_pk_fma_f32 v[76:77], v[76:77], v[44:45], v[78:79]
	v_pk_add_f32 v[52:53], v[52:53], v[54:55]
	v_pk_add_f32 v[40:41], v[40:41], v[76:77]
	v_pk_add_f32 v[52:53], v[52:53], v[74:75]
	v_pk_add_f32 v[40:41], v[40:41], v[72:73]
	v_and_b32_sdwa v55, v53, v129 dst_sel:DWORD dst_unused:UNUSED_PAD src0_sel:WORD_1 src1_sel:DWORD
	v_and_b32_sdwa v58, v52, v129 dst_sel:DWORD dst_unused:UNUSED_PAD src0_sel:WORD_1 src1_sel:DWORD
	v_and_b32_sdwa v19, v41, v129 dst_sel:DWORD dst_unused:UNUSED_PAD src0_sel:WORD_1 src1_sel:DWORD
	v_and_b32_sdwa v54, v40, v129 dst_sel:DWORD dst_unused:UNUSED_PAD src0_sel:WORD_1 src1_sel:DWORD
	v_add3_u32 v55, v53, v55, s4
	v_add3_u32 v58, v52, v58, s4
	v_add3_u32 v54, v40, v54, s4
	v_add3_u32 v19, v41, v19, s4
	v_and_b32_e32 v55, 0xffff0000, v55
	v_and_b32_e32 v58, 0xffff0000, v58
	v_or_b32_sdwa v55, v55, v19 dst_sel:DWORD dst_unused:UNUSED_PAD src0_sel:DWORD src1_sel:WORD_1
	v_or_b32_sdwa v54, v58, v54 dst_sel:DWORD dst_unused:UNUSED_PAD src0_sel:DWORD src1_sel:WORD_1
	global_store_dwordx2 v[20:21], v[54:55], off offset:1536
	v_pk_mul_f32 v[54:55], v[52:53], v[52:53]
	s_nop 0
	v_pk_fma_f32 v[64:65], v[40:41], v[40:41], v[54:55]
	v_cvt_pk_f32_fp8_e32 v[54:55], v152
	v_cvt_pk_f32_fp8_sdwa v[66:67], v154 src0_sel:WORD_1
	v_cvt_pk_f32_fp8_sdwa v[58:59], v152 src0_sel:WORD_1
	v_cvt_pk_f32_fp8_e32 v[62:63], v154
	v_cvt_pk_f32_fp8_e32 v[68:69], v155
	s_waitcnt vmcnt(23)
	v_cvt_pk_f32_fp8_sdwa v[74:75], v156 src0_sel:WORD_1
	v_cvt_pk_f32_fp8_sdwa v[70:71], v155 src0_sel:WORD_1
	v_cvt_pk_f32_fp8_e32 v[72:73], v156
	v_mov_b32_e32 v80, v54
	v_mov_b32_e32 v81, v66
	v_mov_b32_e32 v66, v55
	v_lshlrev_b32_e32 v77, 16, v37
	v_lshlrev_b32_e32 v76, 16, v36
	v_and_b32_e32 v79, 0xffff0000, v37
	v_and_b32_e32 v78, 0xffff0000, v36
	v_mov_b32_e32 v36, v62
	v_mov_b32_e32 v37, v58
	v_pk_mul_f32 v[80:81], v[80:81], v[50:51] op_sel:[0,1] op_sel_hi:[1,0]
	v_mov_b32_e32 v83, v74
	v_mov_b32_e32 v58, v63
	v_pk_mul_f32 v[54:55], v[66:67], v[50:51] op_sel:[0,1] op_sel_hi:[1,0]
	v_mov_b32_e32 v74, v69
	v_pk_fma_f32 v[36:37], v[36:37], v[50:51], v[80:81]
	v_mov_b32_e32 v81, v70
	v_mov_b32_e32 v82, v68
	v_pk_fma_f32 v[54:55], v[58:59], v[50:51], v[54:55]
	v_mov_b32_e32 v70, v73
	v_pk_mul_f32 v[58:59], v[74:75], v[44:45] op_sel:[0,1] op_sel_hi:[1,0]
	v_mov_b32_e32 v80, v72
	v_pk_mul_f32 v[82:83], v[82:83], v[44:45] op_sel:[0,1] op_sel_hi:[1,0]
	v_pk_fma_f32 v[58:59], v[70:71], v[44:45], v[58:59]
	v_pk_fma_f32 v[80:81], v[80:81], v[44:45], v[82:83]
	v_pk_add_f32 v[54:55], v[54:55], v[58:59]
	v_pk_add_f32 v[36:37], v[36:37], v[80:81]
	v_pk_add_f32 v[54:55], v[54:55], v[78:79]
	v_pk_add_f32 v[36:37], v[36:37], v[76:77]
	v_and_b32_sdwa v59, v55, v129 dst_sel:DWORD dst_unused:UNUSED_PAD src0_sel:WORD_1 src1_sel:DWORD
	v_and_b32_sdwa v62, v54, v129 dst_sel:DWORD dst_unused:UNUSED_PAD src0_sel:WORD_1 src1_sel:DWORD
	v_and_b32_sdwa v19, v37, v129 dst_sel:DWORD dst_unused:UNUSED_PAD src0_sel:WORD_1 src1_sel:DWORD
	v_and_b32_sdwa v58, v36, v129 dst_sel:DWORD dst_unused:UNUSED_PAD src0_sel:WORD_1 src1_sel:DWORD
	v_add3_u32 v59, v55, v59, s4
	v_add3_u32 v62, v54, v62, s4
	v_add3_u32 v58, v36, v58, s4
	v_add3_u32 v19, v37, v19, s4
	v_and_b32_e32 v59, 0xffff0000, v59
	v_and_b32_e32 v62, 0xffff0000, v62
	v_or_b32_sdwa v59, v59, v19 dst_sel:DWORD dst_unused:UNUSED_PAD src0_sel:DWORD src1_sel:WORD_1
	v_or_b32_sdwa v58, v62, v58 dst_sel:DWORD dst_unused:UNUSED_PAD src0_sel:DWORD src1_sel:WORD_1
	global_store_dwordx2 v[20:21], v[58:59], off offset:2048
	v_pk_mul_f32 v[58:59], v[54:55], v[54:55]
	s_nop 0
	v_pk_fma_f32 v[66:67], v[36:37], v[36:37], v[58:59]
	v_cvt_pk_f32_fp8_e32 v[58:59], v144
	v_cvt_pk_f32_fp8_sdwa v[70:71], v145 src0_sel:WORD_1
	v_cvt_pk_f32_fp8_sdwa v[62:63], v144 src0_sel:WORD_1
	v_cvt_pk_f32_fp8_e32 v[68:69], v145
	v_cvt_pk_f32_fp8_e32 v[72:73], v146
	s_waitcnt vmcnt(23)
	v_cvt_pk_f32_fp8_sdwa v[78:79], v147 src0_sel:WORD_1
	v_cvt_pk_f32_fp8_sdwa v[74:75], v146 src0_sel:WORD_1
	v_cvt_pk_f32_fp8_e32 v[76:77], v147
	v_mov_b32_e32 v84, v58
	v_mov_b32_e32 v85, v70
	v_mov_b32_e32 v70, v59
	v_lshlrev_b32_e32 v81, 16, v33
	v_lshlrev_b32_e32 v80, 16, v32
	v_and_b32_e32 v83, 0xffff0000, v33
	v_and_b32_e32 v82, 0xffff0000, v32
	v_mov_b32_e32 v32, v68
	v_mov_b32_e32 v33, v62
	v_pk_mul_f32 v[84:85], v[84:85], v[50:51] op_sel:[0,1] op_sel_hi:[1,0]
	v_mov_b32_e32 v89, v78
	v_mov_b32_e32 v62, v69
	v_pk_mul_f32 v[58:59], v[70:71], v[50:51] op_sel:[0,1] op_sel_hi:[1,0]
	v_mov_b32_e32 v78, v73
	v_pk_fma_f32 v[32:33], v[32:33], v[50:51], v[84:85]
	v_mov_b32_e32 v85, v74
	v_mov_b32_e32 v88, v72
	v_pk_fma_f32 v[58:59], v[62:63], v[50:51], v[58:59]
	v_mov_b32_e32 v74, v77
	v_pk_mul_f32 v[62:63], v[78:79], v[44:45] op_sel:[0,1] op_sel_hi:[1,0]
	v_mov_b32_e32 v84, v76
	v_pk_mul_f32 v[88:89], v[88:89], v[44:45] op_sel:[0,1] op_sel_hi:[1,0]
	v_pk_fma_f32 v[62:63], v[74:75], v[44:45], v[62:63]
	v_pk_fma_f32 v[84:85], v[84:85], v[44:45], v[88:89]
	v_pk_add_f32 v[58:59], v[58:59], v[62:63]
	v_pk_add_f32 v[32:33], v[32:33], v[84:85]
	v_pk_add_f32 v[58:59], v[58:59], v[82:83]
	v_pk_add_f32 v[32:33], v[32:33], v[80:81]
	v_and_b32_sdwa v63, v59, v129 dst_sel:DWORD dst_unused:UNUSED_PAD src0_sel:WORD_1 src1_sel:DWORD
	v_and_b32_sdwa v68, v58, v129 dst_sel:DWORD dst_unused:UNUSED_PAD src0_sel:WORD_1 src1_sel:DWORD
	v_and_b32_sdwa v19, v33, v129 dst_sel:DWORD dst_unused:UNUSED_PAD src0_sel:WORD_1 src1_sel:DWORD
	v_and_b32_sdwa v62, v32, v129 dst_sel:DWORD dst_unused:UNUSED_PAD src0_sel:WORD_1 src1_sel:DWORD
	v_add3_u32 v63, v59, v63, s4
	v_add3_u32 v68, v58, v68, s4
	v_add3_u32 v62, v32, v62, s4
	v_add3_u32 v19, v33, v19, s4
	v_and_b32_e32 v63, 0xffff0000, v63
	v_and_b32_e32 v68, 0xffff0000, v68
	v_or_b32_sdwa v63, v63, v19 dst_sel:DWORD dst_unused:UNUSED_PAD src0_sel:DWORD src1_sel:WORD_1
	v_or_b32_sdwa v62, v68, v62 dst_sel:DWORD dst_unused:UNUSED_PAD src0_sel:DWORD src1_sel:WORD_1
	global_store_dwordx2 v[20:21], v[62:63], off offset:2560
	v_pk_mul_f32 v[62:63], v[58:59], v[58:59]
	s_nop 0
	v_pk_fma_f32 v[68:69], v[32:33], v[32:33], v[62:63]
	v_cvt_pk_f32_fp8_e32 v[62:63], v134
	v_cvt_pk_f32_fp8_sdwa v[74:75], v135 src0_sel:WORD_1
	v_cvt_pk_f32_fp8_sdwa v[70:71], v134 src0_sel:WORD_1
	v_cvt_pk_f32_fp8_e32 v[72:73], v135
	v_cvt_pk_f32_fp8_e32 v[76:77], v136
	s_waitcnt vmcnt(23)
	v_cvt_pk_f32_fp8_sdwa v[82:83], v142 src0_sel:WORD_1
	v_cvt_pk_f32_fp8_sdwa v[78:79], v136 src0_sel:WORD_1
	v_cvt_pk_f32_fp8_e32 v[80:81], v142
	v_mov_b32_e32 v134, v62
	v_mov_b32_e32 v135, v74
	v_mov_b32_e32 v74, v63
	v_lshlrev_b32_e32 v85, 16, v31
	v_lshlrev_b32_e32 v84, 16, v30
	v_and_b32_e32 v89, 0xffff0000, v31
	v_and_b32_e32 v88, 0xffff0000, v30
	v_mov_b32_e32 v30, v72
	v_mov_b32_e32 v31, v70
	v_pk_mul_f32 v[134:135], v[134:135], v[50:51] op_sel:[0,1] op_sel_hi:[1,0]
	v_mov_b32_e32 v137, v82
	v_mov_b32_e32 v70, v73
	v_pk_mul_f32 v[62:63], v[74:75], v[50:51] op_sel:[0,1] op_sel_hi:[1,0]
	v_mov_b32_e32 v82, v77
	v_pk_fma_f32 v[30:31], v[30:31], v[50:51], v[134:135]
	v_mov_b32_e32 v135, v78
	v_mov_b32_e32 v136, v76
	v_pk_fma_f32 v[62:63], v[70:71], v[50:51], v[62:63]
	v_mov_b32_e32 v78, v81
	v_pk_mul_f32 v[70:71], v[82:83], v[44:45] op_sel:[0,1] op_sel_hi:[1,0]
	v_mov_b32_e32 v134, v80
	v_pk_mul_f32 v[136:137], v[136:137], v[44:45] op_sel:[0,1] op_sel_hi:[1,0]
	v_pk_fma_f32 v[70:71], v[78:79], v[44:45], v[70:71]
	v_pk_fma_f32 v[134:135], v[134:135], v[44:45], v[136:137]
	v_pk_add_f32 v[62:63], v[62:63], v[70:71]
	v_pk_add_f32 v[30:31], v[30:31], v[134:135]
	v_pk_add_f32 v[62:63], v[62:63], v[88:89]
	v_pk_add_f32 v[30:31], v[30:31], v[84:85]
	v_and_b32_sdwa v71, v63, v129 dst_sel:DWORD dst_unused:UNUSED_PAD src0_sel:WORD_1 src1_sel:DWORD
	v_and_b32_sdwa v72, v62, v129 dst_sel:DWORD dst_unused:UNUSED_PAD src0_sel:WORD_1 src1_sel:DWORD
	v_and_b32_sdwa v19, v31, v129 dst_sel:DWORD dst_unused:UNUSED_PAD src0_sel:WORD_1 src1_sel:DWORD
	v_and_b32_sdwa v70, v30, v129 dst_sel:DWORD dst_unused:UNUSED_PAD src0_sel:WORD_1 src1_sel:DWORD
	v_add3_u32 v71, v63, v71, s4
	v_add3_u32 v72, v62, v72, s4
	v_add3_u32 v70, v30, v70, s4
	v_add3_u32 v19, v31, v19, s4
	v_and_b32_e32 v71, 0xffff0000, v71
	v_and_b32_e32 v72, 0xffff0000, v72
	v_or_b32_sdwa v71, v71, v19 dst_sel:DWORD dst_unused:UNUSED_PAD src0_sel:DWORD src1_sel:WORD_1
	v_or_b32_sdwa v70, v72, v70 dst_sel:DWORD dst_unused:UNUSED_PAD src0_sel:DWORD src1_sel:WORD_1
	global_store_dwordx2 v[20:21], v[70:71], off offset:3072
	v_pk_mul_f32 v[70:71], v[62:63], v[62:63]
	s_nop 0
	v_pk_fma_f32 v[70:71], v[30:31], v[30:31], v[70:71]
	v_cvt_pk_f32_fp8_e32 v[72:73], v86
	v_cvt_pk_f32_fp8_sdwa v[78:79], v87 src0_sel:WORD_1
	v_cvt_pk_f32_fp8_sdwa v[74:75], v86 src0_sel:WORD_1
	v_cvt_pk_f32_fp8_e32 v[76:77], v87
	v_cvt_pk_f32_fp8_e32 v[80:81], v130
	s_waitcnt vmcnt(23)
	v_cvt_pk_f32_fp8_sdwa v[86:87], v132 src0_sel:WORD_1
	v_cvt_pk_f32_fp8_sdwa v[82:83], v130 src0_sel:WORD_1
	v_cvt_pk_f32_fp8_e32 v[84:85], v132
	v_mov_b32_e32 v132, v72
	v_mov_b32_e32 v133, v78
	v_mov_b32_e32 v78, v73
	v_lshlrev_b32_e32 v89, 16, v27
	v_lshlrev_b32_e32 v88, 16, v26
	v_and_b32_e32 v131, 0xffff0000, v27
	v_and_b32_e32 v130, 0xffff0000, v26
	v_mov_b32_e32 v26, v76
	v_mov_b32_e32 v27, v74
	v_pk_mul_f32 v[132:133], v[132:133], v[50:51] op_sel:[0,1] op_sel_hi:[1,0]
	v_mov_b32_e32 v134, v80
	v_mov_b32_e32 v135, v86
	v_mov_b32_e32 v74, v77
	v_pk_mul_f32 v[72:73], v[78:79], v[50:51] op_sel:[0,1] op_sel_hi:[1,0]
	v_mov_b32_e32 v86, v81
	v_pk_fma_f32 v[26:27], v[26:27], v[50:51], v[132:133]
	v_mov_b32_e32 v132, v84
	v_mov_b32_e32 v133, v82
	v_pk_mul_f32 v[134:135], v[134:135], v[44:45] op_sel:[0,1] op_sel_hi:[1,0]
	v_pk_fma_f32 v[50:51], v[74:75], v[50:51], v[72:73]
	v_mov_b32_e32 v82, v85
	v_pk_mul_f32 v[72:73], v[86:87], v[44:45] op_sel:[0,1] op_sel_hi:[1,0]
	v_pk_fma_f32 v[132:133], v[132:133], v[44:45], v[134:135]
	v_pk_fma_f32 v[44:45], v[82:83], v[44:45], v[72:73]
	v_pk_add_f32 v[26:27], v[26:27], v[132:133]
	v_pk_add_f32 v[44:45], v[50:51], v[44:45]
	v_pk_add_f32 v[26:27], v[26:27], v[88:89]
	v_pk_add_f32 v[44:45], v[44:45], v[130:131]
	v_and_b32_sdwa v19, v27, v129 dst_sel:DWORD dst_unused:UNUSED_PAD src0_sel:WORD_1 src1_sel:DWORD
	v_and_b32_sdwa v51, v45, v129 dst_sel:DWORD dst_unused:UNUSED_PAD src0_sel:WORD_1 src1_sel:DWORD
	v_add3_u32 v51, v45, v51, s4
	v_add3_u32 v19, v27, v19, s4
	v_and_b32_e32 v51, 0xffff0000, v51
	v_and_b32_sdwa v72, v44, v129 dst_sel:DWORD dst_unused:UNUSED_PAD src0_sel:WORD_1 src1_sel:DWORD
	v_or_b32_sdwa v51, v51, v19 dst_sel:DWORD dst_unused:UNUSED_PAD src0_sel:DWORD src1_sel:WORD_1
	v_add_f32_e32 v19, v56, v57
	v_add_f32_e32 v48, v48, v49
	v_and_b32_sdwa v50, v26, v129 dst_sel:DWORD dst_unused:UNUSED_PAD src0_sel:WORD_1 src1_sel:DWORD
	v_add3_u32 v72, v44, v72, s4
	v_add_f32_e32 v19, v48, v19
	v_add_f32_e32 v48, v60, v61
	v_add3_u32 v50, v26, v50, s4
	v_and_b32_e32 v72, 0xffff0000, v72
	v_add_f32_e32 v19, v19, v48
	v_add_f32_e32 v48, v64, v65
	v_or_b32_sdwa v50, v72, v50 dst_sel:DWORD dst_unused:UNUSED_PAD src0_sel:DWORD src1_sel:WORD_1
	v_add_f32_e32 v19, v19, v48
	v_add_f32_e32 v48, v66, v67
	global_store_dwordx2 v[20:21], v[50:51], off offset:3584
	v_pk_mul_f32 v[20:21], v[44:45], v[44:45]
	v_add_f32_e32 v19, v19, v48
	v_add_f32_e32 v48, v68, v69
	v_pk_fma_f32 v[20:21], v[26:27], v[26:27], v[20:21]
	v_add_f32_e32 v19, v19, v48
	v_add_f32_e32 v48, v70, v71
	v_add_f32_e32 v19, v19, v48
	v_add_f32_e32 v20, v20, v21
	v_add_f32_e32 v19, v19, v20
	v_mov_b64_e32 v[48:49], v[212:213]
	v_mov_b64_e32 v[50:51], v[214:215]
	ds_bpermute_b32 v20, v1, v19
	s_add_i32 s18, s18, s20
	v_lshl_add_u64 v[14:15], v[14:15], 0, s[22:23]
	v_lshl_add_u64 v[16:17], v[16:17], 0, s[24:25]
	s_cmpk_lt_i32 s18, 0x4000
	s_waitcnt lgkmcnt(0)
	v_add_f32_e32 v19, v19, v20
	ds_bpermute_b32 v20, v90, v19
	v_add_u32_e32 v18, s2, v18
	s_waitcnt lgkmcnt(0)
	v_add_f32_e32 v19, v19, v20
	ds_bpermute_b32 v20, v91, v19
	s_waitcnt lgkmcnt(0)
	v_add_f32_e32 v19, v19, v20
	ds_bpermute_b32 v20, v92, v19
	s_waitcnt lgkmcnt(0)
	v_add_f32_e32 v19, v19, v20
	ds_bpermute_b32 v20, v93, v19
	s_waitcnt lgkmcnt(0)
	v_add_f32_e32 v19, v19, v20
	ds_bpermute_b32 v20, v94, v19
	s_waitcnt lgkmcnt(0)
	v_add_f32_e32 v19, v19, v20
	v_fmamk_f32 v19, v19, 0x3a000000, v127
	v_mul_f32_e32 v20, 0x4f800000, v19
	v_cmp_gt_f32_e32 vcc, s19, v19
	s_nop 1
	v_cndmask_b32_e32 v19, v19, v20, vcc
	v_sqrt_f32_e32 v20, v19
	s_nop 0
	v_add_u32_e32 v21, -1, v20
	v_add_u32_e32 v56, 1, v20
	v_fma_f32 v57, -v21, v20, v19
	v_fma_f32 v60, -v56, v20, v19
	v_cmp_ge_f32_e64 s[8:9], 0, v57
	s_nop 1
	v_cndmask_b32_e64 v20, v20, v21, s[8:9]
	v_cmp_lt_f32_e64 s[8:9], 0, v60
	s_nop 1
	v_cndmask_b32_e64 v20, v20, v56, s[8:9]
	v_mul_f32_e32 v21, 0x37800000, v20
	v_cndmask_b32_e32 v20, v20, v21, vcc
	v_cmp_class_f32_e32 vcc, v19, v128
	v_mov_b32_e32 v56, 0
	s_nop 0
	v_cndmask_b32_e32 v19, v20, v19, vcc
	v_div_scale_f32 v20, s[0:1], v19, v19, 1.0
	v_rcp_f32_e32 v21, v20
	v_div_scale_f32 v57, vcc, 1.0, v19, 1.0
	v_fma_f32 v60, -v20, v21, 1.0
	v_fmac_f32_e32 v21, v60, v21
	v_mul_f32_e32 v60, v57, v21
	v_fma_f32 v61, -v20, v60, v57
	v_fmac_f32_e32 v60, v61, v21
	v_fma_f32 v20, -v20, v60, v57
	v_div_fmas_f32 v20, v20, v21, v60
	v_div_fixup_f32 v19, v20, v19, 1.0
	v_mul_f32_e32 v20, v19, v28
	v_mul_f32_e32 v21, v19, v22

	v_mul_f32_e32 v20, v48, v20
	v_mul_f32_e32 v21, v49, v21
	v_cvt_pk_fp8_f32 v56, v20, v21
	v_mul_f32_e32 v22, v19, v29
	v_mul_f32_e32 v20, v19, v23
	v_mul_f32_e32 v21, v50, v22
	v_mul_f32_e32 v20, v51, v20
	v_cvt_pk_fp8_f32 v56, v21, v20 op_sel:[0,0,1]
	v_mul_f32_e32 v29, v19, v34
	v_mul_f32_e32 v34, v19, v38
	v_mov_b32_e32 v28, 0
	global_store_dword v[24:25], v56, off offset:2048
	v_mov_b64_e32 v[20:21], v[216:217]
	v_mov_b64_e32 v[22:23], v[218:219]
	v_mul_f32_e32 v35, v19, v35
	v_mul_f32_e32 v33, v19, v33
	v_mul_f32_e32 v31, v19, v31
	v_mul_f32_e32 v26, v19, v26
	v_mul_f32_e32 v27, v19, v27

	v_mul_f32_e32 v20, v20, v29
	v_mul_f32_e32 v21, v21, v34
	v_cvt_pk_fp8_f32 v28, v20, v21
	v_mul_f32_e32 v20, v19, v39
	v_mul_f32_e32 v21, v22, v35
	v_mul_f32_e32 v20, v23, v20
	v_cvt_pk_fp8_f32 v28, v21, v20 op_sel:[0,0,1]
	v_mul_f32_e32 v29, v19, v42
	v_mul_f32_e32 v34, v19, v46
	v_mul_f32_e32 v35, v19, v43
	global_store_dword v[24:25], v28, off offset:2304
	v_mov_b64_e32 v[20:21], v[220:221]
	v_mov_b64_e32 v[22:23], v[222:223]
	v_mov_b32_e32 v28, 0

	v_mul_f32_e32 v20, v20, v29
	v_mul_f32_e32 v21, v21, v34
	v_cvt_pk_fp8_f32 v28, v20, v21
	v_mul_f32_e32 v20, v19, v47
	v_mul_f32_e32 v21, v22, v35
	v_mul_f32_e32 v20, v23, v20
	v_cvt_pk_fp8_f32 v28, v21, v20 op_sel:[0,0,1]
	v_mul_f32_e32 v29, v19, v40
	v_mul_f32_e32 v34, v19, v52
	v_mul_f32_e32 v35, v19, v41
	global_store_dword v[24:25], v28, off offset:2560
	v_mov_b64_e32 v[20:21], v[224:225]
	v_mov_b64_e32 v[22:23], v[226:227]
	v_mov_b32_e32 v28, 0

	v_mul_f32_e32 v20, v20, v29
	v_mul_f32_e32 v21, v21, v34
	v_cvt_pk_fp8_f32 v28, v20, v21
	v_mul_f32_e32 v20, v19, v53
	v_mul_f32_e32 v21, v22, v35
	v_mul_f32_e32 v20, v23, v20
	v_cvt_pk_fp8_f32 v28, v21, v20 op_sel:[0,0,1]
	v_mul_f32_e32 v29, v19, v36
	v_mul_f32_e32 v34, v19, v54
	v_mul_f32_e32 v35, v19, v37
	global_store_dword v[24:25], v28, off offset:2816
	v_mov_b64_e32 v[20:21], v[228:229]
	v_mov_b64_e32 v[22:23], v[230:231]
	v_mov_b32_e32 v28, 0

	v_mul_f32_e32 v20, v20, v29
	v_mul_f32_e32 v21, v21, v34
	v_cvt_pk_fp8_f32 v28, v20, v21
	v_mul_f32_e32 v20, v19, v55
	v_mul_f32_e32 v21, v22, v35
	v_mul_f32_e32 v20, v23, v20
	v_cvt_pk_fp8_f32 v28, v21, v20 op_sel:[0,0,1]
	v_mul_f32_e32 v29, v19, v32
	v_mul_f32_e32 v32, v19, v58
	global_store_dword v[24:25], v28, off offset:3072
	v_mov_b64_e32 v[20:21], v[232:233]
	v_mov_b64_e32 v[22:23], v[234:235]
	v_mov_b32_e32 v28, 0

	v_mul_f32_e32 v20, v20, v29
	v_mul_f32_e32 v21, v21, v32
	v_cvt_pk_fp8_f32 v28, v20, v21
	v_mul_f32_e32 v20, v19, v59
	v_mul_f32_e32 v21, v22, v33
	v_mul_f32_e32 v20, v23, v20
	v_cvt_pk_fp8_f32 v28, v21, v20 op_sel:[0,0,1]
	v_mul_f32_e32 v29, v19, v30
	v_mul_f32_e32 v30, v19, v62
	global_store_dword v[24:25], v28, off offset:3328
	v_mov_b64_e32 v[20:21], v[236:237]
	v_mov_b64_e32 v[22:23], v[238:239]
	v_mov_b32_e32 v28, 0

	v_mul_f32_e32 v20, v20, v29
	v_mul_f32_e32 v21, v21, v30
	v_cvt_pk_fp8_f32 v28, v20, v21
	v_mul_f32_e32 v20, v19, v63
	v_mul_f32_e32 v21, v22, v31
	v_mul_f32_e32 v20, v23, v20
	v_cvt_pk_fp8_f32 v28, v21, v20 op_sel:[0,0,1]
	v_mul_f32_e32 v29, v19, v44
	v_mul_f32_e32 v19, v19, v45
	global_store_dword v[24:25], v28, off offset:3584
	v_mov_b64_e32 v[20:21], v[240:241]
	v_mov_b64_e32 v[22:23], v[242:243]
	v_mov_b32_e32 v28, 0

	v_mul_f32_e32 v20, v20, v26
	v_mul_f32_e32 v21, v21, v29
	v_cvt_pk_fp8_f32 v28, v20, v21
	v_mul_f32_e32 v20, v22, v27
	v_mul_f32_e32 v19, v23, v19
	v_cvt_pk_fp8_f32 v28, v20, v19 op_sel:[0,0,1]
	global_store_dword v[24:25], v28, off offset:3840
	s_cbranch_scc0 .LBB0_1431
